# baseline (speedup 1.0000x reference)
.LBB3_7:
	v_add_u32_e32 v182, s33, v161
	v_add_u32_e32 v181, -1, v182
	v_or_b32_e32 v2, v181, v164
	v_add_u32_e32 v180, 0x18400, v171
	v_cmp_gt_u32_e64 s[0:1], 64, v2
	s_mov_b64 s[4:5], -1
	s_and_b64 vcc, exec, s[24:25]
	s_cbranch_vccz .LBB3_45
	s_load_dwordx2 s[4:5], s[22:23], 0x20
	s_waitcnt lgkmcnt(0)
	s_load_dwordx2 s[26:27], s[4:5], 0x0
	s_load_dword s34, s[4:5], 0x8
	v_cmp_lt_u32_e64 s[64:65], 0, v182
	v_cmp_gt_u32_e64 s[66:67], 63, v182
	v_cmp_lt_u32_e64 s[68:69], 0, v162
	v_cmp_gt_u32_e64 s[70:71], 60, v162
	buffer_load_dwordx4 v[186:189], v180, s[16:19], 0 offen nt
	s_and_b64 s[72:73], s[68:69], s[64:65]
	s_and_b64 s[74:75], s[68:69], s[66:67]
	s_and_b64 s[76:77], s[70:71], s[64:65]
	s_and_b64 s[78:79], s[70:71], s[66:67]
	v_add_u32_e32 v249, 0xfffe7c00, v180
	v_add_u32_e32 v250, 0xfffe8000, v180
	s_mov_b64 exec, s[72:73]
	buffer_load_dwordx4 v[110:113], v249, s[16:19], 0 offen
	buffer_load_dwordx4 v[70:73], v249, s[16:19], 0 offen offset:512
	s_mov_b64 exec, -1
	s_mov_b64 exec, s[68:69]
	buffer_load_dwordx4 v[126:129], v250, s[16:19], 0 offen offset:512
	buffer_load_dwordx4 v[98:101], v250, s[16:19], 0 offen offset:1024
	s_mov_b64 exec, -1
	s_mov_b64 exec, s[74:75]
	buffer_load_dwordx4 v[134:137], v250, s[16:19], 0 offen offset:2048
	buffer_load_dwordx4 v[114:117], v250, s[16:19], 0 offen offset:2560
	s_mov_b64 exec, -1
	v_add_u32_e32 v249, 0xfffffc00, v180
	s_mov_b64 exec, s[64:65]
	buffer_load_dwordx4 v[82:85], v249, s[16:19], 0 offen
	buffer_load_dwordx4 v[42:45], v249, s[16:19], 0 offen offset:512
	s_mov_b64 exec, -1
	buffer_load_dwordx4 v[106:109], v180, s[16:19], 0 offen offset:512
	buffer_load_dwordx4 v[62:65], v180, s[16:19], 0 offen offset:1024
	s_mov_b64 exec, s[66:67]
	buffer_load_dwordx4 v[122:125], v180, s[16:19], 0 offen offset:2048
	buffer_load_dwordx4 v[86:89], v180, s[16:19], 0 offen offset:2560
	s_mov_b64 exec, -1
	v_add_u32_e32 v249, 0x17c00, v180
	v_add_u32_e32 v250, 0x18000, v180
	s_mov_b64 exec, s[64:65]
	buffer_load_dwordx4 v[50:53], v249, s[16:19], 0 offen
	buffer_load_dwordx4 v[22:25], v249, s[16:19], 0 offen offset:512
	s_mov_b64 exec, -1
	buffer_load_dwordx4 v[66:69], v250, s[16:19], 0 offen offset:512
	buffer_load_dwordx4 v[30:33], v250, s[16:19], 0 offen offset:1024
	s_mov_b64 exec, s[66:67]
	buffer_load_dwordx4 v[94:97], v250, s[16:19], 0 offen offset:2048
	buffer_load_dwordx4 v[46:49], v250, s[16:19], 0 offen offset:2560
	s_mov_b64 exec, -1
	v_add_u32_e32 v249, 0x18000, v180
	buffer_load_dwordx4 v[154:157], v249, s[16:19], 0 offen nt
	v_add_u32_e32 v250, 0x30000, v180
	buffer_load_dwordx4 v[150:153], v250, s[16:19], 0 offen nt
	v_add_u32_e32 v249, 0x48000, v180
	buffer_load_dwordx4 v[146:149], v249, s[16:19], 0 offen nt
	v_add_u32_e32 v249, 0x2fc00, v180
	v_add_u32_e32 v250, 0x30000, v180
	v_add_u32_e32 v251, 0x47c00, v180
	v_add_u32_e32 v252, 0x48000, v180
	v_add_u32_e32 v253, 0x5fc00, v180
	v_add_u32_e32 v254, 0x60000, v180
	s_cmp_lg_u32 s93, 0
	s_cbranch_scc1 .Lmybg_B1
	s_waitcnt vmcnt(22)
	v_cvt_pk_f16_f32 v172, v230, v231
	v_cvt_pk_f16_f32 v173, v234, v235
	v_cvt_pk_f16_f32 v174, v232, v233
	v_cvt_pk_f16_f32 v175, v236, v237
	v_cvt_pk_f16_f32 v176, v238, v239
	v_cvt_pk_f16_f32 v177, v242, v243
	v_cvt_pk_f16_f32 v178, v240, v241
	v_cvt_pk_f16_f32 v179, v244, v245
	s_mov_b32 s93, 1

.LBB3_45:
	s_and_b64 vcc, exec, s[4:5]
	s_cbranch_vccz .LBB3_6
	s_load_dwordx2 s[0:1], s[22:23], 0x18
	s_waitcnt lgkmcnt(0)
	s_load_dwordx2 s[6:7], s[0:1], 0x0
	s_load_dword s28, s[0:1], 0x8
	v_cmp_lt_u32_e64 s[64:65], 0, v182
	v_cmp_gt_u32_e64 s[66:67], 63, v182
	v_cmp_lt_u32_e64 s[68:69], 0, v162
	v_cmp_gt_u32_e64 s[70:71], 60, v162
	buffer_load_dwordx4 v[184:187], v180, s[16:19], 0 offen nt
	s_and_b64 s[72:73], s[68:69], s[64:65]
	s_and_b64 s[74:75], s[68:69], s[66:67]
	s_and_b64 s[76:77], s[70:71], s[64:65]
	s_and_b64 s[78:79], s[70:71], s[66:67]
	v_add_u32_e32 v249, 0xfffe7c00, v180
	v_add_u32_e32 v250, 0xfffe8000, v180
	s_mov_b64 exec, s[72:73]
	buffer_load_dwordx4 v[110:113], v249, s[16:19], 0 offen
	buffer_load_dwordx4 v[78:81], v249, s[16:19], 0 offen offset:512
	s_mov_b64 exec, -1
	s_mov_b64 exec, s[68:69]
	buffer_load_dwordx4 v[126:129], v250, s[16:19], 0 offen offset:512
	buffer_load_dwordx4 v[102:105], v250, s[16:19], 0 offen offset:1024
	s_mov_b64 exec, -1
	s_mov_b64 exec, s[74:75]
	buffer_load_dwordx4 v[138:141], v250, s[16:19], 0 offen offset:2048
	buffer_load_dwordx4 v[118:121], v250, s[16:19], 0 offen offset:2560
	s_mov_b64 exec, -1
	v_add_u32_e32 v249, 0xfffffc00, v180
	s_mov_b64 exec, s[64:65]
	buffer_load_dwordx4 v[86:89], v249, s[16:19], 0 offen
	buffer_load_dwordx4 v[46:49], v249, s[16:19], 0 offen offset:512
	s_mov_b64 exec, -1
	buffer_load_dwordx4 v[106:109], v180, s[16:19], 0 offen offset:512
	buffer_load_dwordx4 v[62:65], v180, s[16:19], 0 offen offset:1024
	s_mov_b64 exec, s[66:67]
	buffer_load_dwordx4 v[122:125], v180, s[16:19], 0 offen offset:2048
	buffer_load_dwordx4 v[82:85], v180, s[16:19], 0 offen offset:2560
	s_mov_b64 exec, -1
	v_add_u32_e32 v249, 0x17c00, v180
	v_add_u32_e32 v250, 0x18000, v180
	s_mov_b64 exec, s[64:65]
	buffer_load_dwordx4 v[50:53], v249, s[16:19], 0 offen
	buffer_load_dwordx4 v[22:25], v249, s[16:19], 0 offen offset:512
	s_mov_b64 exec, -1
	buffer_load_dwordx4 v[66:69], v250, s[16:19], 0 offen offset:512
	buffer_load_dwordx4 v[34:37], v250, s[16:19], 0 offen offset:1024
	s_mov_b64 exec, s[66:67]
	buffer_load_dwordx4 v[94:97], v250, s[16:19], 0 offen offset:2048
	buffer_load_dwordx4 v[42:45], v250, s[16:19], 0 offen offset:2560
	s_mov_b64 exec, -1
	v_add_u32_e32 v249, 0x18000, v180
	buffer_load_dwordx4 v[154:157], v249, s[16:19], 0 offen nt
	v_add_u32_e32 v250, 0x30000, v180
	buffer_load_dwordx4 v[150:153], v250, s[16:19], 0 offen nt
	v_add_u32_e32 v249, 0x48000, v180
	buffer_load_dwordx4 v[146:149], v249, s[16:19], 0 offen nt
	v_add_u32_e32 v249, 0x2fc00, v180
	v_add_u32_e32 v250, 0x30000, v180
	v_add_u32_e32 v251, 0x47c00, v180
	v_add_u32_e32 v252, 0x48000, v180
	v_add_u32_e32 v253, 0x5fc00, v180
	v_add_u32_e32 v254, 0x60000, v180
	s_cmp_lg_u32 s93, 0
	s_cbranch_scc1 .Lmybg_B2
	s_waitcnt vmcnt(22)
	v_cvt_pk_f16_f32 v172, v230, v231
	v_cvt_pk_f16_f32 v173, v234, v235
	v_cvt_pk_f16_f32 v174, v232, v233
	v_cvt_pk_f16_f32 v175, v236, v237
	v_cvt_pk_f16_f32 v176, v238, v239
	v_cvt_pk_f16_f32 v177, v242, v243
	v_cvt_pk_f16_f32 v178, v240, v241
	v_cvt_pk_f16_f32 v179, v244, v245
	s_mov_b32 s93, 1

.LBB4_4:
	global_load_dwordx4 v[2:5], v[170:171], off
	global_load_dwordx4 v[8:11], v[172:173], off
	global_load_dwordx4 v[210:213], v[170:171], off offset:16
	global_load_dwordx4 v[214:217], v[172:173], off offset:16
	s_lshl_b32 s48, s46, 3
	s_add_i32 s48, s48, s44
	v_or_b32_e32 v199, s48, v178
	v_add_u32_e32 v168, v199, v181
	v_add_u32_e32 v201, -1, v199
	v_mul_lo_u32 v6, v168, s47
	v_or_b32_e32 v7, v201, v182
	v_or_b32_e32 v6, v6, v166
	s_mov_b64 s[4:5], -1
	s_and_b64 vcc, exec, s[26:27]
	v_cmp_gt_u32_e64 s[2:3], 64, v7
	v_lshlrev_b32_e32 v200, 1, v6
	s_cbranch_vccz .LBB4_42
	global_load_dwordx3 v[154:156], v169, s[10:11]
	v_cmp_lt_u32_e64 s[64:65], 0, v199
	v_cmp_gt_u32_e64 s[66:67], 63, v199
	v_cmp_lt_u32_e64 s[68:69], 0, v180
	v_cmp_gt_u32_e64 s[70:71], 60, v180
	buffer_load_dwordx4 v[206:209], v200, s[36:39], 0 offen nt
	s_and_b64 s[72:73], s[68:69], s[64:65]
	s_and_b64 s[74:75], s[68:69], s[66:67]
	s_and_b64 s[76:77], s[70:71], s[64:65]
	s_and_b64 s[78:79], s[70:71], s[66:67]
	v_add_u32_e32 v245, 0xfffe7c00, v200
	v_add_u32_e32 v246, 0xfffe8000, v200
	s_mov_b64 exec, s[72:73]
	buffer_load_dwordx4 v[122:125], v245, s[36:39], 0 offen
	buffer_load_dwordx4 v[82:85], v245, s[36:39], 0 offen offset:512
	s_mov_b64 exec, -1
	s_mov_b64 exec, s[68:69]
	buffer_load_dwordx4 v[138:141], v246, s[36:39], 0 offen offset:512
	buffer_load_dwordx4 v[106:109], v246, s[36:39], 0 offen offset:1024
	s_mov_b64 exec, -1
	s_mov_b64 exec, s[74:75]
	buffer_load_dwordx4 v[146:149], v246, s[36:39], 0 offen offset:2048
	buffer_load_dwordx4 v[126:129], v246, s[36:39], 0 offen offset:2560
	s_mov_b64 exec, -1
	v_add_u32_e32 v245, 0xfffffc00, v200
	s_mov_b64 exec, s[64:65]
	buffer_load_dwordx4 v[94:97], v245, s[36:39], 0 offen
	buffer_load_dwordx4 v[54:57], v245, s[36:39], 0 offen offset:512
	s_mov_b64 exec, -1
	buffer_load_dwordx4 v[118:121], v200, s[36:39], 0 offen offset:512
	buffer_load_dwordx4 v[74:77], v200, s[36:39], 0 offen offset:1024
	s_mov_b64 exec, s[66:67]
	buffer_load_dwordx4 v[134:137], v200, s[36:39], 0 offen offset:2048
	buffer_load_dwordx4 v[98:101], v200, s[36:39], 0 offen offset:2560
	s_mov_b64 exec, -1
	v_add_u32_e32 v245, 0x17c00, v200
	v_add_u32_e32 v246, 0x18000, v200
	s_mov_b64 exec, s[64:65]
	buffer_load_dwordx4 v[62:65], v245, s[36:39], 0 offen
	buffer_load_dwordx4 v[30:33], v245, s[36:39], 0 offen offset:512
	s_mov_b64 exec, -1
	buffer_load_dwordx4 v[78:81], v246, s[36:39], 0 offen offset:512
	buffer_load_dwordx4 v[42:45], v246, s[36:39], 0 offen offset:1024
	s_mov_b64 exec, s[66:67]
	buffer_load_dwordx4 v[102:105], v246, s[36:39], 0 offen offset:2048
	buffer_load_dwordx4 v[58:61], v246, s[36:39], 0 offen offset:2560
	s_mov_b64 exec, -1
	v_add_u32_e32 v245, 0x18000, v200
	buffer_load_dwordx4 v[162:165], v245, s[36:39], 0 offen nt
	v_add_u32_e32 v246, 0x30000, v200
	buffer_load_dwordx4 v[158:161], v246, s[36:39], 0 offen nt
	v_add_u32_e32 v245, 0x2fc00, v200
	v_add_u32_e32 v246, 0x30000, v200
	v_add_u32_e32 v247, 0x47c00, v200
	v_add_u32_e32 v248, 0x48000, v200
	v_add_u32_e32 v249, 0x5fc00, v200
	v_add_u32_e32 v250, 0x60000, v200
	s_waitcnt vmcnt(22)
	v_cvt_pk_f16_f32 v6, v2, v3
	v_cvt_pk_f16_f32 v2, v8, v9
	v_cvt_pk_f16_f32 v7, v4, v5
	v_cvt_pk_f16_f32 v3, v10, v11
	v_cvt_pk_f16_f32 v8, v210, v211
	v_cvt_pk_f16_f32 v4, v214, v215
	v_cvt_pk_f16_f32 v9, v212, v213
	v_cvt_pk_f16_f32 v5, v216, v217
	s_not_b64 exec, s[72:73]
	s_cbranch_execz .Lmyf_C1_0
	v_mov_b32_e32 v122, v6
	v_mov_b32_e32 v123, v7
	v_mov_b32_e32 v124, v8
	v_mov_b32_e32 v125, v9
	v_mov_b32_e32 v82, v2
	v_mov_b32_e32 v83, v3
	v_mov_b32_e32 v84, v4
	v_mov_b32_e32 v85, v5

.Lmyf_C1_7:
	s_mov_b64 exec, -1
	s_waitcnt vmcnt(21)
	v_cvt_f16_f32_e32 v202, v155
	v_cvt_f16_f32_e32 v204, v154
	v_cvt_f16_f32_e32 v203, v156
	v_add_u32_e32 v251, 0x48000, v200
	buffer_load_dwordx4 v[154:157], v251, s[36:39], 0 offen nt
	s_mov_b64 s[4:5], 0
	s_waitcnt vmcnt(3)
	v_pk_mul_f16 v212, v204, v209 op_sel_hi:[0,1]
	v_pk_mul_f16 v216, v202, v209 op_sel_hi:[0,1]
	v_pk_mul_f16 v220, v203, v209 op_sel_hi:[0,1]
	v_pk_mul_f16 v205, v204, v206 op_sel_hi:[0,1]
	v_pk_mul_f16 v210, v204, v207 op_sel_hi:[0,1]
	v_pk_mul_f16 v211, v204, v208 op_sel_hi:[0,1]
	v_pk_mul_f16 v213, v202, v206 op_sel_hi:[0,1]
	s_mov_b64 exec, s[64:65]
	buffer_load_dwordx4 v[34:37], v245, s[36:39], 0 offen
	buffer_load_dwordx4 v[18:21], v245, s[36:39], 0 offen offset:512
	s_mov_b64 exec, -1
	v_pk_mul_f16 v214, v202, v207 op_sel_hi:[0,1]
	v_pk_mul_f16 v215, v202, v208 op_sel_hi:[0,1]
	v_pk_mul_f16 v217, v203, v206 op_sel_hi:[0,1]
	v_pk_mul_f16 v218, v203, v207 op_sel_hi:[0,1]
	v_pk_mul_f16 v219, v203, v208 op_sel_hi:[0,1]
	v_pk_fma_f16 v125, v125, v209, v212
	v_pk_fma_f16 v141, v141, v209, v216
	v_pk_fma_f16 v149, v149, v209, v220
	v_pk_fma_f16 v221, v97, v209, v212
	v_pk_fma_f16 v225, v121, v209, v216
	v_pk_fma_f16 v229, v137, v209, v220
	v_pk_fma_f16 v212, v65, v209, v212
	v_pk_fma_f16 v216, v81, v209, v216
	buffer_load_dwordx4 v[46:49], v246, s[36:39], 0 offen offset:512
	buffer_load_dwordx4 v[22:25], v246, s[36:39], 0 offen offset:1024
	v_pk_fma_f16 v209, v105, v209, v220
	v_pk_maximum3_f16 v220, v125, v141, v149
	v_pk_fma_f16 v124, v124, v208, v211
	v_pk_fma_f16 v123, v123, v207, v210
	v_pk_fma_f16 v122, v122, v206, v205
	v_pk_fma_f16 v140, v140, v208, v215
	v_pk_fma_f16 v139, v139, v207, v214
	v_pk_fma_f16 v138, v138, v206, v213
	v_pk_fma_f16 v148, v148, v208, v219
	v_pk_fma_f16 v147, v147, v207, v218
	v_pk_fma_f16 v146, v146, v206, v217
	v_pk_fma_f16 v222, v96, v208, v211
	v_pk_fma_f16 v223, v95, v207, v210
	v_pk_fma_f16 v224, v94, v206, v205
	v_pk_fma_f16 v226, v120, v208, v215
	v_pk_fma_f16 v227, v119, v207, v214
	s_mov_b64 exec, s[66:67]
	buffer_load_dwordx4 v[66:69], v246, s[36:39], 0 offen offset:2048
	buffer_load_dwordx4 v[26:29], v246, s[36:39], 0 offen offset:2560
	s_mov_b64 exec, -1
	v_pk_fma_f16 v228, v118, v206, v213
	v_pk_fma_f16 v230, v136, v208, v219
	v_pk_fma_f16 v231, v135, v207, v218
	v_pk_fma_f16 v232, v134, v206, v217
	v_pk_fma_f16 v211, v64, v208, v211
	v_pk_fma_f16 v210, v63, v207, v210
	v_pk_fma_f16 v205, v62, v206, v205
	v_pk_fma_f16 v215, v80, v208, v215
	v_pk_fma_f16 v214, v79, v207, v214
	v_pk_fma_f16 v213, v78, v206, v213
	v_pk_fma_f16 v208, v104, v208, v219
	v_pk_fma_f16 v207, v103, v207, v218
	v_pk_fma_f16 v206, v102, v206, v217
	v_pk_maximum3_f16 v217, v122, v138, v146
	v_pk_maximum3_f16 v218, v123, v139, v147
	v_pk_maximum3_f16 v219, v124, v140, v148
	v_pk_maximum3_f16 v236, v221, v225, v229
	v_pk_maximum3_f16 v240, v212, v216, v209
	v_pk_maximum3_f16 v233, v224, v228, v232
	v_pk_maximum3_f16 v234, v223, v227, v231
	v_pk_maximum3_f16 v235, v222, v226, v230
	v_pk_maximum3_f16 v237, v205, v213, v206
	v_pk_maximum3_f16 v238, v210, v214, v207
	v_pk_maximum3_f16 v220, v220, v236, v240
	v_pk_maximum3_f16 v239, v211, v215, v208
	v_pk_maximum3_f16 v217, v217, v233, v237
	v_pk_maximum3_f16 v218, v218, v234, v238
	v_pk_maximum3_f16 v219, v219, v235, v239
	v_pk_add_f16 v125, v125, v220 neg_lo:[0,1] neg_hi:[0,1]
	s_mov_b64 exec, s[64:65]
	buffer_load_dwordx4 v[86:89], v247, s[36:39], 0 offen
	buffer_load_dwordx4 v[38:41], v247, s[36:39], 0 offen offset:512
	s_mov_b64 exec, -1
	v_pk_add_f16 v122, v122, v217 neg_lo:[0,1] neg_hi:[0,1]
	v_pk_add_f16 v123, v123, v218 neg_lo:[0,1] neg_hi:[0,1]
	v_pk_add_f16 v124, v124, v219 neg_lo:[0,1] neg_hi:[0,1]
	v_pk_add_f16 v138, v138, v217 neg_lo:[0,1] neg_hi:[0,1]
	v_exp_f16_sdwa v233, v122 dst_sel:WORD_0 dst_unused:UNUSED_PAD src0_sel:WORD_0
	v_exp_f16_sdwa v234, v123 dst_sel:WORD_0 dst_unused:UNUSED_PAD src0_sel:WORD_0
	v_exp_f16_sdwa v235, v124 dst_sel:WORD_0 dst_unused:UNUSED_PAD src0_sel:WORD_0
	v_exp_f16_sdwa v236, v125 dst_sel:WORD_0 dst_unused:UNUSED_PAD src0_sel:WORD_0
	v_exp_f16_sdwa v233, v122 dst_sel:WORD_1 dst_unused:UNUSED_PRESERVE src0_sel:WORD_1
	v_exp_f16_sdwa v234, v123 dst_sel:WORD_1 dst_unused:UNUSED_PRESERVE src0_sel:WORD_1
	v_exp_f16_sdwa v235, v124 dst_sel:WORD_1 dst_unused:UNUSED_PRESERVE src0_sel:WORD_1
	v_exp_f16_sdwa v236, v125 dst_sel:WORD_1 dst_unused:UNUSED_PRESERVE src0_sel:WORD_1
	v_pk_add_f16 v139, v139, v218 neg_lo:[0,1] neg_hi:[0,1]
	v_pk_add_f16 v125, v233, 0
	v_pk_fma_f16 v85, v85, v236, 0
	v_pk_add_f16 v122, v236, 0
	v_pk_add_f16 v123, v235, 0
	v_pk_add_f16 v124, v234, 0
	v_pk_fma_f16 v84, v84, v235, 0
	v_pk_fma_f16 v83, v83, v234, 0
	v_pk_fma_f16 v82, v82, v233, 0
	v_pk_add_f16 v140, v140, v219 neg_lo:[0,1] neg_hi:[0,1]
	buffer_load_dwordx4 v[114:117], v248, s[36:39], 0 offen offset:512
	buffer_load_dwordx4 v[50:53], v248, s[36:39], 0 offen offset:1024
	v_pk_add_f16 v141, v141, v220 neg_lo:[0,1] neg_hi:[0,1]
	v_exp_f16_sdwa v233, v138 dst_sel:WORD_0 dst_unused:UNUSED_PAD src0_sel:WORD_0
	v_exp_f16_sdwa v234, v139 dst_sel:WORD_0 dst_unused:UNUSED_PAD src0_sel:WORD_0
	v_exp_f16_sdwa v235, v140 dst_sel:WORD_0 dst_unused:UNUSED_PAD src0_sel:WORD_0
	v_exp_f16_sdwa v236, v141 dst_sel:WORD_0 dst_unused:UNUSED_PAD src0_sel:WORD_0
	v_exp_f16_sdwa v233, v138 dst_sel:WORD_1 dst_unused:UNUSED_PRESERVE src0_sel:WORD_1
	v_exp_f16_sdwa v234, v139 dst_sel:WORD_1 dst_unused:UNUSED_PRESERVE src0_sel:WORD_1
	v_exp_f16_sdwa v235, v140 dst_sel:WORD_1 dst_unused:UNUSED_PRESERVE src0_sel:WORD_1
	v_exp_f16_sdwa v236, v141 dst_sel:WORD_1 dst_unused:UNUSED_PRESERVE src0_sel:WORD_1
	v_pk_add_f16 v125, v125, v233
	v_pk_fma_f16 v85, v109, v236, v85
	v_pk_add_f16 v109, v149, v220 neg_lo:[0,1] neg_hi:[0,1]
	v_pk_add_f16 v124, v124, v234
	v_pk_add_f16 v123, v123, v235
	v_pk_add_f16 v122, v122, v236
	v_pk_fma_f16 v82, v106, v233, v82
	v_pk_fma_f16 v83, v107, v234, v83
	v_pk_fma_f16 v84, v108, v235, v84
	v_pk_add_f16 v106, v146, v217 neg_lo:[0,1] neg_hi:[0,1]
	v_pk_add_f16 v107, v147, v218 neg_lo:[0,1] neg_hi:[0,1]
	v_pk_add_f16 v108, v148, v219 neg_lo:[0,1] neg_hi:[0,1]
	v_exp_f16_sdwa v138, v106 dst_sel:WORD_0 dst_unused:UNUSED_PAD src0_sel:WORD_0
	v_exp_f16_sdwa v139, v107 dst_sel:WORD_0 dst_unused:UNUSED_PAD src0_sel:WORD_0
	v_exp_f16_sdwa v140, v108 dst_sel:WORD_0 dst_unused:UNUSED_PAD src0_sel:WORD_0
	v_exp_f16_sdwa v141, v109 dst_sel:WORD_0 dst_unused:UNUSED_PAD src0_sel:WORD_0
	v_exp_f16_sdwa v138, v106 dst_sel:WORD_1 dst_unused:UNUSED_PRESERVE src0_sel:WORD_1
	v_exp_f16_sdwa v139, v107 dst_sel:WORD_1 dst_unused:UNUSED_PRESERVE src0_sel:WORD_1
	v_exp_f16_sdwa v140, v108 dst_sel:WORD_1 dst_unused:UNUSED_PRESERVE src0_sel:WORD_1
	v_exp_f16_sdwa v141, v109 dst_sel:WORD_1 dst_unused:UNUSED_PRESERVE src0_sel:WORD_1
	v_pk_add_f16 v109, v125, v138
	v_pk_add_f16 v106, v122, v141
	s_mov_b64 exec, s[66:67]
	buffer_load_dwordx4 v[130:133], v248, s[36:39], 0 offen offset:2048
	buffer_load_dwordx4 v[70:73], v248, s[36:39], 0 offen offset:2560
	s_mov_b64 exec, -1
	v_pk_add_f16 v107, v123, v140
	v_pk_add_f16 v108, v124, v139
	v_pk_fma_f16 v85, v129, v141, v85
	v_pk_fma_f16 v84, v128, v140, v84
	v_pk_fma_f16 v83, v127, v139, v83
	v_pk_fma_f16 v82, v126, v138, v82
	v_pk_add_f16 v122, v224, v217 neg_lo:[0,1] neg_hi:[0,1]
	v_pk_add_f16 v123, v223, v218 neg_lo:[0,1] neg_hi:[0,1]
	v_pk_add_f16 v124, v222, v219 neg_lo:[0,1] neg_hi:[0,1]
	v_pk_add_f16 v125, v221, v220 neg_lo:[0,1] neg_hi:[0,1]
	v_exp_f16_sdwa v126, v122 dst_sel:WORD_0 dst_unused:UNUSED_PAD src0_sel:WORD_0
	v_exp_f16_sdwa v127, v123 dst_sel:WORD_0 dst_unused:UNUSED_PAD src0_sel:WORD_0
	v_exp_f16_sdwa v128, v124 dst_sel:WORD_0 dst_unused:UNUSED_PAD src0_sel:WORD_0
	v_exp_f16_sdwa v129, v125 dst_sel:WORD_0 dst_unused:UNUSED_PAD src0_sel:WORD_0
	v_exp_f16_sdwa v126, v122 dst_sel:WORD_1 dst_unused:UNUSED_PRESERVE src0_sel:WORD_1
	v_exp_f16_sdwa v127, v123 dst_sel:WORD_1 dst_unused:UNUSED_PRESERVE src0_sel:WORD_1
	v_exp_f16_sdwa v128, v124 dst_sel:WORD_1 dst_unused:UNUSED_PRESERVE src0_sel:WORD_1
	v_exp_f16_sdwa v129, v125 dst_sel:WORD_1 dst_unused:UNUSED_PRESERVE src0_sel:WORD_1
	v_pk_add_f16 v122, v228, v217 neg_lo:[0,1] neg_hi:[0,1]
	v_pk_add_f16 v109, v109, v126
	v_pk_add_f16 v108, v108, v127
	v_pk_add_f16 v107, v107, v128
	s_mov_b64 exec, s[76:77]
	buffer_load_dwordx4 v[142:145], v249, s[36:39], 0 offen
	buffer_load_dwordx4 v[90:93], v249, s[36:39], 0 offen offset:512
	s_mov_b64 exec, -1
	v_pk_add_f16 v106, v106, v129
	v_pk_fma_f16 v82, v54, v126, v82
	v_pk_fma_f16 v83, v55, v127, v83
	v_pk_fma_f16 v84, v56, v128, v84
	v_pk_fma_f16 v85, v57, v129, v85
	v_pk_add_f16 v123, v227, v218 neg_lo:[0,1] neg_hi:[0,1]
	v_pk_add_f16 v124, v226, v219 neg_lo:[0,1] neg_hi:[0,1]
	v_pk_add_f16 v125, v225, v220 neg_lo:[0,1] neg_hi:[0,1]
	v_exp_f16_sdwa v126, v122 dst_sel:WORD_0 dst_unused:UNUSED_PAD src0_sel:WORD_0
	v_exp_f16_sdwa v127, v123 dst_sel:WORD_0 dst_unused:UNUSED_PAD src0_sel:WORD_0
	v_exp_f16_sdwa v128, v124 dst_sel:WORD_0 dst_unused:UNUSED_PAD src0_sel:WORD_0
	v_exp_f16_sdwa v129, v125 dst_sel:WORD_0 dst_unused:UNUSED_PAD src0_sel:WORD_0
	v_exp_f16_sdwa v126, v122 dst_sel:WORD_1 dst_unused:UNUSED_PRESERVE src0_sel:WORD_1
	v_exp_f16_sdwa v127, v123 dst_sel:WORD_1 dst_unused:UNUSED_PRESERVE src0_sel:WORD_1
	v_exp_f16_sdwa v128, v124 dst_sel:WORD_1 dst_unused:UNUSED_PRESERVE src0_sel:WORD_1
	v_exp_f16_sdwa v129, v125 dst_sel:WORD_1 dst_unused:UNUSED_PRESERVE src0_sel:WORD_1
	v_pk_add_f16 v122, v232, v217 neg_lo:[0,1] neg_hi:[0,1]
	v_pk_add_f16 v109, v109, v126
	v_pk_add_f16 v106, v106, v129
	v_pk_add_f16 v107, v107, v128
	v_pk_add_f16 v108, v108, v127
	v_pk_fma_f16 v85, v77, v129, v85
	v_pk_fma_f16 v84, v76, v128, v84
	s_mov_b64 exec, s[70:71]
	buffer_load_dwordx4 v[150:153], v250, s[36:39], 0 offen offset:512
	buffer_load_dwordx4 v[110:113], v250, s[36:39], 0 offen offset:1024
	s_mov_b64 exec, -1
	v_pk_fma_f16 v83, v75, v127, v83
	v_pk_fma_f16 v82, v74, v126, v82
	v_pk_add_f16 v123, v231, v218 neg_lo:[0,1] neg_hi:[0,1]
	v_pk_add_f16 v124, v230, v219 neg_lo:[0,1] neg_hi:[0,1]
	v_pk_add_f16 v125, v229, v220 neg_lo:[0,1] neg_hi:[0,1]
	v_exp_f16_sdwa v126, v122 dst_sel:WORD_0 dst_unused:UNUSED_PAD src0_sel:WORD_0
	v_exp_f16_sdwa v127, v123 dst_sel:WORD_0 dst_unused:UNUSED_PAD src0_sel:WORD_0
	v_exp_f16_sdwa v128, v124 dst_sel:WORD_0 dst_unused:UNUSED_PAD src0_sel:WORD_0
	v_exp_f16_sdwa v129, v125 dst_sel:WORD_0 dst_unused:UNUSED_PAD src0_sel:WORD_0
	v_exp_f16_sdwa v126, v122 dst_sel:WORD_1 dst_unused:UNUSED_PRESERVE src0_sel:WORD_1
	v_exp_f16_sdwa v127, v123 dst_sel:WORD_1 dst_unused:UNUSED_PRESERVE src0_sel:WORD_1
	v_exp_f16_sdwa v128, v124 dst_sel:WORD_1 dst_unused:UNUSED_PRESERVE src0_sel:WORD_1
	v_exp_f16_sdwa v129, v125 dst_sel:WORD_1 dst_unused:UNUSED_PRESERVE src0_sel:WORD_1
	v_pk_add_f16 v122, v205, v217 neg_lo:[0,1] neg_hi:[0,1]
	v_pk_add_f16 v109, v109, v126
	v_pk_add_f16 v108, v108, v127
	v_pk_add_f16 v107, v107, v128
	v_pk_add_f16 v106, v106, v129
	v_pk_fma_f16 v82, v98, v126, v82
	v_pk_fma_f16 v83, v99, v127, v83
	v_pk_fma_f16 v84, v100, v128, v84
	v_pk_fma_f16 v85, v101, v129, v85
	s_mov_b64 exec, s[78:79]
	buffer_load_dwordx4 v[14:17], v250, s[36:39], 0 offen offset:2048
	buffer_load_dwordx4 v[10:13], v250, s[36:39], 0 offen offset:2560
	s_mov_b64 exec, -1
	v_pk_add_f16 v123, v210, v218 neg_lo:[0,1] neg_hi:[0,1]
	v_pk_add_f16 v124, v211, v219 neg_lo:[0,1] neg_hi:[0,1]
	v_pk_add_f16 v125, v212, v220 neg_lo:[0,1] neg_hi:[0,1]
	v_exp_f16_sdwa v126, v122 dst_sel:WORD_0 dst_unused:UNUSED_PAD src0_sel:WORD_0
	v_exp_f16_sdwa v127, v123 dst_sel:WORD_0 dst_unused:UNUSED_PAD src0_sel:WORD_0
	v_exp_f16_sdwa v128, v124 dst_sel:WORD_0 dst_unused:UNUSED_PAD src0_sel:WORD_0
	v_exp_f16_sdwa v129, v125 dst_sel:WORD_0 dst_unused:UNUSED_PAD src0_sel:WORD_0
	v_exp_f16_sdwa v126, v122 dst_sel:WORD_1 dst_unused:UNUSED_PRESERVE src0_sel:WORD_1
	v_exp_f16_sdwa v127, v123 dst_sel:WORD_1 dst_unused:UNUSED_PRESERVE src0_sel:WORD_1
	v_exp_f16_sdwa v128, v124 dst_sel:WORD_1 dst_unused:UNUSED_PRESERVE src0_sel:WORD_1
	v_exp_f16_sdwa v129, v125 dst_sel:WORD_1 dst_unused:UNUSED_PRESERVE src0_sel:WORD_1
	v_pk_add_f16 v122, v213, v217 neg_lo:[0,1] neg_hi:[0,1]
	v_pk_add_f16 v109, v109, v126
	v_pk_add_f16 v106, v106, v129
	v_pk_add_f16 v107, v107, v128
	v_pk_add_f16 v108, v108, v127
	v_pk_fma_f16 v85, v33, v129, v85
	v_pk_fma_f16 v84, v32, v128, v84
	v_pk_fma_f16 v83, v31, v127, v83
	v_pk_fma_f16 v82, v30, v126, v82
	v_pk_add_f16 v123, v214, v218 neg_lo:[0,1] neg_hi:[0,1]
	v_pk_add_f16 v124, v215, v219 neg_lo:[0,1] neg_hi:[0,1]
	v_pk_add_f16 v125, v216, v220 neg_lo:[0,1] neg_hi:[0,1]
	v_exp_f16_sdwa v126, v122 dst_sel:WORD_0 dst_unused:UNUSED_PAD src0_sel:WORD_0
	v_exp_f16_sdwa v127, v123 dst_sel:WORD_0 dst_unused:UNUSED_PAD src0_sel:WORD_0
	v_exp_f16_sdwa v128, v124 dst_sel:WORD_0 dst_unused:UNUSED_PAD src0_sel:WORD_0
	v_exp_f16_sdwa v129, v125 dst_sel:WORD_0 dst_unused:UNUSED_PAD src0_sel:WORD_0
	v_exp_f16_sdwa v126, v122 dst_sel:WORD_1 dst_unused:UNUSED_PRESERVE src0_sel:WORD_1
	v_exp_f16_sdwa v127, v123 dst_sel:WORD_1 dst_unused:UNUSED_PRESERVE src0_sel:WORD_1
	v_exp_f16_sdwa v128, v124 dst_sel:WORD_1 dst_unused:UNUSED_PRESERVE src0_sel:WORD_1
	v_exp_f16_sdwa v129, v125 dst_sel:WORD_1 dst_unused:UNUSED_PRESERVE src0_sel:WORD_1
	v_pk_add_f16 v122, v206, v217 neg_lo:[0,1] neg_hi:[0,1]
	v_pk_add_f16 v109, v109, v126
	v_pk_add_f16 v108, v108, v127
	v_pk_add_f16 v107, v107, v128
	v_pk_add_f16 v106, v106, v129
	v_pk_fma_f16 v82, v42, v126, v82
	v_pk_fma_f16 v83, v43, v127, v83
	v_pk_fma_f16 v84, v44, v128, v84
	v_pk_fma_f16 v85, v45, v129, v85
	v_pk_add_f16 v123, v207, v218 neg_lo:[0,1] neg_hi:[0,1]
	v_pk_add_f16 v124, v208, v219 neg_lo:[0,1] neg_hi:[0,1]
	v_pk_add_f16 v125, v209, v220 neg_lo:[0,1] neg_hi:[0,1]
	v_exp_f16_sdwa v126, v122 dst_sel:WORD_0 dst_unused:UNUSED_PAD src0_sel:WORD_0
	v_exp_f16_sdwa v127, v123 dst_sel:WORD_0 dst_unused:UNUSED_PAD src0_sel:WORD_0
	v_exp_f16_sdwa v128, v124 dst_sel:WORD_0 dst_unused:UNUSED_PAD src0_sel:WORD_0
	v_exp_f16_sdwa v129, v125 dst_sel:WORD_0 dst_unused:UNUSED_PAD src0_sel:WORD_0
	v_exp_f16_sdwa v126, v122 dst_sel:WORD_1 dst_unused:UNUSED_PRESERVE src0_sel:WORD_1
	v_exp_f16_sdwa v127, v123 dst_sel:WORD_1 dst_unused:UNUSED_PRESERVE src0_sel:WORD_1
	v_exp_f16_sdwa v128, v124 dst_sel:WORD_1 dst_unused:UNUSED_PRESERVE src0_sel:WORD_1
	v_exp_f16_sdwa v129, v125 dst_sel:WORD_1 dst_unused:UNUSED_PRESERVE src0_sel:WORD_1
	v_pk_add_f16 v109, v109, v126
	v_pk_add_f16 v108, v108, v127
	v_rcp_f16_e32 v122, v109
	v_rcp_f16_sdwa v109, v109 dst_sel:DWORD dst_unused:UNUSED_PAD src0_sel:WORD_1
	v_pk_add_f16 v107, v107, v128
	v_rcp_f16_e32 v123, v108
	v_rcp_f16_sdwa v108, v108 dst_sel:DWORD dst_unused:UNUSED_PAD src0_sel:WORD_1
	v_pk_add_f16 v106, v106, v129
	v_rcp_f16_e32 v124, v107
	v_rcp_f16_sdwa v107, v107 dst_sel:DWORD dst_unused:UNUSED_PAD src0_sel:WORD_1
	v_rcp_f16_e32 v125, v106
	v_rcp_f16_sdwa v106, v106 dst_sel:DWORD dst_unused:UNUSED_PAD src0_sel:WORD_1
	v_pk_fma_f16 v82, v58, v126, v82
	v_pack_b32_f16 v109, v122, v109
	v_pk_fma_f16 v83, v59, v127, v83
	v_pk_mul_f16 v138, v82, v109
	v_pack_b32_f16 v82, v123, v108
	v_pk_fma_f16 v84, v60, v128, v84
	v_pk_mul_f16 v139, v83, v82
	v_pack_b32_f16 v82, v124, v107
	v_pk_fma_f16 v85, v61, v129, v85
	v_pk_mul_f16 v140, v84, v82
	v_pack_b32_f16 v82, v125, v106
	v_pk_mul_f16 v141, v85, v82
	s_waitcnt vmcnt(12)
	v_pk_mul_f16 v85, v204, v165 op_sel_hi:[0,1]
	v_pk_mul_f16 v109, v202, v165 op_sel_hi:[0,1]
	v_pk_mul_f16 v122, v203, v162 op_sel_hi:[0,1]
	v_pk_mul_f16 v125, v203, v165 op_sel_hi:[0,1]
	v_pk_mul_f16 v82, v204, v162 op_sel_hi:[0,1]
	v_pk_mul_f16 v83, v204, v163 op_sel_hi:[0,1]
	v_pk_mul_f16 v84, v204, v164 op_sel_hi:[0,1]
	v_pk_mul_f16 v106, v202, v162 op_sel_hi:[0,1]
	v_pk_mul_f16 v107, v202, v163 op_sel_hi:[0,1]
	v_pk_mul_f16 v108, v202, v164 op_sel_hi:[0,1]
	v_pk_mul_f16 v123, v203, v163 op_sel_hi:[0,1]
	v_pk_mul_f16 v124, v203, v164 op_sel_hi:[0,1]
	v_pk_fma_f16 v97, v97, v165, v85
	v_pk_fma_f16 v121, v121, v165, v109
	v_pk_fma_f16 v126, v137, v165, v125
	v_pk_fma_f16 v129, v134, v162, v122
	v_pk_fma_f16 v134, v65, v165, v85
	v_pk_fma_f16 v146, v81, v165, v109
	v_pk_fma_f16 v205, v105, v165, v125
	v_pk_fma_f16 v85, v37, v165, v85
	v_pk_fma_f16 v109, v49, v165, v109
	v_pk_fma_f16 v125, v69, v165, v125
	v_pk_maximum3_f16 v165, v97, v121, v126
	v_pk_fma_f16 v96, v96, v164, v84
	v_pk_fma_f16 v95, v95, v163, v83
	v_pk_fma_f16 v94, v94, v162, v82
	v_pk_fma_f16 v120, v120, v164, v108
	v_pk_fma_f16 v119, v119, v163, v107
	v_pk_fma_f16 v118, v118, v162, v106
	v_pk_fma_f16 v127, v136, v164, v124
	v_pk_fma_f16 v128, v135, v163, v123
	v_pk_fma_f16 v135, v64, v164, v84
	v_pk_fma_f16 v136, v63, v163, v83
	v_pk_fma_f16 v137, v62, v162, v82
	v_pk_fma_f16 v147, v80, v164, v108
	v_pk_fma_f16 v148, v79, v163, v107
	v_pk_fma_f16 v149, v78, v162, v106
	v_pk_fma_f16 v206, v104, v164, v124
	v_pk_fma_f16 v207, v103, v163, v123
	v_pk_fma_f16 v208, v102, v162, v122
	v_pk_fma_f16 v84, v36, v164, v84
	v_pk_fma_f16 v83, v35, v163, v83
	v_pk_fma_f16 v82, v34, v162, v82
	v_pk_fma_f16 v108, v48, v164, v108
	v_pk_fma_f16 v107, v47, v163, v107
	v_pk_fma_f16 v106, v46, v162, v106
	v_pk_fma_f16 v124, v68, v164, v124
	v_pk_fma_f16 v123, v67, v163, v123
	v_pk_fma_f16 v122, v66, v162, v122
	v_pk_maximum3_f16 v162, v94, v118, v129
	v_pk_maximum3_f16 v163, v95, v119, v128
	v_pk_maximum3_f16 v164, v96, v120, v127
	v_pk_maximum3_f16 v212, v134, v146, v205
	v_pk_maximum3_f16 v216, v85, v109, v125
	v_pk_maximum3_f16 v209, v137, v149, v208
	v_pk_maximum3_f16 v210, v136, v148, v207
	v_pk_maximum3_f16 v211, v135, v147, v206
	v_pk_maximum3_f16 v213, v82, v106, v122
	v_pk_maximum3_f16 v214, v83, v107, v123
	v_pk_maximum3_f16 v165, v165, v212, v216
	v_pk_maximum3_f16 v215, v84, v108, v124
	v_pk_maximum3_f16 v162, v162, v209, v213
	v_pk_maximum3_f16 v163, v163, v210, v214
	v_pk_maximum3_f16 v164, v164, v211, v215
	v_pk_add_f16 v97, v97, v165 neg_lo:[0,1] neg_hi:[0,1]
	v_pk_add_f16 v94, v94, v162 neg_lo:[0,1] neg_hi:[0,1]
	v_pk_add_f16 v95, v95, v163 neg_lo:[0,1] neg_hi:[0,1]
	v_pk_add_f16 v96, v96, v164 neg_lo:[0,1] neg_hi:[0,1]
	v_pk_add_f16 v118, v118, v162 neg_lo:[0,1] neg_hi:[0,1]
	v_exp_f16_sdwa v209, v94 dst_sel:WORD_0 dst_unused:UNUSED_PAD src0_sel:WORD_0
	v_exp_f16_sdwa v210, v95 dst_sel:WORD_0 dst_unused:UNUSED_PAD src0_sel:WORD_0
	v_exp_f16_sdwa v211, v96 dst_sel:WORD_0 dst_unused:UNUSED_PAD src0_sel:WORD_0
	v_exp_f16_sdwa v212, v97 dst_sel:WORD_0 dst_unused:UNUSED_PAD src0_sel:WORD_0
	v_exp_f16_sdwa v209, v94 dst_sel:WORD_1 dst_unused:UNUSED_PRESERVE src0_sel:WORD_1
	v_exp_f16_sdwa v210, v95 dst_sel:WORD_1 dst_unused:UNUSED_PRESERVE src0_sel:WORD_1
	v_exp_f16_sdwa v211, v96 dst_sel:WORD_1 dst_unused:UNUSED_PRESERVE src0_sel:WORD_1
	v_exp_f16_sdwa v212, v97 dst_sel:WORD_1 dst_unused:UNUSED_PRESERVE src0_sel:WORD_1
	v_pk_add_f16 v119, v119, v163 neg_lo:[0,1] neg_hi:[0,1]
	v_pk_add_f16 v97, v209, 0
	v_pk_fma_f16 v57, v57, v212, 0
	v_pk_add_f16 v94, v212, 0
	v_pk_add_f16 v95, v211, 0
	v_pk_add_f16 v96, v210, 0
	v_pk_fma_f16 v56, v56, v211, 0
	v_pk_fma_f16 v55, v55, v210, 0
	v_pk_fma_f16 v54, v54, v209, 0
	v_pk_add_f16 v120, v120, v164 neg_lo:[0,1] neg_hi:[0,1]
	v_pk_add_f16 v121, v121, v165 neg_lo:[0,1] neg_hi:[0,1]
	v_pk_add_f16 v82, v82, v162 neg_lo:[0,1] neg_hi:[0,1]
	v_exp_f16_sdwa v209, v118 dst_sel:WORD_0 dst_unused:UNUSED_PAD src0_sel:WORD_0
	v_exp_f16_sdwa v210, v119 dst_sel:WORD_0 dst_unused:UNUSED_PAD src0_sel:WORD_0
	v_exp_f16_sdwa v211, v120 dst_sel:WORD_0 dst_unused:UNUSED_PAD src0_sel:WORD_0
	v_exp_f16_sdwa v212, v121 dst_sel:WORD_0 dst_unused:UNUSED_PAD src0_sel:WORD_0
	v_exp_f16_sdwa v209, v118 dst_sel:WORD_1 dst_unused:UNUSED_PRESERVE src0_sel:WORD_1
	v_exp_f16_sdwa v210, v119 dst_sel:WORD_1 dst_unused:UNUSED_PRESERVE src0_sel:WORD_1
	v_exp_f16_sdwa v211, v120 dst_sel:WORD_1 dst_unused:UNUSED_PRESERVE src0_sel:WORD_1
	v_exp_f16_sdwa v212, v121 dst_sel:WORD_1 dst_unused:UNUSED_PRESERVE src0_sel:WORD_1
	v_pk_add_f16 v83, v83, v163 neg_lo:[0,1] neg_hi:[0,1]
	v_pk_add_f16 v97, v97, v209
	v_pk_fma_f16 v57, v77, v212, v57
	v_pk_add_f16 v77, v126, v165 neg_lo:[0,1] neg_hi:[0,1]
	v_pk_add_f16 v96, v96, v210
	v_pk_add_f16 v95, v95, v211
	v_pk_add_f16 v94, v94, v212
	v_pk_fma_f16 v54, v74, v209, v54
	v_pk_fma_f16 v55, v75, v210, v55
	v_pk_fma_f16 v56, v76, v211, v56
	v_pk_add_f16 v74, v129, v162 neg_lo:[0,1] neg_hi:[0,1]
	v_pk_add_f16 v75, v128, v163 neg_lo:[0,1] neg_hi:[0,1]
	v_pk_add_f16 v76, v127, v164 neg_lo:[0,1] neg_hi:[0,1]
	v_pk_add_f16 v84, v84, v164 neg_lo:[0,1] neg_hi:[0,1]
	v_exp_f16_sdwa v118, v74 dst_sel:WORD_0 dst_unused:UNUSED_PAD src0_sel:WORD_0
	v_exp_f16_sdwa v119, v75 dst_sel:WORD_0 dst_unused:UNUSED_PAD src0_sel:WORD_0
	v_exp_f16_sdwa v120, v76 dst_sel:WORD_0 dst_unused:UNUSED_PAD src0_sel:WORD_0
	v_exp_f16_sdwa v121, v77 dst_sel:WORD_0 dst_unused:UNUSED_PAD src0_sel:WORD_0
	v_exp_f16_sdwa v118, v74 dst_sel:WORD_1 dst_unused:UNUSED_PRESERVE src0_sel:WORD_1
	v_exp_f16_sdwa v119, v75 dst_sel:WORD_1 dst_unused:UNUSED_PRESERVE src0_sel:WORD_1
	v_exp_f16_sdwa v120, v76 dst_sel:WORD_1 dst_unused:UNUSED_PRESERVE src0_sel:WORD_1
	v_exp_f16_sdwa v121, v77 dst_sel:WORD_1 dst_unused:UNUSED_PRESERVE src0_sel:WORD_1
	v_pk_add_f16 v85, v85, v165 neg_lo:[0,1] neg_hi:[0,1]
	v_pk_add_f16 v77, v97, v118
	v_pk_add_f16 v74, v94, v121
	v_pk_add_f16 v75, v95, v120
	v_pk_add_f16 v76, v96, v119
	v_pk_fma_f16 v57, v101, v121, v57
	v_pk_fma_f16 v56, v100, v120, v56
	v_pk_fma_f16 v55, v99, v119, v55
	v_pk_fma_f16 v54, v98, v118, v54
	v_pk_add_f16 v94, v137, v162 neg_lo:[0,1] neg_hi:[0,1]
	v_pk_add_f16 v95, v136, v163 neg_lo:[0,1] neg_hi:[0,1]
	v_pk_add_f16 v96, v135, v164 neg_lo:[0,1] neg_hi:[0,1]
	v_pk_add_f16 v97, v134, v165 neg_lo:[0,1] neg_hi:[0,1]
	v_exp_f16_sdwa v98, v94 dst_sel:WORD_0 dst_unused:UNUSED_PAD src0_sel:WORD_0
	v_exp_f16_sdwa v99, v95 dst_sel:WORD_0 dst_unused:UNUSED_PAD src0_sel:WORD_0
	v_exp_f16_sdwa v100, v96 dst_sel:WORD_0 dst_unused:UNUSED_PAD src0_sel:WORD_0
	v_exp_f16_sdwa v101, v97 dst_sel:WORD_0 dst_unused:UNUSED_PAD src0_sel:WORD_0
	v_exp_f16_sdwa v98, v94 dst_sel:WORD_1 dst_unused:UNUSED_PRESERVE src0_sel:WORD_1
	v_exp_f16_sdwa v99, v95 dst_sel:WORD_1 dst_unused:UNUSED_PRESERVE src0_sel:WORD_1
	v_exp_f16_sdwa v100, v96 dst_sel:WORD_1 dst_unused:UNUSED_PRESERVE src0_sel:WORD_1
	v_exp_f16_sdwa v101, v97 dst_sel:WORD_1 dst_unused:UNUSED_PRESERVE src0_sel:WORD_1
	v_pk_add_f16 v94, v149, v162 neg_lo:[0,1] neg_hi:[0,1]
	v_pk_add_f16 v77, v77, v98
	v_pk_add_f16 v76, v76, v99
	v_pk_add_f16 v75, v75, v100
	v_pk_add_f16 v74, v74, v101
	v_pk_fma_f16 v54, v30, v98, v54
	v_pk_fma_f16 v55, v31, v99, v55
	v_pk_fma_f16 v56, v32, v100, v56
	v_pk_fma_f16 v57, v33, v101, v57
	v_pk_add_f16 v95, v148, v163 neg_lo:[0,1] neg_hi:[0,1]
	v_pk_add_f16 v96, v147, v164 neg_lo:[0,1] neg_hi:[0,1]
	v_pk_add_f16 v97, v146, v165 neg_lo:[0,1] neg_hi:[0,1]
	v_exp_f16_sdwa v98, v94 dst_sel:WORD_0 dst_unused:UNUSED_PAD src0_sel:WORD_0
	v_exp_f16_sdwa v99, v95 dst_sel:WORD_0 dst_unused:UNUSED_PAD src0_sel:WORD_0
	v_exp_f16_sdwa v100, v96 dst_sel:WORD_0 dst_unused:UNUSED_PAD src0_sel:WORD_0
	v_exp_f16_sdwa v101, v97 dst_sel:WORD_0 dst_unused:UNUSED_PAD src0_sel:WORD_0
	v_exp_f16_sdwa v98, v94 dst_sel:WORD_1 dst_unused:UNUSED_PRESERVE src0_sel:WORD_1
	v_exp_f16_sdwa v99, v95 dst_sel:WORD_1 dst_unused:UNUSED_PRESERVE src0_sel:WORD_1
	v_exp_f16_sdwa v100, v96 dst_sel:WORD_1 dst_unused:UNUSED_PRESERVE src0_sel:WORD_1
	v_exp_f16_sdwa v101, v97 dst_sel:WORD_1 dst_unused:UNUSED_PRESERVE src0_sel:WORD_1
	v_pk_add_f16 v94, v208, v162 neg_lo:[0,1] neg_hi:[0,1]
	v_pk_add_f16 v77, v77, v98
	v_pk_add_f16 v74, v74, v101
	v_pk_add_f16 v75, v75, v100
	v_pk_add_f16 v76, v76, v99
	v_pk_fma_f16 v57, v45, v101, v57
	v_pk_fma_f16 v56, v44, v100, v56
	v_pk_fma_f16 v55, v43, v99, v55
	v_pk_fma_f16 v54, v42, v98, v54
	v_pk_add_f16 v95, v207, v163 neg_lo:[0,1] neg_hi:[0,1]
	v_pk_add_f16 v96, v206, v164 neg_lo:[0,1] neg_hi:[0,1]
	v_pk_add_f16 v97, v205, v165 neg_lo:[0,1] neg_hi:[0,1]
	v_exp_f16_sdwa v98, v94 dst_sel:WORD_0 dst_unused:UNUSED_PAD src0_sel:WORD_0
	v_exp_f16_sdwa v99, v95 dst_sel:WORD_0 dst_unused:UNUSED_PAD src0_sel:WORD_0
	v_exp_f16_sdwa v100, v96 dst_sel:WORD_0 dst_unused:UNUSED_PAD src0_sel:WORD_0
	v_exp_f16_sdwa v101, v97 dst_sel:WORD_0 dst_unused:UNUSED_PAD src0_sel:WORD_0
	v_exp_f16_sdwa v98, v94 dst_sel:WORD_1 dst_unused:UNUSED_PRESERVE src0_sel:WORD_1
	v_exp_f16_sdwa v99, v95 dst_sel:WORD_1 dst_unused:UNUSED_PRESERVE src0_sel:WORD_1
	v_exp_f16_sdwa v100, v96 dst_sel:WORD_1 dst_unused:UNUSED_PRESERVE src0_sel:WORD_1
	v_exp_f16_sdwa v101, v97 dst_sel:WORD_1 dst_unused:UNUSED_PRESERVE src0_sel:WORD_1
	v_exp_f16_sdwa v94, v82 dst_sel:WORD_0 dst_unused:UNUSED_PAD src0_sel:WORD_0
	v_exp_f16_sdwa v95, v83 dst_sel:WORD_0 dst_unused:UNUSED_PAD src0_sel:WORD_0
	v_exp_f16_sdwa v96, v84 dst_sel:WORD_0 dst_unused:UNUSED_PAD src0_sel:WORD_0
	v_exp_f16_sdwa v97, v85 dst_sel:WORD_0 dst_unused:UNUSED_PAD src0_sel:WORD_0
	v_exp_f16_sdwa v94, v82 dst_sel:WORD_1 dst_unused:UNUSED_PRESERVE src0_sel:WORD_1
	v_exp_f16_sdwa v95, v83 dst_sel:WORD_1 dst_unused:UNUSED_PRESERVE src0_sel:WORD_1
	v_exp_f16_sdwa v96, v84 dst_sel:WORD_1 dst_unused:UNUSED_PRESERVE src0_sel:WORD_1
	v_exp_f16_sdwa v97, v85 dst_sel:WORD_1 dst_unused:UNUSED_PRESERVE src0_sel:WORD_1
	v_pk_add_f16 v82, v106, v162 neg_lo:[0,1] neg_hi:[0,1]
	v_pk_add_f16 v77, v77, v98
	v_pk_add_f16 v76, v76, v99
	v_pk_add_f16 v75, v75, v100
	v_pk_add_f16 v74, v74, v101
	v_pk_fma_f16 v54, v58, v98, v54
	v_pk_fma_f16 v55, v59, v99, v55
	v_pk_fma_f16 v56, v60, v100, v56
	v_pk_fma_f16 v57, v61, v101, v57
	v_pk_add_f16 v77, v77, v94
	v_pk_add_f16 v74, v74, v97
	v_pk_add_f16 v75, v75, v96
	v_pk_add_f16 v76, v76, v95
	v_pk_fma_f16 v57, v21, v97, v57
	v_pk_fma_f16 v56, v20, v96, v56
	v_pk_fma_f16 v55, v19, v95, v55
	v_pk_fma_f16 v54, v18, v94, v54
	v_pk_add_f16 v83, v107, v163 neg_lo:[0,1] neg_hi:[0,1]
	v_pk_add_f16 v84, v108, v164 neg_lo:[0,1] neg_hi:[0,1]
	v_pk_add_f16 v85, v109, v165 neg_lo:[0,1] neg_hi:[0,1]
	v_exp_f16_sdwa v94, v82 dst_sel:WORD_0 dst_unused:UNUSED_PAD src0_sel:WORD_0
	v_exp_f16_sdwa v95, v83 dst_sel:WORD_0 dst_unused:UNUSED_PAD src0_sel:WORD_0
	v_exp_f16_sdwa v96, v84 dst_sel:WORD_0 dst_unused:UNUSED_PAD src0_sel:WORD_0
	v_exp_f16_sdwa v97, v85 dst_sel:WORD_0 dst_unused:UNUSED_PAD src0_sel:WORD_0
	v_exp_f16_sdwa v94, v82 dst_sel:WORD_1 dst_unused:UNUSED_PRESERVE src0_sel:WORD_1
	v_exp_f16_sdwa v95, v83 dst_sel:WORD_1 dst_unused:UNUSED_PRESERVE src0_sel:WORD_1
	v_exp_f16_sdwa v96, v84 dst_sel:WORD_1 dst_unused:UNUSED_PRESERVE src0_sel:WORD_1
	v_exp_f16_sdwa v97, v85 dst_sel:WORD_1 dst_unused:UNUSED_PRESERVE src0_sel:WORD_1
	v_pk_add_f16 v82, v122, v162 neg_lo:[0,1] neg_hi:[0,1]
	v_pk_add_f16 v77, v77, v94
	v_pk_add_f16 v76, v76, v95
	v_pk_add_f16 v75, v75, v96
	v_pk_add_f16 v74, v74, v97
	v_pk_fma_f16 v54, v22, v94, v54
	v_pk_fma_f16 v55, v23, v95, v55
	v_pk_fma_f16 v56, v24, v96, v56
	v_pk_fma_f16 v57, v25, v97, v57
	v_pk_add_f16 v83, v123, v163 neg_lo:[0,1] neg_hi:[0,1]
	v_pk_add_f16 v84, v124, v164 neg_lo:[0,1] neg_hi:[0,1]
	v_pk_add_f16 v85, v125, v165 neg_lo:[0,1] neg_hi:[0,1]
	v_exp_f16_sdwa v94, v82 dst_sel:WORD_0 dst_unused:UNUSED_PAD src0_sel:WORD_0
	v_exp_f16_sdwa v95, v83 dst_sel:WORD_0 dst_unused:UNUSED_PAD src0_sel:WORD_0
	v_exp_f16_sdwa v96, v84 dst_sel:WORD_0 dst_unused:UNUSED_PAD src0_sel:WORD_0
	v_exp_f16_sdwa v97, v85 dst_sel:WORD_0 dst_unused:UNUSED_PAD src0_sel:WORD_0
	v_exp_f16_sdwa v94, v82 dst_sel:WORD_1 dst_unused:UNUSED_PRESERVE src0_sel:WORD_1
	v_exp_f16_sdwa v95, v83 dst_sel:WORD_1 dst_unused:UNUSED_PRESERVE src0_sel:WORD_1
	v_exp_f16_sdwa v96, v84 dst_sel:WORD_1 dst_unused:UNUSED_PRESERVE src0_sel:WORD_1
	v_exp_f16_sdwa v97, v85 dst_sel:WORD_1 dst_unused:UNUSED_PRESERVE src0_sel:WORD_1
	v_pk_add_f16 v77, v77, v94
	v_pk_add_f16 v76, v76, v95
	v_rcp_f16_e32 v82, v77
	v_rcp_f16_sdwa v77, v77 dst_sel:DWORD dst_unused:UNUSED_PAD src0_sel:WORD_1
	v_pk_add_f16 v75, v75, v96
	v_rcp_f16_e32 v83, v76
	v_rcp_f16_sdwa v76, v76 dst_sel:DWORD dst_unused:UNUSED_PAD src0_sel:WORD_1
	v_pk_add_f16 v74, v74, v97
	v_rcp_f16_e32 v84, v75
	v_rcp_f16_sdwa v75, v75 dst_sel:DWORD dst_unused:UNUSED_PAD src0_sel:WORD_1
	v_rcp_f16_e32 v85, v74
	v_rcp_f16_sdwa v74, v74 dst_sel:DWORD dst_unused:UNUSED_PAD src0_sel:WORD_1
	v_pk_fma_f16 v54, v26, v94, v54
	v_pack_b32_f16 v77, v82, v77
	v_pk_fma_f16 v55, v27, v95, v55
	v_pk_mul_f16 v77, v54, v77
	v_pack_b32_f16 v54, v83, v76
	v_pk_fma_f16 v56, v28, v96, v56
	v_pk_mul_f16 v76, v55, v54
	v_pack_b32_f16 v54, v84, v75
	v_pk_fma_f16 v57, v29, v97, v57
	v_pk_mul_f16 v75, v56, v54
	v_pack_b32_f16 v54, v85, v74
	v_pk_mul_f16 v74, v57, v54
	s_waitcnt vmcnt(6)
	v_pk_mul_f16 v57, v204, v161 op_sel_hi:[0,1]
	v_pk_mul_f16 v85, v202, v161 op_sel_hi:[0,1]
	v_pk_mul_f16 v97, v203, v161 op_sel_hi:[0,1]
	v_pk_mul_f16 v54, v204, v158 op_sel_hi:[0,1]
	v_pk_mul_f16 v55, v204, v159 op_sel_hi:[0,1]
	v_pk_mul_f16 v56, v204, v160 op_sel_hi:[0,1]
	v_pk_mul_f16 v82, v202, v158 op_sel_hi:[0,1]
	v_pk_mul_f16 v83, v202, v159 op_sel_hi:[0,1]
	v_pk_mul_f16 v84, v202, v160 op_sel_hi:[0,1]
	v_pk_mul_f16 v94, v203, v158 op_sel_hi:[0,1]
	v_pk_mul_f16 v95, v203, v159 op_sel_hi:[0,1]
	v_pk_mul_f16 v96, v203, v160 op_sel_hi:[0,1]
	v_pk_fma_f16 v65, v65, v161, v57
	v_pk_fma_f16 v81, v81, v161, v85
	v_pk_fma_f16 v98, v105, v161, v97
	v_pk_fma_f16 v64, v64, v160, v56
	v_pk_maximum3_f16 v125, v65, v81, v98
	v_pk_fma_f16 v63, v63, v159, v55
	v_pk_fma_f16 v62, v62, v158, v54
	v_pk_fma_f16 v80, v80, v160, v84
	v_pk_fma_f16 v79, v79, v159, v83
	v_pk_fma_f16 v78, v78, v158, v82
	v_pk_fma_f16 v99, v104, v160, v96
	v_pk_fma_f16 v100, v103, v159, v95
	v_pk_fma_f16 v101, v102, v158, v94
	v_pk_fma_f16 v102, v37, v161, v57
	v_pk_fma_f16 v106, v49, v161, v85
	v_pk_fma_f16 v118, v69, v161, v97
	v_pk_fma_f16 v57, v89, v161, v57
	v_pk_fma_f16 v85, v117, v161, v85
	v_pk_fma_f16 v97, v133, v161, v97
	v_pk_maximum3_f16 v122, v62, v78, v101
	v_pk_maximum3_f16 v123, v63, v79, v100
	v_pk_maximum3_f16 v124, v64, v80, v99
	v_pk_maximum3_f16 v129, v102, v106, v118
	v_pk_fma_f16 v103, v36, v160, v56
	v_pk_maximum3_f16 v137, v57, v85, v97
	v_pk_fma_f16 v104, v35, v159, v55
	v_pk_maximum3_f16 v125, v125, v129, v137
	v_pk_fma_f16 v105, v34, v158, v54
	v_pk_fma_f16 v107, v48, v160, v84
	v_pk_fma_f16 v108, v47, v159, v83
	v_pk_fma_f16 v109, v46, v158, v82
	v_pk_fma_f16 v119, v68, v160, v96
	v_pk_fma_f16 v120, v67, v159, v95
	v_pk_fma_f16 v121, v66, v158, v94
	v_pk_fma_f16 v56, v88, v160, v56
	v_pk_fma_f16 v55, v87, v159, v55
	v_pk_fma_f16 v54, v86, v158, v54
	v_pk_fma_f16 v84, v116, v160, v84
	v_pk_fma_f16 v83, v115, v159, v83
	v_pk_fma_f16 v82, v114, v158, v82
	v_pk_fma_f16 v96, v132, v160, v96
	v_pk_fma_f16 v95, v131, v159, v95
	v_pk_fma_f16 v94, v130, v158, v94
	v_pk_maximum3_f16 v126, v105, v109, v121
	v_pk_maximum3_f16 v127, v104, v108, v120
	v_pk_maximum3_f16 v128, v103, v107, v119
	v_pk_maximum3_f16 v135, v55, v83, v95
	v_pk_maximum3_f16 v136, v56, v84, v96
	v_pk_maximum3_f16 v134, v54, v82, v94
	v_pk_maximum3_f16 v122, v122, v126, v134
	v_pk_maximum3_f16 v123, v123, v127, v135
	v_pk_maximum3_f16 v124, v124, v128, v136
	v_pk_add_f16 v65, v65, v125 neg_lo:[0,1] neg_hi:[0,1]
	v_pk_add_f16 v62, v62, v122 neg_lo:[0,1] neg_hi:[0,1]
	v_pk_add_f16 v63, v63, v123 neg_lo:[0,1] neg_hi:[0,1]
	v_pk_add_f16 v64, v64, v124 neg_lo:[0,1] neg_hi:[0,1]
	v_pk_add_f16 v78, v78, v122 neg_lo:[0,1] neg_hi:[0,1]
	v_exp_f16_sdwa v126, v62 dst_sel:WORD_0 dst_unused:UNUSED_PAD src0_sel:WORD_0
	v_exp_f16_sdwa v127, v63 dst_sel:WORD_0 dst_unused:UNUSED_PAD src0_sel:WORD_0
	v_exp_f16_sdwa v128, v64 dst_sel:WORD_0 dst_unused:UNUSED_PAD src0_sel:WORD_0
	v_exp_f16_sdwa v129, v65 dst_sel:WORD_0 dst_unused:UNUSED_PAD src0_sel:WORD_0
	v_exp_f16_sdwa v126, v62 dst_sel:WORD_1 dst_unused:UNUSED_PRESERVE src0_sel:WORD_1
	v_exp_f16_sdwa v127, v63 dst_sel:WORD_1 dst_unused:UNUSED_PRESERVE src0_sel:WORD_1
	v_exp_f16_sdwa v128, v64 dst_sel:WORD_1 dst_unused:UNUSED_PRESERVE src0_sel:WORD_1
	v_exp_f16_sdwa v129, v65 dst_sel:WORD_1 dst_unused:UNUSED_PRESERVE src0_sel:WORD_1
	v_pk_add_f16 v79, v79, v123 neg_lo:[0,1] neg_hi:[0,1]
	v_pk_add_f16 v65, v126, 0
	v_pk_fma_f16 v33, v33, v129, 0
	v_pk_add_f16 v62, v129, 0
	v_pk_add_f16 v63, v128, 0
	v_pk_add_f16 v64, v127, 0
	v_pk_fma_f16 v32, v32, v128, 0
	v_pk_fma_f16 v31, v31, v127, 0
	v_pk_fma_f16 v30, v30, v126, 0
	v_pk_add_f16 v80, v80, v124 neg_lo:[0,1] neg_hi:[0,1]
	v_pk_add_f16 v81, v81, v125 neg_lo:[0,1] neg_hi:[0,1]
	v_pk_add_f16 v54, v54, v122 neg_lo:[0,1] neg_hi:[0,1]
	v_exp_f16_sdwa v126, v78 dst_sel:WORD_0 dst_unused:UNUSED_PAD src0_sel:WORD_0
	v_exp_f16_sdwa v127, v79 dst_sel:WORD_0 dst_unused:UNUSED_PAD src0_sel:WORD_0
	v_exp_f16_sdwa v128, v80 dst_sel:WORD_0 dst_unused:UNUSED_PAD src0_sel:WORD_0
	v_exp_f16_sdwa v129, v81 dst_sel:WORD_0 dst_unused:UNUSED_PAD src0_sel:WORD_0
	v_exp_f16_sdwa v126, v78 dst_sel:WORD_1 dst_unused:UNUSED_PRESERVE src0_sel:WORD_1
	v_exp_f16_sdwa v127, v79 dst_sel:WORD_1 dst_unused:UNUSED_PRESERVE src0_sel:WORD_1
	v_exp_f16_sdwa v128, v80 dst_sel:WORD_1 dst_unused:UNUSED_PRESERVE src0_sel:WORD_1
	v_exp_f16_sdwa v129, v81 dst_sel:WORD_1 dst_unused:UNUSED_PRESERVE src0_sel:WORD_1
	v_pk_add_f16 v55, v55, v123 neg_lo:[0,1] neg_hi:[0,1]
	v_pk_add_f16 v65, v65, v126
	v_pk_fma_f16 v33, v45, v129, v33
	v_pk_add_f16 v45, v98, v125 neg_lo:[0,1] neg_hi:[0,1]
	v_pk_add_f16 v64, v64, v127
	v_pk_add_f16 v63, v63, v128
	v_pk_add_f16 v62, v62, v129
	v_pk_fma_f16 v30, v42, v126, v30
	v_pk_fma_f16 v31, v43, v127, v31
	v_pk_fma_f16 v32, v44, v128, v32
	v_pk_add_f16 v42, v101, v122 neg_lo:[0,1] neg_hi:[0,1]
	v_pk_add_f16 v43, v100, v123 neg_lo:[0,1] neg_hi:[0,1]
	v_pk_add_f16 v44, v99, v124 neg_lo:[0,1] neg_hi:[0,1]
	v_pk_add_f16 v56, v56, v124 neg_lo:[0,1] neg_hi:[0,1]
	v_exp_f16_sdwa v78, v42 dst_sel:WORD_0 dst_unused:UNUSED_PAD src0_sel:WORD_0
	v_exp_f16_sdwa v79, v43 dst_sel:WORD_0 dst_unused:UNUSED_PAD src0_sel:WORD_0
	v_exp_f16_sdwa v80, v44 dst_sel:WORD_0 dst_unused:UNUSED_PAD src0_sel:WORD_0
	v_exp_f16_sdwa v81, v45 dst_sel:WORD_0 dst_unused:UNUSED_PAD src0_sel:WORD_0
	v_exp_f16_sdwa v78, v42 dst_sel:WORD_1 dst_unused:UNUSED_PRESERVE src0_sel:WORD_1
	v_exp_f16_sdwa v79, v43 dst_sel:WORD_1 dst_unused:UNUSED_PRESERVE src0_sel:WORD_1
	v_exp_f16_sdwa v80, v44 dst_sel:WORD_1 dst_unused:UNUSED_PRESERVE src0_sel:WORD_1
	v_exp_f16_sdwa v81, v45 dst_sel:WORD_1 dst_unused:UNUSED_PRESERVE src0_sel:WORD_1
	v_pk_add_f16 v57, v57, v125 neg_lo:[0,1] neg_hi:[0,1]
	v_pk_add_f16 v45, v65, v78
	v_pk_add_f16 v42, v62, v81
	v_pk_add_f16 v43, v63, v80
	v_pk_add_f16 v44, v64, v79
	v_pk_fma_f16 v33, v61, v81, v33
	v_pk_fma_f16 v32, v60, v80, v32
	v_pk_fma_f16 v31, v59, v79, v31
	v_pk_fma_f16 v30, v58, v78, v30
	v_pk_add_f16 v58, v105, v122 neg_lo:[0,1] neg_hi:[0,1]
	v_pk_add_f16 v59, v104, v123 neg_lo:[0,1] neg_hi:[0,1]
	v_pk_add_f16 v60, v103, v124 neg_lo:[0,1] neg_hi:[0,1]
	v_pk_add_f16 v61, v102, v125 neg_lo:[0,1] neg_hi:[0,1]
	v_exp_f16_sdwa v62, v58 dst_sel:WORD_0 dst_unused:UNUSED_PAD src0_sel:WORD_0
	v_exp_f16_sdwa v63, v59 dst_sel:WORD_0 dst_unused:UNUSED_PAD src0_sel:WORD_0
	v_exp_f16_sdwa v64, v60 dst_sel:WORD_0 dst_unused:UNUSED_PAD src0_sel:WORD_0
	v_exp_f16_sdwa v65, v61 dst_sel:WORD_0 dst_unused:UNUSED_PAD src0_sel:WORD_0
	v_exp_f16_sdwa v62, v58 dst_sel:WORD_1 dst_unused:UNUSED_PRESERVE src0_sel:WORD_1
	v_exp_f16_sdwa v63, v59 dst_sel:WORD_1 dst_unused:UNUSED_PRESERVE src0_sel:WORD_1
	v_exp_f16_sdwa v64, v60 dst_sel:WORD_1 dst_unused:UNUSED_PRESERVE src0_sel:WORD_1
	v_exp_f16_sdwa v65, v61 dst_sel:WORD_1 dst_unused:UNUSED_PRESERVE src0_sel:WORD_1
	v_pk_add_f16 v58, v109, v122 neg_lo:[0,1] neg_hi:[0,1]
	v_pk_add_f16 v45, v45, v62
	v_pk_add_f16 v44, v44, v63
	v_pk_add_f16 v43, v43, v64
	v_pk_add_f16 v42, v42, v65
	v_pk_fma_f16 v30, v18, v62, v30
	v_pk_fma_f16 v31, v19, v63, v31
	v_pk_fma_f16 v32, v20, v64, v32
	v_pk_fma_f16 v33, v21, v65, v33
	v_pk_add_f16 v59, v108, v123 neg_lo:[0,1] neg_hi:[0,1]
	v_pk_add_f16 v60, v107, v124 neg_lo:[0,1] neg_hi:[0,1]
	v_pk_add_f16 v61, v106, v125 neg_lo:[0,1] neg_hi:[0,1]
	v_exp_f16_sdwa v62, v58 dst_sel:WORD_0 dst_unused:UNUSED_PAD src0_sel:WORD_0
	v_exp_f16_sdwa v63, v59 dst_sel:WORD_0 dst_unused:UNUSED_PAD src0_sel:WORD_0
	v_exp_f16_sdwa v64, v60 dst_sel:WORD_0 dst_unused:UNUSED_PAD src0_sel:WORD_0
	v_exp_f16_sdwa v65, v61 dst_sel:WORD_0 dst_unused:UNUSED_PAD src0_sel:WORD_0
	v_exp_f16_sdwa v62, v58 dst_sel:WORD_1 dst_unused:UNUSED_PRESERVE src0_sel:WORD_1
	v_exp_f16_sdwa v63, v59 dst_sel:WORD_1 dst_unused:UNUSED_PRESERVE src0_sel:WORD_1
	v_exp_f16_sdwa v64, v60 dst_sel:WORD_1 dst_unused:UNUSED_PRESERVE src0_sel:WORD_1
	v_exp_f16_sdwa v65, v61 dst_sel:WORD_1 dst_unused:UNUSED_PRESERVE src0_sel:WORD_1
	v_pk_add_f16 v58, v121, v122 neg_lo:[0,1] neg_hi:[0,1]
	v_pk_add_f16 v45, v45, v62
	v_pk_add_f16 v42, v42, v65
	v_pk_add_f16 v43, v43, v64
	v_pk_add_f16 v44, v44, v63
	v_pk_fma_f16 v33, v25, v65, v33
	v_pk_fma_f16 v32, v24, v64, v32
	v_pk_fma_f16 v31, v23, v63, v31
	v_pk_fma_f16 v30, v22, v62, v30
	v_pk_add_f16 v59, v120, v123 neg_lo:[0,1] neg_hi:[0,1]
	v_pk_add_f16 v60, v119, v124 neg_lo:[0,1] neg_hi:[0,1]
	v_pk_add_f16 v61, v118, v125 neg_lo:[0,1] neg_hi:[0,1]
	v_exp_f16_sdwa v62, v58 dst_sel:WORD_0 dst_unused:UNUSED_PAD src0_sel:WORD_0
	v_exp_f16_sdwa v63, v59 dst_sel:WORD_0 dst_unused:UNUSED_PAD src0_sel:WORD_0
	v_exp_f16_sdwa v64, v60 dst_sel:WORD_0 dst_unused:UNUSED_PAD src0_sel:WORD_0
	v_exp_f16_sdwa v65, v61 dst_sel:WORD_0 dst_unused:UNUSED_PAD src0_sel:WORD_0
	v_exp_f16_sdwa v62, v58 dst_sel:WORD_1 dst_unused:UNUSED_PRESERVE src0_sel:WORD_1
	v_exp_f16_sdwa v63, v59 dst_sel:WORD_1 dst_unused:UNUSED_PRESERVE src0_sel:WORD_1
	v_exp_f16_sdwa v64, v60 dst_sel:WORD_1 dst_unused:UNUSED_PRESERVE src0_sel:WORD_1
	v_exp_f16_sdwa v65, v61 dst_sel:WORD_1 dst_unused:UNUSED_PRESERVE src0_sel:WORD_1
	v_exp_f16_sdwa v58, v54 dst_sel:WORD_0 dst_unused:UNUSED_PAD src0_sel:WORD_0
	v_exp_f16_sdwa v59, v55 dst_sel:WORD_0 dst_unused:UNUSED_PAD src0_sel:WORD_0
	v_exp_f16_sdwa v60, v56 dst_sel:WORD_0 dst_unused:UNUSED_PAD src0_sel:WORD_0
	v_exp_f16_sdwa v61, v57 dst_sel:WORD_0 dst_unused:UNUSED_PAD src0_sel:WORD_0
	v_exp_f16_sdwa v58, v54 dst_sel:WORD_1 dst_unused:UNUSED_PRESERVE src0_sel:WORD_1
	v_exp_f16_sdwa v59, v55 dst_sel:WORD_1 dst_unused:UNUSED_PRESERVE src0_sel:WORD_1
	v_exp_f16_sdwa v60, v56 dst_sel:WORD_1 dst_unused:UNUSED_PRESERVE src0_sel:WORD_1
	v_exp_f16_sdwa v61, v57 dst_sel:WORD_1 dst_unused:UNUSED_PRESERVE src0_sel:WORD_1
	v_pk_add_f16 v54, v82, v122 neg_lo:[0,1] neg_hi:[0,1]
	v_pk_add_f16 v45, v45, v62
	v_pk_add_f16 v44, v44, v63
	v_pk_add_f16 v43, v43, v64
	v_pk_add_f16 v42, v42, v65
	v_pk_fma_f16 v30, v26, v62, v30
	v_pk_fma_f16 v31, v27, v63, v31
	v_pk_fma_f16 v32, v28, v64, v32
	v_pk_fma_f16 v33, v29, v65, v33
	v_pk_add_f16 v45, v45, v58
	v_pk_add_f16 v42, v42, v61
	v_pk_add_f16 v43, v43, v60
	v_pk_add_f16 v44, v44, v59
	v_pk_fma_f16 v33, v41, v61, v33
	v_pk_fma_f16 v32, v40, v60, v32
	v_pk_fma_f16 v31, v39, v59, v31
	v_pk_fma_f16 v30, v38, v58, v30
	v_pk_add_f16 v55, v83, v123 neg_lo:[0,1] neg_hi:[0,1]
	v_pk_add_f16 v56, v84, v124 neg_lo:[0,1] neg_hi:[0,1]
	v_pk_add_f16 v57, v85, v125 neg_lo:[0,1] neg_hi:[0,1]
	v_exp_f16_sdwa v58, v54 dst_sel:WORD_0 dst_unused:UNUSED_PAD src0_sel:WORD_0
	v_exp_f16_sdwa v59, v55 dst_sel:WORD_0 dst_unused:UNUSED_PAD src0_sel:WORD_0
	v_exp_f16_sdwa v60, v56 dst_sel:WORD_0 dst_unused:UNUSED_PAD src0_sel:WORD_0
	v_exp_f16_sdwa v61, v57 dst_sel:WORD_0 dst_unused:UNUSED_PAD src0_sel:WORD_0
	v_exp_f16_sdwa v58, v54 dst_sel:WORD_1 dst_unused:UNUSED_PRESERVE src0_sel:WORD_1
	v_exp_f16_sdwa v59, v55 dst_sel:WORD_1 dst_unused:UNUSED_PRESERVE src0_sel:WORD_1
	v_exp_f16_sdwa v60, v56 dst_sel:WORD_1 dst_unused:UNUSED_PRESERVE src0_sel:WORD_1
	v_exp_f16_sdwa v61, v57 dst_sel:WORD_1 dst_unused:UNUSED_PRESERVE src0_sel:WORD_1
	v_pk_add_f16 v54, v94, v122 neg_lo:[0,1] neg_hi:[0,1]
	v_pk_add_f16 v45, v45, v58
	v_pk_add_f16 v44, v44, v59
	v_pk_add_f16 v43, v43, v60
	v_pk_add_f16 v42, v42, v61
	v_pk_fma_f16 v30, v50, v58, v30
	v_pk_fma_f16 v31, v51, v59, v31
	v_pk_fma_f16 v32, v52, v60, v32
	v_pk_fma_f16 v33, v53, v61, v33
	v_pk_add_f16 v55, v95, v123 neg_lo:[0,1] neg_hi:[0,1]
	v_pk_add_f16 v56, v96, v124 neg_lo:[0,1] neg_hi:[0,1]
	v_pk_add_f16 v57, v97, v125 neg_lo:[0,1] neg_hi:[0,1]
	v_exp_f16_sdwa v58, v54 dst_sel:WORD_0 dst_unused:UNUSED_PAD src0_sel:WORD_0
	v_exp_f16_sdwa v59, v55 dst_sel:WORD_0 dst_unused:UNUSED_PAD src0_sel:WORD_0
	v_exp_f16_sdwa v60, v56 dst_sel:WORD_0 dst_unused:UNUSED_PAD src0_sel:WORD_0
	v_exp_f16_sdwa v61, v57 dst_sel:WORD_0 dst_unused:UNUSED_PAD src0_sel:WORD_0
	v_exp_f16_sdwa v58, v54 dst_sel:WORD_1 dst_unused:UNUSED_PRESERVE src0_sel:WORD_1
	v_exp_f16_sdwa v59, v55 dst_sel:WORD_1 dst_unused:UNUSED_PRESERVE src0_sel:WORD_1
	v_exp_f16_sdwa v60, v56 dst_sel:WORD_1 dst_unused:UNUSED_PRESERVE src0_sel:WORD_1
	v_exp_f16_sdwa v61, v57 dst_sel:WORD_1 dst_unused:UNUSED_PRESERVE src0_sel:WORD_1
	v_pk_add_f16 v45, v45, v58
	v_pk_add_f16 v44, v44, v59
	v_rcp_f16_e32 v54, v45
	v_rcp_f16_sdwa v45, v45 dst_sel:DWORD dst_unused:UNUSED_PAD src0_sel:WORD_1
	v_pk_add_f16 v43, v43, v60
	v_rcp_f16_e32 v55, v44
	v_rcp_f16_sdwa v44, v44 dst_sel:DWORD dst_unused:UNUSED_PAD src0_sel:WORD_1
	v_pk_add_f16 v42, v42, v61
	v_pk_fma_f16 v30, v70, v58, v30
	v_rcp_f16_e32 v58, v43
	v_rcp_f16_sdwa v43, v43 dst_sel:DWORD dst_unused:UNUSED_PAD src0_sel:WORD_1
	v_pk_fma_f16 v31, v71, v59, v31
	v_rcp_f16_e32 v59, v42
	v_rcp_f16_sdwa v42, v42 dst_sel:DWORD dst_unused:UNUSED_PAD src0_sel:WORD_1
	v_pack_b32_f16 v45, v54, v45
	v_pk_mul_f16 v57, v30, v45
	v_pack_b32_f16 v30, v55, v44
	v_pk_fma_f16 v32, v72, v60, v32
	v_pk_mul_f16 v56, v31, v30
	v_pack_b32_f16 v30, v58, v43
	v_pk_fma_f16 v33, v73, v61, v33
	v_pk_mul_f16 v55, v32, v30
	v_pack_b32_f16 v30, v59, v42
	v_pk_mul_f16 v54, v33, v30
	s_waitcnt vmcnt(0)
	v_pk_mul_f16 v30, v204, v154 op_sel_hi:[0,1]
	v_pk_mul_f16 v31, v204, v155 op_sel_hi:[0,1]
	v_pk_mul_f16 v32, v204, v156 op_sel_hi:[0,1]
	v_pk_mul_f16 v33, v204, v157 op_sel_hi:[0,1]
	v_pk_mul_f16 v42, v202, v154 op_sel_hi:[0,1]
	v_pk_mul_f16 v43, v202, v155 op_sel_hi:[0,1]
	v_pk_mul_f16 v44, v202, v156 op_sel_hi:[0,1]
	v_pk_mul_f16 v45, v202, v157 op_sel_hi:[0,1]
	v_pk_mul_f16 v58, v203, v154 op_sel_hi:[0,1]
	v_pk_mul_f16 v59, v203, v155 op_sel_hi:[0,1]
	v_pk_mul_f16 v60, v203, v156 op_sel_hi:[0,1]
	v_pk_mul_f16 v61, v203, v157 op_sel_hi:[0,1]
	v_pk_fma_f16 v37, v37, v157, v33
	v_pk_fma_f16 v36, v36, v156, v32
	v_pk_fma_f16 v35, v35, v155, v31
	v_pk_fma_f16 v34, v34, v154, v30
	v_pk_fma_f16 v49, v49, v157, v45
	v_pk_fma_f16 v48, v48, v156, v44
	v_pk_fma_f16 v47, v47, v155, v43
	v_pk_fma_f16 v46, v46, v154, v42
	v_pk_fma_f16 v62, v69, v157, v61
	v_pk_fma_f16 v63, v68, v156, v60
	v_pk_fma_f16 v64, v67, v155, v59
	v_pk_fma_f16 v65, v66, v154, v58
	v_pk_fma_f16 v66, v89, v157, v33
	v_pk_fma_f16 v67, v88, v156, v32
	v_pk_fma_f16 v68, v87, v155, v31
	v_pk_fma_f16 v69, v86, v154, v30
	v_pk_fma_f16 v78, v117, v157, v45
	v_pk_fma_f16 v79, v116, v156, v44
	v_pk_fma_f16 v80, v115, v155, v43
	v_pk_fma_f16 v81, v114, v154, v42
	v_pk_fma_f16 v82, v133, v157, v61
	v_pk_fma_f16 v83, v132, v156, v60
	v_pk_fma_f16 v84, v131, v155, v59
	v_pk_fma_f16 v85, v130, v154, v58
	v_pk_fma_f16 v61, v17, v157, v61
	v_pk_fma_f16 v60, v16, v156, v60
	v_pk_fma_f16 v59, v15, v155, v59
	v_pk_fma_f16 v58, v14, v154, v58
	v_pk_maximum3_f16 v14, v34, v46, v65
	v_pk_maximum3_f16 v15, v35, v47, v64
	v_pk_maximum3_f16 v16, v36, v48, v63
	v_pk_maximum3_f16 v17, v37, v49, v62
	v_pk_maximum3_f16 v86, v69, v81, v85
	v_pk_maximum3_f16 v87, v68, v80, v84
	v_pk_maximum3_f16 v88, v67, v79, v83
	v_pk_maximum3_f16 v89, v66, v78, v82
	v_pk_fma_f16 v33, v145, v157, v33
	v_pk_fma_f16 v32, v144, v156, v32
	v_pk_fma_f16 v31, v143, v155, v31
	v_pk_fma_f16 v30, v142, v154, v30
	v_pk_fma_f16 v45, v153, v157, v45
	v_pk_fma_f16 v44, v152, v156, v44
	v_pk_fma_f16 v43, v151, v155, v43
	v_pk_fma_f16 v42, v150, v154, v42
	v_pk_maximum3_f16 v95, v31, v43, v59
	v_pk_maximum3_f16 v96, v32, v44, v60
	v_pk_maximum3_f16 v97, v33, v45, v61
	v_pk_maximum3_f16 v94, v30, v42, v58
	v_pk_maximum3_f16 v15, v15, v87, v95
	v_pk_maximum3_f16 v16, v16, v88, v96
	v_pk_maximum3_f16 v17, v17, v89, v97
	v_pk_maximum3_f16 v14, v14, v86, v94
	v_xor_b32_e32 v86, 0x80008000, v17
	v_xor_b32_e32 v87, 0x80008000, v16
	v_xor_b32_e32 v88, 0x80008000, v15
	v_xor_b32_e32 v89, 0x80008000, v14
	v_pk_add_f16 v14, v34, v89
	v_pk_add_f16 v15, v35, v88
	v_pk_add_f16 v16, v36, v87
	v_pk_add_f16 v17, v37, v86
	v_exp_f16_sdwa v34, v14 dst_sel:WORD_0 dst_unused:UNUSED_PAD src0_sel:WORD_0
	v_exp_f16_sdwa v35, v15 dst_sel:WORD_0 dst_unused:UNUSED_PAD src0_sel:WORD_0
	v_exp_f16_sdwa v36, v16 dst_sel:WORD_0 dst_unused:UNUSED_PAD src0_sel:WORD_0
	v_exp_f16_sdwa v37, v17 dst_sel:WORD_0 dst_unused:UNUSED_PAD src0_sel:WORD_0
	v_exp_f16_sdwa v34, v14 dst_sel:WORD_1 dst_unused:UNUSED_PRESERVE src0_sel:WORD_1
	v_exp_f16_sdwa v35, v15 dst_sel:WORD_1 dst_unused:UNUSED_PRESERVE src0_sel:WORD_1
	v_exp_f16_sdwa v36, v16 dst_sel:WORD_1 dst_unused:UNUSED_PRESERVE src0_sel:WORD_1
	v_exp_f16_sdwa v37, v17 dst_sel:WORD_1 dst_unused:UNUSED_PRESERVE src0_sel:WORD_1
	v_pk_add_f16 v14, v34, 0
	v_pk_add_f16 v15, v35, 0
	v_pk_add_f16 v16, v36, 0
	v_pk_add_f16 v17, v37, 0
	v_pk_fma_f16 v18, v18, v34, 0
	v_pk_fma_f16 v19, v19, v35, 0
	v_pk_fma_f16 v20, v20, v36, 0
	v_pk_fma_f16 v21, v21, v37, 0
	v_pk_add_f16 v34, v46, v89
	v_pk_add_f16 v35, v47, v88
	v_pk_add_f16 v36, v48, v87
	v_pk_add_f16 v37, v49, v86
	v_exp_f16_sdwa v46, v34 dst_sel:WORD_0 dst_unused:UNUSED_PAD src0_sel:WORD_0
	v_exp_f16_sdwa v47, v35 dst_sel:WORD_0 dst_unused:UNUSED_PAD src0_sel:WORD_0
	v_exp_f16_sdwa v48, v36 dst_sel:WORD_0 dst_unused:UNUSED_PAD src0_sel:WORD_0
	v_exp_f16_sdwa v49, v37 dst_sel:WORD_0 dst_unused:UNUSED_PAD src0_sel:WORD_0
	v_exp_f16_sdwa v46, v34 dst_sel:WORD_1 dst_unused:UNUSED_PRESERVE src0_sel:WORD_1
	v_exp_f16_sdwa v47, v35 dst_sel:WORD_1 dst_unused:UNUSED_PRESERVE src0_sel:WORD_1
	v_exp_f16_sdwa v48, v36 dst_sel:WORD_1 dst_unused:UNUSED_PRESERVE src0_sel:WORD_1
	v_exp_f16_sdwa v49, v37 dst_sel:WORD_1 dst_unused:UNUSED_PRESERVE src0_sel:WORD_1
	s_nop 0
	v_pk_add_f16 v17, v17, v49
	v_pk_add_f16 v16, v16, v48
	v_pk_add_f16 v15, v15, v47
	v_pk_add_f16 v14, v14, v46
	v_pk_fma_f16 v21, v25, v49, v21
	v_pk_fma_f16 v20, v24, v48, v20
	v_pk_fma_f16 v19, v23, v47, v19
	v_pk_fma_f16 v18, v22, v46, v18
	v_pk_add_f16 v22, v65, v89
	v_pk_add_f16 v23, v64, v88
	v_pk_add_f16 v24, v63, v87
	v_pk_add_f16 v25, v62, v86
	v_exp_f16_sdwa v34, v22 dst_sel:WORD_0 dst_unused:UNUSED_PAD src0_sel:WORD_0
	v_exp_f16_sdwa v35, v23 dst_sel:WORD_0 dst_unused:UNUSED_PAD src0_sel:WORD_0
	v_exp_f16_sdwa v36, v24 dst_sel:WORD_0 dst_unused:UNUSED_PAD src0_sel:WORD_0
	v_exp_f16_sdwa v37, v25 dst_sel:WORD_0 dst_unused:UNUSED_PAD src0_sel:WORD_0
	v_exp_f16_sdwa v34, v22 dst_sel:WORD_1 dst_unused:UNUSED_PRESERVE src0_sel:WORD_1
	v_exp_f16_sdwa v35, v23 dst_sel:WORD_1 dst_unused:UNUSED_PRESERVE src0_sel:WORD_1
	v_exp_f16_sdwa v36, v24 dst_sel:WORD_1 dst_unused:UNUSED_PRESERVE src0_sel:WORD_1
	v_exp_f16_sdwa v37, v25 dst_sel:WORD_1 dst_unused:UNUSED_PRESERVE src0_sel:WORD_1
	v_pk_add_f16 v22, v69, v89
	v_pk_add_f16 v14, v14, v34
	v_pk_add_f16 v15, v15, v35
	v_pk_add_f16 v16, v16, v36
	v_pk_add_f16 v17, v17, v37
	v_pk_fma_f16 v18, v26, v34, v18
	v_pk_fma_f16 v19, v27, v35, v19
	v_pk_fma_f16 v20, v28, v36, v20
	v_pk_fma_f16 v21, v29, v37, v21
	v_pk_add_f16 v23, v68, v88
	v_pk_add_f16 v24, v67, v87
	v_pk_add_f16 v25, v66, v86
	v_exp_f16_sdwa v26, v22 dst_sel:WORD_0 dst_unused:UNUSED_PAD src0_sel:WORD_0
	v_exp_f16_sdwa v27, v23 dst_sel:WORD_0 dst_unused:UNUSED_PAD src0_sel:WORD_0
	v_exp_f16_sdwa v28, v24 dst_sel:WORD_0 dst_unused:UNUSED_PAD src0_sel:WORD_0
	v_exp_f16_sdwa v29, v25 dst_sel:WORD_0 dst_unused:UNUSED_PAD src0_sel:WORD_0
	v_exp_f16_sdwa v26, v22 dst_sel:WORD_1 dst_unused:UNUSED_PRESERVE src0_sel:WORD_1
	v_exp_f16_sdwa v27, v23 dst_sel:WORD_1 dst_unused:UNUSED_PRESERVE src0_sel:WORD_1
	v_exp_f16_sdwa v28, v24 dst_sel:WORD_1 dst_unused:UNUSED_PRESERVE src0_sel:WORD_1
	v_exp_f16_sdwa v29, v25 dst_sel:WORD_1 dst_unused:UNUSED_PRESERVE src0_sel:WORD_1
	v_pk_add_f16 v22, v81, v89
	v_pk_add_f16 v17, v17, v29
	v_pk_add_f16 v16, v16, v28
	v_pk_add_f16 v15, v15, v27
	v_pk_add_f16 v14, v14, v26
	v_pk_fma_f16 v21, v41, v29, v21
	v_pk_fma_f16 v20, v40, v28, v20
	v_pk_fma_f16 v19, v39, v27, v19
	v_pk_fma_f16 v18, v38, v26, v18
	v_pk_add_f16 v23, v80, v88
	v_pk_add_f16 v24, v79, v87
	v_pk_add_f16 v25, v78, v86
	v_exp_f16_sdwa v26, v22 dst_sel:WORD_0 dst_unused:UNUSED_PAD src0_sel:WORD_0
	v_exp_f16_sdwa v27, v23 dst_sel:WORD_0 dst_unused:UNUSED_PAD src0_sel:WORD_0
	v_exp_f16_sdwa v28, v24 dst_sel:WORD_0 dst_unused:UNUSED_PAD src0_sel:WORD_0
	v_exp_f16_sdwa v29, v25 dst_sel:WORD_0 dst_unused:UNUSED_PAD src0_sel:WORD_0
	v_exp_f16_sdwa v26, v22 dst_sel:WORD_1 dst_unused:UNUSED_PRESERVE src0_sel:WORD_1
	v_exp_f16_sdwa v27, v23 dst_sel:WORD_1 dst_unused:UNUSED_PRESERVE src0_sel:WORD_1
	v_exp_f16_sdwa v28, v24 dst_sel:WORD_1 dst_unused:UNUSED_PRESERVE src0_sel:WORD_1
	v_exp_f16_sdwa v29, v25 dst_sel:WORD_1 dst_unused:UNUSED_PRESERVE src0_sel:WORD_1
	v_pk_add_f16 v22, v85, v89
	v_pk_add_f16 v14, v14, v26
	v_pk_add_f16 v15, v15, v27
	v_pk_add_f16 v16, v16, v28
	v_pk_add_f16 v17, v17, v29
	v_pk_fma_f16 v18, v50, v26, v18
	v_pk_fma_f16 v19, v51, v27, v19
	v_pk_fma_f16 v20, v52, v28, v20
	v_pk_fma_f16 v21, v53, v29, v21
	v_pk_add_f16 v23, v84, v88
	v_pk_add_f16 v24, v83, v87
	v_pk_add_f16 v25, v82, v86
	v_exp_f16_sdwa v26, v22 dst_sel:WORD_0 dst_unused:UNUSED_PAD src0_sel:WORD_0
	v_exp_f16_sdwa v27, v23 dst_sel:WORD_0 dst_unused:UNUSED_PAD src0_sel:WORD_0
	v_exp_f16_sdwa v28, v24 dst_sel:WORD_0 dst_unused:UNUSED_PAD src0_sel:WORD_0
	v_exp_f16_sdwa v29, v25 dst_sel:WORD_0 dst_unused:UNUSED_PAD src0_sel:WORD_0
	v_exp_f16_sdwa v26, v22 dst_sel:WORD_1 dst_unused:UNUSED_PRESERVE src0_sel:WORD_1
	v_exp_f16_sdwa v27, v23 dst_sel:WORD_1 dst_unused:UNUSED_PRESERVE src0_sel:WORD_1
	v_exp_f16_sdwa v28, v24 dst_sel:WORD_1 dst_unused:UNUSED_PRESERVE src0_sel:WORD_1
	v_exp_f16_sdwa v29, v25 dst_sel:WORD_1 dst_unused:UNUSED_PRESERVE src0_sel:WORD_1
	v_pk_add_f16 v22, v30, v89
	v_pk_add_f16 v17, v17, v29
	v_pk_add_f16 v16, v16, v28
	v_pk_add_f16 v15, v15, v27
	v_pk_add_f16 v14, v14, v26
	v_pk_fma_f16 v21, v73, v29, v21
	v_pk_fma_f16 v20, v72, v28, v20
	v_pk_fma_f16 v19, v71, v27, v19
	v_pk_fma_f16 v18, v70, v26, v18
	v_pk_add_f16 v23, v31, v88
	v_pk_add_f16 v24, v32, v87
	v_pk_add_f16 v25, v33, v86
	v_exp_f16_sdwa v26, v22 dst_sel:WORD_0 dst_unused:UNUSED_PAD src0_sel:WORD_0
	v_exp_f16_sdwa v27, v23 dst_sel:WORD_0 dst_unused:UNUSED_PAD src0_sel:WORD_0
	v_exp_f16_sdwa v28, v24 dst_sel:WORD_0 dst_unused:UNUSED_PAD src0_sel:WORD_0
	v_exp_f16_sdwa v29, v25 dst_sel:WORD_0 dst_unused:UNUSED_PAD src0_sel:WORD_0
	v_exp_f16_sdwa v26, v22 dst_sel:WORD_1 dst_unused:UNUSED_PRESERVE src0_sel:WORD_1
	v_exp_f16_sdwa v27, v23 dst_sel:WORD_1 dst_unused:UNUSED_PRESERVE src0_sel:WORD_1
	v_exp_f16_sdwa v28, v24 dst_sel:WORD_1 dst_unused:UNUSED_PRESERVE src0_sel:WORD_1
	v_exp_f16_sdwa v29, v25 dst_sel:WORD_1 dst_unused:UNUSED_PRESERVE src0_sel:WORD_1
	v_pk_add_f16 v22, v42, v89
	v_pk_add_f16 v14, v14, v26
	v_pk_add_f16 v15, v15, v27
	v_pk_add_f16 v16, v16, v28
	v_pk_add_f16 v17, v17, v29
	v_pk_fma_f16 v18, v90, v26, v18
	v_pk_fma_f16 v19, v91, v27, v19
	v_pk_fma_f16 v20, v92, v28, v20
	v_pk_fma_f16 v21, v93, v29, v21
	v_pk_add_f16 v23, v43, v88
	v_pk_add_f16 v24, v44, v87
	v_pk_add_f16 v25, v45, v86
	v_exp_f16_sdwa v26, v22 dst_sel:WORD_0 dst_unused:UNUSED_PAD src0_sel:WORD_0
	v_exp_f16_sdwa v27, v23 dst_sel:WORD_0 dst_unused:UNUSED_PAD src0_sel:WORD_0
	v_exp_f16_sdwa v28, v24 dst_sel:WORD_0 dst_unused:UNUSED_PAD src0_sel:WORD_0
	v_exp_f16_sdwa v29, v25 dst_sel:WORD_0 dst_unused:UNUSED_PAD src0_sel:WORD_0
	v_exp_f16_sdwa v26, v22 dst_sel:WORD_1 dst_unused:UNUSED_PRESERVE src0_sel:WORD_1
	v_exp_f16_sdwa v27, v23 dst_sel:WORD_1 dst_unused:UNUSED_PRESERVE src0_sel:WORD_1
	v_exp_f16_sdwa v28, v24 dst_sel:WORD_1 dst_unused:UNUSED_PRESERVE src0_sel:WORD_1
	v_exp_f16_sdwa v29, v25 dst_sel:WORD_1 dst_unused:UNUSED_PRESERVE src0_sel:WORD_1
	v_pk_add_f16 v22, v58, v89
	v_pk_add_f16 v17, v17, v29
	v_pk_add_f16 v16, v16, v28
	v_pk_add_f16 v15, v15, v27
	v_pk_add_f16 v14, v14, v26
	v_pk_fma_f16 v21, v113, v29, v21
	v_pk_fma_f16 v20, v112, v28, v20
	v_pk_fma_f16 v19, v111, v27, v19
	v_pk_fma_f16 v18, v110, v26, v18
	v_pk_add_f16 v23, v59, v88
	v_pk_add_f16 v24, v60, v87
	v_pk_add_f16 v25, v61, v86
	v_exp_f16_sdwa v30, v22 dst_sel:WORD_0 dst_unused:UNUSED_PAD src0_sel:WORD_0
	v_exp_f16_sdwa v31, v23 dst_sel:WORD_0 dst_unused:UNUSED_PAD src0_sel:WORD_0
	v_exp_f16_sdwa v32, v24 dst_sel:WORD_0 dst_unused:UNUSED_PAD src0_sel:WORD_0
	v_exp_f16_sdwa v33, v25 dst_sel:WORD_0 dst_unused:UNUSED_PAD src0_sel:WORD_0
	v_exp_f16_sdwa v30, v22 dst_sel:WORD_1 dst_unused:UNUSED_PRESERVE src0_sel:WORD_1
	v_exp_f16_sdwa v31, v23 dst_sel:WORD_1 dst_unused:UNUSED_PRESERVE src0_sel:WORD_1
	v_exp_f16_sdwa v32, v24 dst_sel:WORD_1 dst_unused:UNUSED_PRESERVE src0_sel:WORD_1
	v_exp_f16_sdwa v33, v25 dst_sel:WORD_1 dst_unused:UNUSED_PRESERVE src0_sel:WORD_1
	s_nop 0
.LBB4_42:
	s_and_b64 vcc, exec, s[4:5]
	s_cbranch_vccz .LBB4_80
	global_load_dwordx3 v[146:148], v169, s[8:9]
	v_cmp_lt_u32_e64 s[64:65], 0, v199
	v_cmp_gt_u32_e64 s[66:67], 63, v199
	v_cmp_lt_u32_e64 s[68:69], 0, v180
	v_cmp_gt_u32_e64 s[70:71], 60, v180
	buffer_load_dwordx4 v[162:165], v200, s[36:39], 0 offen nt
	s_and_b64 s[72:73], s[68:69], s[64:65]
	s_and_b64 s[74:75], s[68:69], s[66:67]
	s_and_b64 s[76:77], s[70:71], s[64:65]
	s_and_b64 s[78:79], s[70:71], s[66:67]
	v_add_u32_e32 v245, 0xfffe7c00, v200
	v_add_u32_e32 v246, 0xfffe8000, v200
	s_mov_b64 exec, s[72:73]
	buffer_load_dwordx4 v[114:117], v245, s[36:39], 0 offen
	buffer_load_dwordx4 v[74:77], v245, s[36:39], 0 offen offset:512
	s_mov_b64 exec, -1
	s_mov_b64 exec, s[68:69]
	buffer_load_dwordx4 v[130:133], v246, s[36:39], 0 offen offset:512
	buffer_load_dwordx4 v[98:101], v246, s[36:39], 0 offen offset:1024
	s_mov_b64 exec, -1
	s_mov_b64 exec, s[74:75]
	buffer_load_dwordx4 v[138:141], v246, s[36:39], 0 offen offset:2048
	buffer_load_dwordx4 v[118:121], v246, s[36:39], 0 offen offset:2560
	s_mov_b64 exec, -1
	v_add_u32_e32 v245, 0xfffffc00, v200
	s_mov_b64 exec, s[64:65]
	buffer_load_dwordx4 v[86:89], v245, s[36:39], 0 offen
	buffer_load_dwordx4 v[46:49], v245, s[36:39], 0 offen offset:512
	s_mov_b64 exec, -1
	buffer_load_dwordx4 v[110:113], v200, s[36:39], 0 offen offset:512
	buffer_load_dwordx4 v[66:69], v200, s[36:39], 0 offen offset:1024
	s_mov_b64 exec, s[66:67]
	buffer_load_dwordx4 v[126:129], v200, s[36:39], 0 offen offset:2048
	buffer_load_dwordx4 v[90:93], v200, s[36:39], 0 offen offset:2560
	s_mov_b64 exec, -1
	v_add_u32_e32 v245, 0x17c00, v200
	v_add_u32_e32 v246, 0x18000, v200
	s_mov_b64 exec, s[64:65]
	buffer_load_dwordx4 v[54:57], v245, s[36:39], 0 offen
	buffer_load_dwordx4 v[22:25], v245, s[36:39], 0 offen offset:512
	s_mov_b64 exec, -1
	buffer_load_dwordx4 v[70:73], v246, s[36:39], 0 offen offset:512
	buffer_load_dwordx4 v[34:37], v246, s[36:39], 0 offen offset:1024
	s_mov_b64 exec, s[66:67]
	buffer_load_dwordx4 v[94:97], v246, s[36:39], 0 offen offset:2048
	buffer_load_dwordx4 v[50:53], v246, s[36:39], 0 offen offset:2560
	s_mov_b64 exec, -1
	v_add_u32_e32 v245, 0x18000, v200
	buffer_load_dwordx4 v[154:157], v245, s[36:39], 0 offen nt
	v_add_u32_e32 v246, 0x30000, v200
	buffer_load_dwordx4 v[150:153], v246, s[36:39], 0 offen nt
	v_add_u32_e32 v245, 0x2fc00, v200
	v_add_u32_e32 v246, 0x30000, v200
	v_add_u32_e32 v247, 0x47c00, v200
	v_add_u32_e32 v248, 0x48000, v200
	v_add_u32_e32 v249, 0x5fc00, v200
	v_add_u32_e32 v250, 0x60000, v200
	s_waitcnt vmcnt(22)
	v_cvt_pk_f16_f32 v6, v2, v3
	v_cvt_pk_f16_f32 v2, v8, v9
	v_cvt_pk_f16_f32 v7, v4, v5
	v_cvt_pk_f16_f32 v3, v10, v11
	v_cvt_pk_f16_f32 v8, v210, v211
	v_cvt_pk_f16_f32 v4, v214, v215
	v_cvt_pk_f16_f32 v9, v212, v213
	v_cvt_pk_f16_f32 v5, v216, v217
	s_not_b64 exec, s[72:73]
	s_cbranch_execz .Lmyf_C2_0
	v_mov_b32_e32 v114, v6
	v_mov_b32_e32 v115, v7
	v_mov_b32_e32 v116, v8
	v_mov_b32_e32 v117, v9
	v_mov_b32_e32 v74, v2
	v_mov_b32_e32 v75, v3
	v_mov_b32_e32 v76, v4
	v_mov_b32_e32 v77, v5

.Lmyf_C2_7:
	s_mov_b64 exec, -1
	s_waitcnt vmcnt(21)
	v_cvt_f16_f32_e32 v158, v147
	v_cvt_f16_f32_e32 v160, v146
	v_cvt_f16_f32_e32 v159, v148
	v_add_u32_e32 v251, 0x48000, v200
	buffer_load_dwordx4 v[146:149], v251, s[36:39], 0 offen nt
	s_waitcnt vmcnt(3)
	v_pk_mul_f16 v161, v160, v162 op_sel_hi:[0,1]
	v_pk_mul_f16 v204, v160, v165 op_sel_hi:[0,1]
	v_pk_mul_f16 v208, v158, v165 op_sel_hi:[0,1]
	v_pk_mul_f16 v212, v159, v165 op_sel_hi:[0,1]
	v_pk_mul_f16 v202, v160, v163 op_sel_hi:[0,1]
	v_pk_mul_f16 v203, v160, v164 op_sel_hi:[0,1]
	v_pk_mul_f16 v205, v158, v162 op_sel_hi:[0,1]
	s_mov_b64 exec, s[64:65]
	buffer_load_dwordx4 v[26:29], v245, s[36:39], 0 offen
	buffer_load_dwordx4 v[10:13], v245, s[36:39], 0 offen offset:512
	s_mov_b64 exec, -1
	v_pk_mul_f16 v206, v158, v163 op_sel_hi:[0,1]
	v_pk_mul_f16 v207, v158, v164 op_sel_hi:[0,1]
	v_pk_mul_f16 v209, v159, v162 op_sel_hi:[0,1]
	v_pk_mul_f16 v210, v159, v163 op_sel_hi:[0,1]
	v_pk_mul_f16 v211, v159, v164 op_sel_hi:[0,1]
	v_pk_fma_f16 v117, v117, v165, v204
	v_pk_fma_f16 v114, v114, v162, v161
	v_pk_fma_f16 v133, v133, v165, v204
	v_pk_fma_f16 v130, v130, v162, v161
	v_pk_fma_f16 v141, v141, v165, v204
	v_pk_fma_f16 v138, v138, v162, v161
	v_pk_fma_f16 v161, v89, v165, v208
	v_pk_fma_f16 v213, v113, v165, v208
	buffer_load_dwordx4 v[38:41], v246, s[36:39], 0 offen offset:512
	buffer_load_dwordx4 v[14:17], v246, s[36:39], 0 offen offset:1024
	v_pk_fma_f16 v208, v129, v165, v208
	v_pk_fma_f16 v217, v57, v165, v212
	v_pk_fma_f16 v221, v73, v165, v212
	v_pk_fma_f16 v165, v97, v165, v212
	v_pk_maximum3_f16 v212, v117, v133, v141
	v_pk_fma_f16 v116, v116, v164, v203
	v_pk_fma_f16 v115, v115, v163, v202
	v_pk_fma_f16 v132, v132, v164, v203
	v_pk_fma_f16 v131, v131, v163, v202
	v_pk_fma_f16 v140, v140, v164, v203
	v_pk_fma_f16 v139, v139, v163, v202
	v_pk_fma_f16 v202, v88, v164, v207
	v_pk_fma_f16 v203, v87, v163, v206
	v_pk_fma_f16 v204, v86, v162, v205
	v_pk_fma_f16 v214, v112, v164, v207
	v_pk_fma_f16 v215, v111, v163, v206
	s_mov_b64 exec, s[66:67]
	buffer_load_dwordx4 v[58:61], v246, s[36:39], 0 offen offset:2048
	buffer_load_dwordx4 v[18:21], v246, s[36:39], 0 offen offset:2560
	s_mov_b64 exec, -1
	v_pk_fma_f16 v216, v110, v162, v205
	v_pk_fma_f16 v207, v128, v164, v207
	v_pk_fma_f16 v206, v127, v163, v206
	v_pk_fma_f16 v205, v126, v162, v205
	v_pk_fma_f16 v218, v56, v164, v211
	v_pk_fma_f16 v219, v55, v163, v210
	v_pk_fma_f16 v220, v54, v162, v209
	v_pk_fma_f16 v222, v72, v164, v211
	v_pk_fma_f16 v223, v71, v163, v210
	v_pk_fma_f16 v224, v70, v162, v209
	v_pk_fma_f16 v164, v96, v164, v211
	v_pk_fma_f16 v163, v95, v163, v210
	v_pk_fma_f16 v162, v94, v162, v209
	v_pk_maximum3_f16 v209, v114, v130, v138
	v_pk_maximum3_f16 v210, v115, v131, v139
	v_pk_maximum3_f16 v211, v116, v132, v140
	v_pk_maximum3_f16 v228, v161, v213, v208
	v_pk_maximum3_f16 v232, v217, v221, v165
	v_pk_maximum3_f16 v225, v204, v216, v205
	v_pk_maximum3_f16 v226, v203, v215, v206
	v_pk_maximum3_f16 v227, v202, v214, v207
	v_pk_maximum3_f16 v229, v220, v224, v162
	v_pk_maximum3_f16 v230, v219, v223, v163
	v_pk_maximum3_f16 v212, v212, v228, v232
	v_pk_maximum3_f16 v231, v218, v222, v164
	v_pk_maximum3_f16 v209, v209, v225, v229
	v_pk_maximum3_f16 v210, v210, v226, v230
	v_pk_maximum3_f16 v211, v211, v227, v231
	v_pk_add_f16 v117, v117, v212 neg_lo:[0,1] neg_hi:[0,1]
	s_mov_b64 exec, s[64:65]
	buffer_load_dwordx4 v[78:81], v247, s[36:39], 0 offen
	buffer_load_dwordx4 v[30:33], v247, s[36:39], 0 offen offset:512
	s_mov_b64 exec, -1
	v_pk_add_f16 v114, v114, v209 neg_lo:[0,1] neg_hi:[0,1]
	v_pk_add_f16 v115, v115, v210 neg_lo:[0,1] neg_hi:[0,1]
	v_pk_add_f16 v116, v116, v211 neg_lo:[0,1] neg_hi:[0,1]
	v_pk_add_f16 v130, v130, v209 neg_lo:[0,1] neg_hi:[0,1]
	v_exp_f16_sdwa v225, v114 dst_sel:WORD_0 dst_unused:UNUSED_PAD src0_sel:WORD_0
	v_exp_f16_sdwa v226, v115 dst_sel:WORD_0 dst_unused:UNUSED_PAD src0_sel:WORD_0
	v_exp_f16_sdwa v227, v116 dst_sel:WORD_0 dst_unused:UNUSED_PAD src0_sel:WORD_0
	v_exp_f16_sdwa v228, v117 dst_sel:WORD_0 dst_unused:UNUSED_PAD src0_sel:WORD_0
	v_exp_f16_sdwa v225, v114 dst_sel:WORD_1 dst_unused:UNUSED_PRESERVE src0_sel:WORD_1
	v_exp_f16_sdwa v226, v115 dst_sel:WORD_1 dst_unused:UNUSED_PRESERVE src0_sel:WORD_1
	v_exp_f16_sdwa v227, v116 dst_sel:WORD_1 dst_unused:UNUSED_PRESERVE src0_sel:WORD_1
	v_exp_f16_sdwa v228, v117 dst_sel:WORD_1 dst_unused:UNUSED_PRESERVE src0_sel:WORD_1
	v_pk_add_f16 v131, v131, v210 neg_lo:[0,1] neg_hi:[0,1]
	v_pk_add_f16 v117, v225, 0
	v_pk_fma_f16 v77, v77, v228, 0
	v_pk_add_f16 v114, v228, 0
	v_pk_add_f16 v115, v227, 0
	v_pk_add_f16 v116, v226, 0
	v_pk_fma_f16 v76, v76, v227, 0
	v_pk_fma_f16 v75, v75, v226, 0
	v_pk_fma_f16 v74, v74, v225, 0
	v_pk_add_f16 v132, v132, v211 neg_lo:[0,1] neg_hi:[0,1]
	buffer_load_dwordx4 v[106:109], v248, s[36:39], 0 offen offset:512
	buffer_load_dwordx4 v[42:45], v248, s[36:39], 0 offen offset:1024
	v_pk_add_f16 v133, v133, v212 neg_lo:[0,1] neg_hi:[0,1]
	v_exp_f16_sdwa v225, v130 dst_sel:WORD_0 dst_unused:UNUSED_PAD src0_sel:WORD_0
	v_exp_f16_sdwa v226, v131 dst_sel:WORD_0 dst_unused:UNUSED_PAD src0_sel:WORD_0
	v_exp_f16_sdwa v227, v132 dst_sel:WORD_0 dst_unused:UNUSED_PAD src0_sel:WORD_0
	v_exp_f16_sdwa v228, v133 dst_sel:WORD_0 dst_unused:UNUSED_PAD src0_sel:WORD_0
	v_exp_f16_sdwa v225, v130 dst_sel:WORD_1 dst_unused:UNUSED_PRESERVE src0_sel:WORD_1
	v_exp_f16_sdwa v226, v131 dst_sel:WORD_1 dst_unused:UNUSED_PRESERVE src0_sel:WORD_1
	v_exp_f16_sdwa v227, v132 dst_sel:WORD_1 dst_unused:UNUSED_PRESERVE src0_sel:WORD_1
	v_exp_f16_sdwa v228, v133 dst_sel:WORD_1 dst_unused:UNUSED_PRESERVE src0_sel:WORD_1
	v_pk_add_f16 v117, v117, v225
	v_pk_fma_f16 v77, v101, v228, v77
	v_pk_add_f16 v101, v141, v212 neg_lo:[0,1] neg_hi:[0,1]
	v_pk_add_f16 v116, v116, v226
	v_pk_add_f16 v115, v115, v227
	v_pk_add_f16 v114, v114, v228
	v_pk_fma_f16 v74, v98, v225, v74
	v_pk_fma_f16 v75, v99, v226, v75
	v_pk_fma_f16 v76, v100, v227, v76
	v_pk_add_f16 v98, v138, v209 neg_lo:[0,1] neg_hi:[0,1]
	v_pk_add_f16 v99, v139, v210 neg_lo:[0,1] neg_hi:[0,1]
	v_pk_add_f16 v100, v140, v211 neg_lo:[0,1] neg_hi:[0,1]
	v_exp_f16_sdwa v130, v98 dst_sel:WORD_0 dst_unused:UNUSED_PAD src0_sel:WORD_0
	v_exp_f16_sdwa v131, v99 dst_sel:WORD_0 dst_unused:UNUSED_PAD src0_sel:WORD_0
	v_exp_f16_sdwa v132, v100 dst_sel:WORD_0 dst_unused:UNUSED_PAD src0_sel:WORD_0
	v_exp_f16_sdwa v133, v101 dst_sel:WORD_0 dst_unused:UNUSED_PAD src0_sel:WORD_0
	v_exp_f16_sdwa v130, v98 dst_sel:WORD_1 dst_unused:UNUSED_PRESERVE src0_sel:WORD_1
	v_exp_f16_sdwa v131, v99 dst_sel:WORD_1 dst_unused:UNUSED_PRESERVE src0_sel:WORD_1
	v_exp_f16_sdwa v132, v100 dst_sel:WORD_1 dst_unused:UNUSED_PRESERVE src0_sel:WORD_1
	v_exp_f16_sdwa v133, v101 dst_sel:WORD_1 dst_unused:UNUSED_PRESERVE src0_sel:WORD_1
	v_pk_add_f16 v101, v117, v130
	v_pk_add_f16 v98, v114, v133
	s_mov_b64 exec, s[66:67]
	buffer_load_dwordx4 v[122:125], v248, s[36:39], 0 offen offset:2048
	buffer_load_dwordx4 v[62:65], v248, s[36:39], 0 offen offset:2560
	s_mov_b64 exec, -1
	v_pk_add_f16 v99, v115, v132
	v_pk_add_f16 v100, v116, v131
	v_pk_fma_f16 v77, v121, v133, v77
	v_pk_fma_f16 v76, v120, v132, v76
	v_pk_fma_f16 v75, v119, v131, v75
	v_pk_fma_f16 v74, v118, v130, v74
	v_pk_add_f16 v114, v204, v209 neg_lo:[0,1] neg_hi:[0,1]
	v_pk_add_f16 v115, v203, v210 neg_lo:[0,1] neg_hi:[0,1]
	v_pk_add_f16 v116, v202, v211 neg_lo:[0,1] neg_hi:[0,1]
	v_pk_add_f16 v117, v161, v212 neg_lo:[0,1] neg_hi:[0,1]
	v_exp_f16_sdwa v118, v114 dst_sel:WORD_0 dst_unused:UNUSED_PAD src0_sel:WORD_0
	v_exp_f16_sdwa v119, v115 dst_sel:WORD_0 dst_unused:UNUSED_PAD src0_sel:WORD_0
	v_exp_f16_sdwa v120, v116 dst_sel:WORD_0 dst_unused:UNUSED_PAD src0_sel:WORD_0
	v_exp_f16_sdwa v121, v117 dst_sel:WORD_0 dst_unused:UNUSED_PAD src0_sel:WORD_0
	v_exp_f16_sdwa v118, v114 dst_sel:WORD_1 dst_unused:UNUSED_PRESERVE src0_sel:WORD_1
	v_exp_f16_sdwa v119, v115 dst_sel:WORD_1 dst_unused:UNUSED_PRESERVE src0_sel:WORD_1
	v_exp_f16_sdwa v120, v116 dst_sel:WORD_1 dst_unused:UNUSED_PRESERVE src0_sel:WORD_1
	v_exp_f16_sdwa v121, v117 dst_sel:WORD_1 dst_unused:UNUSED_PRESERVE src0_sel:WORD_1
	v_pk_add_f16 v114, v216, v209 neg_lo:[0,1] neg_hi:[0,1]
	v_pk_add_f16 v101, v101, v118
	v_pk_add_f16 v100, v100, v119
	v_pk_add_f16 v99, v99, v120
	s_mov_b64 exec, s[76:77]
	buffer_load_dwordx4 v[134:137], v249, s[36:39], 0 offen
	buffer_load_dwordx4 v[82:85], v249, s[36:39], 0 offen offset:512
	s_mov_b64 exec, -1
	v_pk_add_f16 v98, v98, v121
	v_pk_fma_f16 v74, v46, v118, v74
	v_pk_fma_f16 v75, v47, v119, v75
	v_pk_fma_f16 v76, v48, v120, v76
	v_pk_fma_f16 v77, v49, v121, v77
	v_pk_add_f16 v115, v215, v210 neg_lo:[0,1] neg_hi:[0,1]
	v_pk_add_f16 v116, v214, v211 neg_lo:[0,1] neg_hi:[0,1]
	v_pk_add_f16 v117, v213, v212 neg_lo:[0,1] neg_hi:[0,1]
	v_exp_f16_sdwa v118, v114 dst_sel:WORD_0 dst_unused:UNUSED_PAD src0_sel:WORD_0
	v_exp_f16_sdwa v119, v115 dst_sel:WORD_0 dst_unused:UNUSED_PAD src0_sel:WORD_0
	v_exp_f16_sdwa v120, v116 dst_sel:WORD_0 dst_unused:UNUSED_PAD src0_sel:WORD_0
	v_exp_f16_sdwa v121, v117 dst_sel:WORD_0 dst_unused:UNUSED_PAD src0_sel:WORD_0
	v_exp_f16_sdwa v118, v114 dst_sel:WORD_1 dst_unused:UNUSED_PRESERVE src0_sel:WORD_1
	v_exp_f16_sdwa v119, v115 dst_sel:WORD_1 dst_unused:UNUSED_PRESERVE src0_sel:WORD_1
	v_exp_f16_sdwa v120, v116 dst_sel:WORD_1 dst_unused:UNUSED_PRESERVE src0_sel:WORD_1
	v_exp_f16_sdwa v121, v117 dst_sel:WORD_1 dst_unused:UNUSED_PRESERVE src0_sel:WORD_1
	v_pk_add_f16 v114, v205, v209 neg_lo:[0,1] neg_hi:[0,1]
	v_pk_add_f16 v101, v101, v118
	v_pk_add_f16 v98, v98, v121
	v_pk_add_f16 v99, v99, v120
	v_pk_add_f16 v100, v100, v119
	v_pk_fma_f16 v77, v69, v121, v77
	v_pk_fma_f16 v76, v68, v120, v76
	s_mov_b64 exec, s[70:71]
	buffer_load_dwordx4 v[142:145], v250, s[36:39], 0 offen offset:512
	buffer_load_dwordx4 v[102:105], v250, s[36:39], 0 offen offset:1024
	s_mov_b64 exec, -1
	v_pk_fma_f16 v75, v67, v119, v75
	v_pk_fma_f16 v74, v66, v118, v74
	v_pk_add_f16 v115, v206, v210 neg_lo:[0,1] neg_hi:[0,1]
	v_pk_add_f16 v116, v207, v211 neg_lo:[0,1] neg_hi:[0,1]
	v_pk_add_f16 v117, v208, v212 neg_lo:[0,1] neg_hi:[0,1]
	v_exp_f16_sdwa v118, v114 dst_sel:WORD_0 dst_unused:UNUSED_PAD src0_sel:WORD_0
	v_exp_f16_sdwa v119, v115 dst_sel:WORD_0 dst_unused:UNUSED_PAD src0_sel:WORD_0
	v_exp_f16_sdwa v120, v116 dst_sel:WORD_0 dst_unused:UNUSED_PAD src0_sel:WORD_0
	v_exp_f16_sdwa v121, v117 dst_sel:WORD_0 dst_unused:UNUSED_PAD src0_sel:WORD_0
	v_exp_f16_sdwa v118, v114 dst_sel:WORD_1 dst_unused:UNUSED_PRESERVE src0_sel:WORD_1
	v_exp_f16_sdwa v119, v115 dst_sel:WORD_1 dst_unused:UNUSED_PRESERVE src0_sel:WORD_1
	v_exp_f16_sdwa v120, v116 dst_sel:WORD_1 dst_unused:UNUSED_PRESERVE src0_sel:WORD_1
	v_exp_f16_sdwa v121, v117 dst_sel:WORD_1 dst_unused:UNUSED_PRESERVE src0_sel:WORD_1
	v_pk_add_f16 v114, v220, v209 neg_lo:[0,1] neg_hi:[0,1]
	v_pk_add_f16 v101, v101, v118
	v_pk_add_f16 v100, v100, v119
	v_pk_add_f16 v99, v99, v120
	v_pk_add_f16 v98, v98, v121
	v_pk_fma_f16 v74, v90, v118, v74
	v_pk_fma_f16 v75, v91, v119, v75
	v_pk_fma_f16 v76, v92, v120, v76
	v_pk_fma_f16 v77, v93, v121, v77
	s_mov_b64 exec, s[78:79]
	buffer_load_dwordx4 v[6:9], v250, s[36:39], 0 offen offset:2048
	buffer_load_dwordx4 v[2:5], v250, s[36:39], 0 offen offset:2560
	s_mov_b64 exec, -1
	v_pk_add_f16 v115, v219, v210 neg_lo:[0,1] neg_hi:[0,1]
	v_pk_add_f16 v116, v218, v211 neg_lo:[0,1] neg_hi:[0,1]
	v_pk_add_f16 v117, v217, v212 neg_lo:[0,1] neg_hi:[0,1]
	v_exp_f16_sdwa v118, v114 dst_sel:WORD_0 dst_unused:UNUSED_PAD src0_sel:WORD_0
	v_exp_f16_sdwa v119, v115 dst_sel:WORD_0 dst_unused:UNUSED_PAD src0_sel:WORD_0
	v_exp_f16_sdwa v120, v116 dst_sel:WORD_0 dst_unused:UNUSED_PAD src0_sel:WORD_0
	v_exp_f16_sdwa v121, v117 dst_sel:WORD_0 dst_unused:UNUSED_PAD src0_sel:WORD_0
	v_exp_f16_sdwa v118, v114 dst_sel:WORD_1 dst_unused:UNUSED_PRESERVE src0_sel:WORD_1
	v_exp_f16_sdwa v119, v115 dst_sel:WORD_1 dst_unused:UNUSED_PRESERVE src0_sel:WORD_1
	v_exp_f16_sdwa v120, v116 dst_sel:WORD_1 dst_unused:UNUSED_PRESERVE src0_sel:WORD_1
	v_exp_f16_sdwa v121, v117 dst_sel:WORD_1 dst_unused:UNUSED_PRESERVE src0_sel:WORD_1
	v_pk_add_f16 v114, v224, v209 neg_lo:[0,1] neg_hi:[0,1]
	v_pk_add_f16 v101, v101, v118
	v_pk_add_f16 v98, v98, v121
	v_pk_add_f16 v99, v99, v120
	v_pk_add_f16 v100, v100, v119
	v_pk_fma_f16 v77, v25, v121, v77
	v_pk_fma_f16 v76, v24, v120, v76
	v_pk_fma_f16 v75, v23, v119, v75
	v_pk_fma_f16 v74, v22, v118, v74
	v_pk_add_f16 v115, v223, v210 neg_lo:[0,1] neg_hi:[0,1]
	v_pk_add_f16 v116, v222, v211 neg_lo:[0,1] neg_hi:[0,1]
	v_pk_add_f16 v117, v221, v212 neg_lo:[0,1] neg_hi:[0,1]
	v_exp_f16_sdwa v118, v114 dst_sel:WORD_0 dst_unused:UNUSED_PAD src0_sel:WORD_0
	v_exp_f16_sdwa v119, v115 dst_sel:WORD_0 dst_unused:UNUSED_PAD src0_sel:WORD_0
	v_exp_f16_sdwa v120, v116 dst_sel:WORD_0 dst_unused:UNUSED_PAD src0_sel:WORD_0
	v_exp_f16_sdwa v121, v117 dst_sel:WORD_0 dst_unused:UNUSED_PAD src0_sel:WORD_0
	v_exp_f16_sdwa v118, v114 dst_sel:WORD_1 dst_unused:UNUSED_PRESERVE src0_sel:WORD_1
	v_exp_f16_sdwa v119, v115 dst_sel:WORD_1 dst_unused:UNUSED_PRESERVE src0_sel:WORD_1
	v_exp_f16_sdwa v120, v116 dst_sel:WORD_1 dst_unused:UNUSED_PRESERVE src0_sel:WORD_1
	v_exp_f16_sdwa v121, v117 dst_sel:WORD_1 dst_unused:UNUSED_PRESERVE src0_sel:WORD_1
	v_pk_add_f16 v114, v162, v209 neg_lo:[0,1] neg_hi:[0,1]
	v_pk_add_f16 v101, v101, v118
	v_pk_add_f16 v100, v100, v119
	v_pk_add_f16 v99, v99, v120
	v_pk_add_f16 v98, v98, v121
	v_pk_fma_f16 v74, v34, v118, v74
	v_pk_fma_f16 v75, v35, v119, v75
	v_pk_fma_f16 v76, v36, v120, v76
	v_pk_fma_f16 v77, v37, v121, v77
	v_pk_add_f16 v115, v163, v210 neg_lo:[0,1] neg_hi:[0,1]
	v_pk_add_f16 v116, v164, v211 neg_lo:[0,1] neg_hi:[0,1]
	v_pk_add_f16 v117, v165, v212 neg_lo:[0,1] neg_hi:[0,1]
	v_exp_f16_sdwa v118, v114 dst_sel:WORD_0 dst_unused:UNUSED_PAD src0_sel:WORD_0
	v_exp_f16_sdwa v119, v115 dst_sel:WORD_0 dst_unused:UNUSED_PAD src0_sel:WORD_0
	v_exp_f16_sdwa v120, v116 dst_sel:WORD_0 dst_unused:UNUSED_PAD src0_sel:WORD_0
	v_exp_f16_sdwa v121, v117 dst_sel:WORD_0 dst_unused:UNUSED_PAD src0_sel:WORD_0
	v_exp_f16_sdwa v118, v114 dst_sel:WORD_1 dst_unused:UNUSED_PRESERVE src0_sel:WORD_1
	v_exp_f16_sdwa v119, v115 dst_sel:WORD_1 dst_unused:UNUSED_PRESERVE src0_sel:WORD_1
	v_exp_f16_sdwa v120, v116 dst_sel:WORD_1 dst_unused:UNUSED_PRESERVE src0_sel:WORD_1
	v_exp_f16_sdwa v121, v117 dst_sel:WORD_1 dst_unused:UNUSED_PRESERVE src0_sel:WORD_1
	v_pk_add_f16 v101, v101, v118
	v_pk_add_f16 v100, v100, v119
	v_rcp_f16_e32 v114, v101
	v_rcp_f16_sdwa v101, v101 dst_sel:DWORD dst_unused:UNUSED_PAD src0_sel:WORD_1
	v_pk_add_f16 v99, v99, v120
	v_rcp_f16_e32 v115, v100
	v_rcp_f16_sdwa v100, v100 dst_sel:DWORD dst_unused:UNUSED_PAD src0_sel:WORD_1
	v_pk_add_f16 v98, v98, v121
	v_rcp_f16_e32 v116, v99
	v_rcp_f16_sdwa v99, v99 dst_sel:DWORD dst_unused:UNUSED_PAD src0_sel:WORD_1
	v_rcp_f16_e32 v117, v98
	v_rcp_f16_sdwa v98, v98 dst_sel:DWORD dst_unused:UNUSED_PAD src0_sel:WORD_1
	v_pk_fma_f16 v74, v50, v118, v74
	v_pack_b32_f16 v101, v114, v101
	v_pk_fma_f16 v75, v51, v119, v75
	v_pk_mul_f16 v138, v74, v101
	v_pack_b32_f16 v74, v115, v100
	v_pk_fma_f16 v76, v52, v120, v76
	v_pk_mul_f16 v139, v75, v74
	v_pack_b32_f16 v74, v116, v99
	v_pk_fma_f16 v77, v53, v121, v77
	v_pk_mul_f16 v140, v76, v74
	v_pack_b32_f16 v74, v117, v98
	v_pk_mul_f16 v141, v77, v74
	s_waitcnt vmcnt(12)
	v_pk_mul_f16 v74, v160, v154 op_sel_hi:[0,1]
	v_pk_mul_f16 v77, v160, v157 op_sel_hi:[0,1]
	v_pk_mul_f16 v101, v158, v157 op_sel_hi:[0,1]
	v_pk_mul_f16 v117, v159, v157 op_sel_hi:[0,1]
	v_pk_mul_f16 v75, v160, v155 op_sel_hi:[0,1]
	v_pk_mul_f16 v76, v160, v156 op_sel_hi:[0,1]
	v_pk_mul_f16 v98, v158, v154 op_sel_hi:[0,1]
	v_pk_mul_f16 v99, v158, v155 op_sel_hi:[0,1]
	v_pk_mul_f16 v100, v158, v156 op_sel_hi:[0,1]
	v_pk_mul_f16 v114, v159, v154 op_sel_hi:[0,1]
	v_pk_mul_f16 v115, v159, v155 op_sel_hi:[0,1]
	v_pk_mul_f16 v116, v159, v156 op_sel_hi:[0,1]
	v_pk_fma_f16 v89, v89, v157, v77
	v_pk_fma_f16 v86, v86, v154, v74
	v_pk_fma_f16 v113, v113, v157, v77
	v_pk_fma_f16 v110, v110, v154, v74
	v_pk_fma_f16 v77, v129, v157, v77
	v_pk_fma_f16 v74, v126, v154, v74
	v_pk_fma_f16 v118, v57, v157, v101
	v_pk_fma_f16 v126, v73, v157, v101
	v_pk_fma_f16 v101, v97, v157, v101
	v_pk_fma_f16 v130, v29, v157, v117
	v_pk_fma_f16 v161, v41, v157, v117
	v_pk_fma_f16 v117, v61, v157, v117
	v_pk_maximum3_f16 v157, v89, v113, v77
	v_pk_fma_f16 v88, v88, v156, v76
	v_pk_fma_f16 v87, v87, v155, v75
	v_pk_fma_f16 v112, v112, v156, v76
	v_pk_fma_f16 v111, v111, v155, v75
	v_pk_fma_f16 v76, v128, v156, v76
	v_pk_fma_f16 v75, v127, v155, v75
	v_pk_fma_f16 v119, v56, v156, v100
	v_pk_fma_f16 v120, v55, v155, v99
	v_pk_fma_f16 v121, v54, v154, v98
	v_pk_fma_f16 v127, v72, v156, v100
	v_pk_fma_f16 v128, v71, v155, v99
	v_pk_fma_f16 v129, v70, v154, v98
	v_pk_fma_f16 v100, v96, v156, v100
	v_pk_fma_f16 v99, v95, v155, v99
	v_pk_fma_f16 v98, v94, v154, v98
	v_pk_fma_f16 v131, v28, v156, v116
	v_pk_fma_f16 v132, v27, v155, v115
	v_pk_fma_f16 v133, v26, v154, v114
	v_pk_fma_f16 v162, v40, v156, v116
	v_pk_fma_f16 v163, v39, v155, v115
	v_pk_fma_f16 v164, v38, v154, v114
	v_pk_fma_f16 v116, v60, v156, v116
	v_pk_fma_f16 v115, v59, v155, v115
	v_pk_fma_f16 v114, v58, v154, v114
	v_pk_maximum3_f16 v154, v86, v110, v74
	v_pk_maximum3_f16 v155, v87, v111, v75
	v_pk_maximum3_f16 v156, v88, v112, v76
	v_pk_maximum3_f16 v204, v118, v126, v101
	v_pk_maximum3_f16 v208, v130, v161, v117
	v_pk_maximum3_f16 v165, v121, v129, v98
	v_pk_maximum3_f16 v202, v120, v128, v99
	v_pk_maximum3_f16 v203, v119, v127, v100
	v_pk_maximum3_f16 v205, v133, v164, v114
	v_pk_maximum3_f16 v206, v132, v163, v115
	v_pk_maximum3_f16 v157, v157, v204, v208
	v_pk_maximum3_f16 v207, v131, v162, v116
	v_pk_maximum3_f16 v154, v154, v165, v205
	v_pk_maximum3_f16 v155, v155, v202, v206
	v_pk_maximum3_f16 v156, v156, v203, v207
	v_pk_add_f16 v89, v89, v157 neg_lo:[0,1] neg_hi:[0,1]
	v_pk_add_f16 v86, v86, v154 neg_lo:[0,1] neg_hi:[0,1]
	v_pk_add_f16 v87, v87, v155 neg_lo:[0,1] neg_hi:[0,1]
	v_pk_add_f16 v88, v88, v156 neg_lo:[0,1] neg_hi:[0,1]
	v_pk_add_f16 v110, v110, v154 neg_lo:[0,1] neg_hi:[0,1]
	v_exp_f16_sdwa v165, v86 dst_sel:WORD_0 dst_unused:UNUSED_PAD src0_sel:WORD_0
	v_exp_f16_sdwa v202, v87 dst_sel:WORD_0 dst_unused:UNUSED_PAD src0_sel:WORD_0
	v_exp_f16_sdwa v203, v88 dst_sel:WORD_0 dst_unused:UNUSED_PAD src0_sel:WORD_0
	v_exp_f16_sdwa v204, v89 dst_sel:WORD_0 dst_unused:UNUSED_PAD src0_sel:WORD_0
	v_exp_f16_sdwa v165, v86 dst_sel:WORD_1 dst_unused:UNUSED_PRESERVE src0_sel:WORD_1
	v_exp_f16_sdwa v202, v87 dst_sel:WORD_1 dst_unused:UNUSED_PRESERVE src0_sel:WORD_1
	v_exp_f16_sdwa v203, v88 dst_sel:WORD_1 dst_unused:UNUSED_PRESERVE src0_sel:WORD_1
	v_exp_f16_sdwa v204, v89 dst_sel:WORD_1 dst_unused:UNUSED_PRESERVE src0_sel:WORD_1
	v_pk_add_f16 v111, v111, v155 neg_lo:[0,1] neg_hi:[0,1]
	v_pk_add_f16 v89, v165, 0
	v_pk_fma_f16 v49, v49, v204, 0
	v_pk_add_f16 v86, v204, 0
	v_pk_add_f16 v87, v203, 0
	v_pk_add_f16 v88, v202, 0
	v_pk_fma_f16 v48, v48, v203, 0
	v_pk_fma_f16 v47, v47, v202, 0
	v_pk_fma_f16 v46, v46, v165, 0
	v_pk_add_f16 v112, v112, v156 neg_lo:[0,1] neg_hi:[0,1]
	v_pk_add_f16 v113, v113, v157 neg_lo:[0,1] neg_hi:[0,1]
	v_exp_f16_sdwa v165, v110 dst_sel:WORD_0 dst_unused:UNUSED_PAD src0_sel:WORD_0
	v_exp_f16_sdwa v202, v111 dst_sel:WORD_0 dst_unused:UNUSED_PAD src0_sel:WORD_0
	v_exp_f16_sdwa v203, v112 dst_sel:WORD_0 dst_unused:UNUSED_PAD src0_sel:WORD_0
	v_exp_f16_sdwa v204, v113 dst_sel:WORD_0 dst_unused:UNUSED_PAD src0_sel:WORD_0
	v_exp_f16_sdwa v165, v110 dst_sel:WORD_1 dst_unused:UNUSED_PRESERVE src0_sel:WORD_1
	v_exp_f16_sdwa v202, v111 dst_sel:WORD_1 dst_unused:UNUSED_PRESERVE src0_sel:WORD_1
	v_exp_f16_sdwa v203, v112 dst_sel:WORD_1 dst_unused:UNUSED_PRESERVE src0_sel:WORD_1
	v_exp_f16_sdwa v204, v113 dst_sel:WORD_1 dst_unused:UNUSED_PRESERVE src0_sel:WORD_1
	v_pk_add_f16 v89, v89, v165
	v_pk_fma_f16 v49, v69, v204, v49
	v_pk_add_f16 v69, v77, v157 neg_lo:[0,1] neg_hi:[0,1]
	v_pk_add_f16 v88, v88, v202
	v_pk_add_f16 v87, v87, v203
	v_pk_add_f16 v86, v86, v204
	v_pk_fma_f16 v46, v66, v165, v46
	v_pk_fma_f16 v47, v67, v202, v47
	v_pk_fma_f16 v48, v68, v203, v48
	v_pk_add_f16 v66, v74, v154 neg_lo:[0,1] neg_hi:[0,1]
	v_pk_add_f16 v67, v75, v155 neg_lo:[0,1] neg_hi:[0,1]
	v_pk_add_f16 v68, v76, v156 neg_lo:[0,1] neg_hi:[0,1]
	v_exp_f16_sdwa v74, v66 dst_sel:WORD_0 dst_unused:UNUSED_PAD src0_sel:WORD_0
	v_exp_f16_sdwa v75, v67 dst_sel:WORD_0 dst_unused:UNUSED_PAD src0_sel:WORD_0
	v_exp_f16_sdwa v76, v68 dst_sel:WORD_0 dst_unused:UNUSED_PAD src0_sel:WORD_0
	v_exp_f16_sdwa v77, v69 dst_sel:WORD_0 dst_unused:UNUSED_PAD src0_sel:WORD_0
	v_exp_f16_sdwa v74, v66 dst_sel:WORD_1 dst_unused:UNUSED_PRESERVE src0_sel:WORD_1
	v_exp_f16_sdwa v75, v67 dst_sel:WORD_1 dst_unused:UNUSED_PRESERVE src0_sel:WORD_1
	v_exp_f16_sdwa v76, v68 dst_sel:WORD_1 dst_unused:UNUSED_PRESERVE src0_sel:WORD_1
	v_exp_f16_sdwa v77, v69 dst_sel:WORD_1 dst_unused:UNUSED_PRESERVE src0_sel:WORD_1
	v_pk_add_f16 v69, v89, v74
	v_pk_add_f16 v66, v86, v77
	v_pk_add_f16 v67, v87, v76
	v_pk_add_f16 v68, v88, v75
	v_pk_fma_f16 v49, v93, v77, v49
	v_pk_fma_f16 v48, v92, v76, v48
	v_pk_fma_f16 v47, v91, v75, v47
	v_pk_fma_f16 v46, v90, v74, v46
	v_pk_add_f16 v74, v121, v154 neg_lo:[0,1] neg_hi:[0,1]
	v_pk_add_f16 v75, v120, v155 neg_lo:[0,1] neg_hi:[0,1]
	v_pk_add_f16 v76, v119, v156 neg_lo:[0,1] neg_hi:[0,1]
	v_pk_add_f16 v77, v118, v157 neg_lo:[0,1] neg_hi:[0,1]
	v_exp_f16_sdwa v86, v74 dst_sel:WORD_0 dst_unused:UNUSED_PAD src0_sel:WORD_0
	v_exp_f16_sdwa v87, v75 dst_sel:WORD_0 dst_unused:UNUSED_PAD src0_sel:WORD_0
	v_exp_f16_sdwa v88, v76 dst_sel:WORD_0 dst_unused:UNUSED_PAD src0_sel:WORD_0
	v_exp_f16_sdwa v89, v77 dst_sel:WORD_0 dst_unused:UNUSED_PAD src0_sel:WORD_0
	v_exp_f16_sdwa v86, v74 dst_sel:WORD_1 dst_unused:UNUSED_PRESERVE src0_sel:WORD_1
	v_exp_f16_sdwa v87, v75 dst_sel:WORD_1 dst_unused:UNUSED_PRESERVE src0_sel:WORD_1
	v_exp_f16_sdwa v88, v76 dst_sel:WORD_1 dst_unused:UNUSED_PRESERVE src0_sel:WORD_1
	v_exp_f16_sdwa v89, v77 dst_sel:WORD_1 dst_unused:UNUSED_PRESERVE src0_sel:WORD_1
	v_pk_add_f16 v74, v129, v154 neg_lo:[0,1] neg_hi:[0,1]
	v_pk_add_f16 v69, v69, v86
	v_pk_add_f16 v68, v68, v87
	v_pk_add_f16 v67, v67, v88
	v_pk_add_f16 v66, v66, v89
	v_pk_fma_f16 v46, v22, v86, v46
	v_pk_fma_f16 v47, v23, v87, v47
	v_pk_fma_f16 v48, v24, v88, v48
	v_pk_fma_f16 v49, v25, v89, v49
	v_pk_add_f16 v75, v128, v155 neg_lo:[0,1] neg_hi:[0,1]
	v_pk_add_f16 v76, v127, v156 neg_lo:[0,1] neg_hi:[0,1]
	v_pk_add_f16 v77, v126, v157 neg_lo:[0,1] neg_hi:[0,1]
	v_exp_f16_sdwa v86, v74 dst_sel:WORD_0 dst_unused:UNUSED_PAD src0_sel:WORD_0
	v_exp_f16_sdwa v87, v75 dst_sel:WORD_0 dst_unused:UNUSED_PAD src0_sel:WORD_0
	v_exp_f16_sdwa v88, v76 dst_sel:WORD_0 dst_unused:UNUSED_PAD src0_sel:WORD_0
	v_exp_f16_sdwa v89, v77 dst_sel:WORD_0 dst_unused:UNUSED_PAD src0_sel:WORD_0
	v_exp_f16_sdwa v86, v74 dst_sel:WORD_1 dst_unused:UNUSED_PRESERVE src0_sel:WORD_1
	v_exp_f16_sdwa v87, v75 dst_sel:WORD_1 dst_unused:UNUSED_PRESERVE src0_sel:WORD_1
	v_exp_f16_sdwa v88, v76 dst_sel:WORD_1 dst_unused:UNUSED_PRESERVE src0_sel:WORD_1
	v_exp_f16_sdwa v89, v77 dst_sel:WORD_1 dst_unused:UNUSED_PRESERVE src0_sel:WORD_1
	v_pk_add_f16 v74, v98, v154 neg_lo:[0,1] neg_hi:[0,1]
	v_pk_add_f16 v69, v69, v86
	v_pk_add_f16 v66, v66, v89
	v_pk_add_f16 v67, v67, v88
	v_pk_add_f16 v68, v68, v87
	v_pk_fma_f16 v49, v37, v89, v49
	v_pk_fma_f16 v48, v36, v88, v48
	v_pk_fma_f16 v47, v35, v87, v47
	v_pk_fma_f16 v46, v34, v86, v46
	v_pk_add_f16 v75, v99, v155 neg_lo:[0,1] neg_hi:[0,1]
	v_pk_add_f16 v76, v100, v156 neg_lo:[0,1] neg_hi:[0,1]
	v_pk_add_f16 v77, v101, v157 neg_lo:[0,1] neg_hi:[0,1]
	v_exp_f16_sdwa v86, v74 dst_sel:WORD_0 dst_unused:UNUSED_PAD src0_sel:WORD_0
	v_exp_f16_sdwa v87, v75 dst_sel:WORD_0 dst_unused:UNUSED_PAD src0_sel:WORD_0
	v_exp_f16_sdwa v88, v76 dst_sel:WORD_0 dst_unused:UNUSED_PAD src0_sel:WORD_0
	v_exp_f16_sdwa v89, v77 dst_sel:WORD_0 dst_unused:UNUSED_PAD src0_sel:WORD_0
	v_exp_f16_sdwa v86, v74 dst_sel:WORD_1 dst_unused:UNUSED_PRESERVE src0_sel:WORD_1
	v_exp_f16_sdwa v87, v75 dst_sel:WORD_1 dst_unused:UNUSED_PRESERVE src0_sel:WORD_1
	v_exp_f16_sdwa v88, v76 dst_sel:WORD_1 dst_unused:UNUSED_PRESERVE src0_sel:WORD_1
	v_exp_f16_sdwa v89, v77 dst_sel:WORD_1 dst_unused:UNUSED_PRESERVE src0_sel:WORD_1
	v_pk_add_f16 v74, v133, v154 neg_lo:[0,1] neg_hi:[0,1]
	v_pk_add_f16 v69, v69, v86
	v_pk_add_f16 v68, v68, v87
	v_pk_add_f16 v67, v67, v88
	v_pk_add_f16 v66, v66, v89
	v_pk_fma_f16 v46, v50, v86, v46
	v_pk_fma_f16 v47, v51, v87, v47
	v_pk_fma_f16 v48, v52, v88, v48
	v_pk_fma_f16 v49, v53, v89, v49
	v_pk_add_f16 v75, v132, v155 neg_lo:[0,1] neg_hi:[0,1]
	v_pk_add_f16 v76, v131, v156 neg_lo:[0,1] neg_hi:[0,1]
	v_pk_add_f16 v77, v130, v157 neg_lo:[0,1] neg_hi:[0,1]
	v_exp_f16_sdwa v86, v74 dst_sel:WORD_0 dst_unused:UNUSED_PAD src0_sel:WORD_0
	v_exp_f16_sdwa v87, v75 dst_sel:WORD_0 dst_unused:UNUSED_PAD src0_sel:WORD_0
	v_exp_f16_sdwa v88, v76 dst_sel:WORD_0 dst_unused:UNUSED_PAD src0_sel:WORD_0
	v_exp_f16_sdwa v89, v77 dst_sel:WORD_0 dst_unused:UNUSED_PAD src0_sel:WORD_0
	v_exp_f16_sdwa v86, v74 dst_sel:WORD_1 dst_unused:UNUSED_PRESERVE src0_sel:WORD_1
	v_exp_f16_sdwa v87, v75 dst_sel:WORD_1 dst_unused:UNUSED_PRESERVE src0_sel:WORD_1
	v_exp_f16_sdwa v88, v76 dst_sel:WORD_1 dst_unused:UNUSED_PRESERVE src0_sel:WORD_1
	v_exp_f16_sdwa v89, v77 dst_sel:WORD_1 dst_unused:UNUSED_PRESERVE src0_sel:WORD_1
	v_pk_add_f16 v74, v164, v154 neg_lo:[0,1] neg_hi:[0,1]
	v_pk_add_f16 v69, v69, v86
	v_pk_add_f16 v66, v66, v89
	v_pk_add_f16 v67, v67, v88
	v_pk_add_f16 v68, v68, v87
	v_pk_fma_f16 v49, v13, v89, v49
	v_pk_fma_f16 v48, v12, v88, v48
	v_pk_fma_f16 v47, v11, v87, v47
	v_pk_fma_f16 v46, v10, v86, v46
	v_pk_add_f16 v75, v163, v155 neg_lo:[0,1] neg_hi:[0,1]
	v_pk_add_f16 v76, v162, v156 neg_lo:[0,1] neg_hi:[0,1]
	v_pk_add_f16 v77, v161, v157 neg_lo:[0,1] neg_hi:[0,1]
	v_exp_f16_sdwa v86, v74 dst_sel:WORD_0 dst_unused:UNUSED_PAD src0_sel:WORD_0
	v_exp_f16_sdwa v87, v75 dst_sel:WORD_0 dst_unused:UNUSED_PAD src0_sel:WORD_0
	v_exp_f16_sdwa v88, v76 dst_sel:WORD_0 dst_unused:UNUSED_PAD src0_sel:WORD_0
	v_exp_f16_sdwa v89, v77 dst_sel:WORD_0 dst_unused:UNUSED_PAD src0_sel:WORD_0
	v_exp_f16_sdwa v86, v74 dst_sel:WORD_1 dst_unused:UNUSED_PRESERVE src0_sel:WORD_1
	v_exp_f16_sdwa v87, v75 dst_sel:WORD_1 dst_unused:UNUSED_PRESERVE src0_sel:WORD_1
	v_exp_f16_sdwa v88, v76 dst_sel:WORD_1 dst_unused:UNUSED_PRESERVE src0_sel:WORD_1
	v_exp_f16_sdwa v89, v77 dst_sel:WORD_1 dst_unused:UNUSED_PRESERVE src0_sel:WORD_1
	v_pk_add_f16 v74, v114, v154 neg_lo:[0,1] neg_hi:[0,1]
	v_pk_add_f16 v69, v69, v86
	v_pk_add_f16 v68, v68, v87
	v_pk_add_f16 v67, v67, v88
	v_pk_add_f16 v66, v66, v89
	v_pk_fma_f16 v46, v14, v86, v46
	v_pk_fma_f16 v47, v15, v87, v47
	v_pk_fma_f16 v48, v16, v88, v48
	v_pk_fma_f16 v49, v17, v89, v49
	v_pk_add_f16 v75, v115, v155 neg_lo:[0,1] neg_hi:[0,1]
	v_pk_add_f16 v76, v116, v156 neg_lo:[0,1] neg_hi:[0,1]
	v_pk_add_f16 v77, v117, v157 neg_lo:[0,1] neg_hi:[0,1]
	v_exp_f16_sdwa v86, v74 dst_sel:WORD_0 dst_unused:UNUSED_PAD src0_sel:WORD_0
	v_exp_f16_sdwa v87, v75 dst_sel:WORD_0 dst_unused:UNUSED_PAD src0_sel:WORD_0
	v_exp_f16_sdwa v88, v76 dst_sel:WORD_0 dst_unused:UNUSED_PAD src0_sel:WORD_0
	v_exp_f16_sdwa v89, v77 dst_sel:WORD_0 dst_unused:UNUSED_PAD src0_sel:WORD_0
	v_exp_f16_sdwa v86, v74 dst_sel:WORD_1 dst_unused:UNUSED_PRESERVE src0_sel:WORD_1
	v_exp_f16_sdwa v87, v75 dst_sel:WORD_1 dst_unused:UNUSED_PRESERVE src0_sel:WORD_1
	v_exp_f16_sdwa v88, v76 dst_sel:WORD_1 dst_unused:UNUSED_PRESERVE src0_sel:WORD_1
	v_exp_f16_sdwa v89, v77 dst_sel:WORD_1 dst_unused:UNUSED_PRESERVE src0_sel:WORD_1
	v_pk_add_f16 v69, v69, v86
	v_pk_add_f16 v68, v68, v87
	v_rcp_f16_e32 v74, v69
	v_rcp_f16_sdwa v69, v69 dst_sel:DWORD dst_unused:UNUSED_PAD src0_sel:WORD_1
	v_pk_add_f16 v67, v67, v88
	v_rcp_f16_e32 v75, v68
	v_rcp_f16_sdwa v68, v68 dst_sel:DWORD dst_unused:UNUSED_PAD src0_sel:WORD_1
	v_pk_add_f16 v66, v66, v89
	v_pk_fma_f16 v46, v18, v86, v46
	v_rcp_f16_e32 v86, v67
	v_rcp_f16_sdwa v67, v67 dst_sel:DWORD dst_unused:UNUSED_PAD src0_sel:WORD_1
	v_pk_fma_f16 v47, v19, v87, v47
	v_rcp_f16_e32 v87, v66
	v_rcp_f16_sdwa v66, v66 dst_sel:DWORD dst_unused:UNUSED_PAD src0_sel:WORD_1
	v_pack_b32_f16 v69, v74, v69
	v_pk_mul_f16 v77, v46, v69
	v_pack_b32_f16 v46, v75, v68
	v_pk_fma_f16 v48, v20, v88, v48
	v_pk_mul_f16 v76, v47, v46
	v_pack_b32_f16 v46, v86, v67
	v_pk_fma_f16 v49, v21, v89, v49
	v_pk_mul_f16 v75, v48, v46
	v_pack_b32_f16 v46, v87, v66
	v_pk_mul_f16 v74, v49, v46
	s_waitcnt vmcnt(6)
	v_pk_mul_f16 v49, v160, v153 op_sel_hi:[0,1]
	v_pk_mul_f16 v46, v160, v150 op_sel_hi:[0,1]
	v_pk_mul_f16 v47, v160, v151 op_sel_hi:[0,1]
	v_pk_mul_f16 v48, v160, v152 op_sel_hi:[0,1]
	v_pk_mul_f16 v69, v158, v153 op_sel_hi:[0,1]
	v_pk_mul_f16 v89, v159, v153 op_sel_hi:[0,1]
	v_pk_fma_f16 v57, v57, v153, v49
	v_pk_fma_f16 v73, v73, v153, v49
	v_pk_fma_f16 v49, v97, v153, v49
	v_pk_mul_f16 v66, v158, v150 op_sel_hi:[0,1]
	v_pk_maximum3_f16 v117, v57, v73, v49
	v_pk_mul_f16 v67, v158, v151 op_sel_hi:[0,1]
	v_pk_mul_f16 v68, v158, v152 op_sel_hi:[0,1]
	v_pk_mul_f16 v86, v159, v150 op_sel_hi:[0,1]
	v_pk_mul_f16 v87, v159, v151 op_sel_hi:[0,1]
	v_pk_mul_f16 v88, v159, v152 op_sel_hi:[0,1]
	v_pk_fma_f16 v56, v56, v152, v48
	v_pk_fma_f16 v55, v55, v151, v47
	v_pk_fma_f16 v54, v54, v150, v46
	v_pk_fma_f16 v72, v72, v152, v48
	v_pk_fma_f16 v71, v71, v151, v47
	v_pk_fma_f16 v70, v70, v150, v46
	v_pk_fma_f16 v48, v96, v152, v48
	v_pk_fma_f16 v47, v95, v151, v47
	v_pk_fma_f16 v46, v94, v150, v46
	v_pk_fma_f16 v90, v29, v153, v69
	v_pk_fma_f16 v94, v41, v153, v69
	v_pk_fma_f16 v69, v61, v153, v69
	v_pk_fma_f16 v98, v81, v153, v89
	v_pk_fma_f16 v110, v109, v153, v89
	v_pk_fma_f16 v89, v125, v153, v89
	v_pk_maximum3_f16 v114, v54, v70, v46
	v_pk_maximum3_f16 v115, v55, v71, v47
	v_pk_maximum3_f16 v116, v56, v72, v48
	v_pk_maximum3_f16 v121, v90, v94, v69
	v_pk_fma_f16 v91, v28, v152, v68
	v_pk_maximum3_f16 v129, v98, v110, v89
	v_pk_fma_f16 v92, v27, v151, v67
	v_pk_maximum3_f16 v117, v117, v121, v129
	v_pk_fma_f16 v93, v26, v150, v66
	v_pk_fma_f16 v95, v40, v152, v68
	v_pk_fma_f16 v96, v39, v151, v67
	v_pk_fma_f16 v97, v38, v150, v66
	v_pk_fma_f16 v68, v60, v152, v68
	v_pk_fma_f16 v67, v59, v151, v67
	v_pk_fma_f16 v66, v58, v150, v66
	v_pk_fma_f16 v99, v80, v152, v88
	v_pk_fma_f16 v100, v79, v151, v87
	v_pk_fma_f16 v101, v78, v150, v86
	v_pk_fma_f16 v111, v108, v152, v88
	v_pk_fma_f16 v112, v107, v151, v87
	v_pk_fma_f16 v113, v106, v150, v86
	v_pk_fma_f16 v88, v124, v152, v88
	v_pk_fma_f16 v87, v123, v151, v87
	v_pk_fma_f16 v86, v122, v150, v86
	v_pk_maximum3_f16 v118, v93, v97, v66
	v_pk_maximum3_f16 v119, v92, v96, v67
	v_pk_maximum3_f16 v120, v91, v95, v68
	v_pk_maximum3_f16 v127, v100, v112, v87
	v_pk_maximum3_f16 v128, v99, v111, v88
	v_pk_maximum3_f16 v126, v101, v113, v86
	v_pk_maximum3_f16 v114, v114, v118, v126
	v_pk_maximum3_f16 v115, v115, v119, v127
	v_pk_maximum3_f16 v116, v116, v120, v128
	v_pk_add_f16 v57, v57, v117 neg_lo:[0,1] neg_hi:[0,1]
	v_pk_add_f16 v54, v54, v114 neg_lo:[0,1] neg_hi:[0,1]
	v_pk_add_f16 v55, v55, v115 neg_lo:[0,1] neg_hi:[0,1]
	v_pk_add_f16 v56, v56, v116 neg_lo:[0,1] neg_hi:[0,1]
	v_pk_add_f16 v70, v70, v114 neg_lo:[0,1] neg_hi:[0,1]
	v_exp_f16_sdwa v118, v54 dst_sel:WORD_0 dst_unused:UNUSED_PAD src0_sel:WORD_0
	v_exp_f16_sdwa v119, v55 dst_sel:WORD_0 dst_unused:UNUSED_PAD src0_sel:WORD_0
	v_exp_f16_sdwa v120, v56 dst_sel:WORD_0 dst_unused:UNUSED_PAD src0_sel:WORD_0
	v_exp_f16_sdwa v121, v57 dst_sel:WORD_0 dst_unused:UNUSED_PAD src0_sel:WORD_0
	v_exp_f16_sdwa v118, v54 dst_sel:WORD_1 dst_unused:UNUSED_PRESERVE src0_sel:WORD_1
	v_exp_f16_sdwa v119, v55 dst_sel:WORD_1 dst_unused:UNUSED_PRESERVE src0_sel:WORD_1
	v_exp_f16_sdwa v120, v56 dst_sel:WORD_1 dst_unused:UNUSED_PRESERVE src0_sel:WORD_1
	v_exp_f16_sdwa v121, v57 dst_sel:WORD_1 dst_unused:UNUSED_PRESERVE src0_sel:WORD_1
	v_pk_add_f16 v71, v71, v115 neg_lo:[0,1] neg_hi:[0,1]
	v_pk_add_f16 v57, v118, 0
	v_pk_fma_f16 v25, v25, v121, 0
	v_pk_add_f16 v54, v121, 0
	v_pk_add_f16 v55, v120, 0
	v_pk_add_f16 v56, v119, 0
	v_pk_fma_f16 v24, v24, v120, 0
	v_pk_fma_f16 v23, v23, v119, 0
	v_pk_fma_f16 v22, v22, v118, 0
	v_pk_add_f16 v72, v72, v116 neg_lo:[0,1] neg_hi:[0,1]
	v_pk_add_f16 v73, v73, v117 neg_lo:[0,1] neg_hi:[0,1]
	v_exp_f16_sdwa v118, v70 dst_sel:WORD_0 dst_unused:UNUSED_PAD src0_sel:WORD_0
	v_exp_f16_sdwa v119, v71 dst_sel:WORD_0 dst_unused:UNUSED_PAD src0_sel:WORD_0
	v_exp_f16_sdwa v120, v72 dst_sel:WORD_0 dst_unused:UNUSED_PAD src0_sel:WORD_0
	v_exp_f16_sdwa v121, v73 dst_sel:WORD_0 dst_unused:UNUSED_PAD src0_sel:WORD_0
	v_exp_f16_sdwa v118, v70 dst_sel:WORD_1 dst_unused:UNUSED_PRESERVE src0_sel:WORD_1
	v_exp_f16_sdwa v119, v71 dst_sel:WORD_1 dst_unused:UNUSED_PRESERVE src0_sel:WORD_1
	v_exp_f16_sdwa v120, v72 dst_sel:WORD_1 dst_unused:UNUSED_PRESERVE src0_sel:WORD_1
	v_exp_f16_sdwa v121, v73 dst_sel:WORD_1 dst_unused:UNUSED_PRESERVE src0_sel:WORD_1
	v_pk_add_f16 v57, v57, v118
	v_pk_fma_f16 v25, v37, v121, v25
	v_pk_add_f16 v37, v49, v117 neg_lo:[0,1] neg_hi:[0,1]
	v_pk_add_f16 v56, v56, v119
	v_pk_add_f16 v55, v55, v120
	v_pk_add_f16 v54, v54, v121
	v_pk_fma_f16 v22, v34, v118, v22
	v_pk_fma_f16 v23, v35, v119, v23
	v_pk_fma_f16 v24, v36, v120, v24
	v_pk_add_f16 v34, v46, v114 neg_lo:[0,1] neg_hi:[0,1]
	v_pk_add_f16 v35, v47, v115 neg_lo:[0,1] neg_hi:[0,1]
	v_pk_add_f16 v36, v48, v116 neg_lo:[0,1] neg_hi:[0,1]
	v_exp_f16_sdwa v46, v34 dst_sel:WORD_0 dst_unused:UNUSED_PAD src0_sel:WORD_0
	v_exp_f16_sdwa v47, v35 dst_sel:WORD_0 dst_unused:UNUSED_PAD src0_sel:WORD_0
	v_exp_f16_sdwa v48, v36 dst_sel:WORD_0 dst_unused:UNUSED_PAD src0_sel:WORD_0
	v_exp_f16_sdwa v49, v37 dst_sel:WORD_0 dst_unused:UNUSED_PAD src0_sel:WORD_0
	v_exp_f16_sdwa v46, v34 dst_sel:WORD_1 dst_unused:UNUSED_PRESERVE src0_sel:WORD_1
	v_exp_f16_sdwa v47, v35 dst_sel:WORD_1 dst_unused:UNUSED_PRESERVE src0_sel:WORD_1
	v_exp_f16_sdwa v48, v36 dst_sel:WORD_1 dst_unused:UNUSED_PRESERVE src0_sel:WORD_1
	v_exp_f16_sdwa v49, v37 dst_sel:WORD_1 dst_unused:UNUSED_PRESERVE src0_sel:WORD_1
	v_pk_add_f16 v37, v57, v46
	v_pk_add_f16 v34, v54, v49
	v_pk_add_f16 v35, v55, v48
	v_pk_add_f16 v36, v56, v47
	v_pk_fma_f16 v25, v53, v49, v25
	v_pk_fma_f16 v24, v52, v48, v24
	v_pk_fma_f16 v23, v51, v47, v23
	v_pk_fma_f16 v22, v50, v46, v22
	v_pk_add_f16 v46, v93, v114 neg_lo:[0,1] neg_hi:[0,1]
	v_pk_add_f16 v47, v92, v115 neg_lo:[0,1] neg_hi:[0,1]
	v_pk_add_f16 v48, v91, v116 neg_lo:[0,1] neg_hi:[0,1]
	v_pk_add_f16 v49, v90, v117 neg_lo:[0,1] neg_hi:[0,1]
	v_exp_f16_sdwa v50, v46 dst_sel:WORD_0 dst_unused:UNUSED_PAD src0_sel:WORD_0
	v_exp_f16_sdwa v51, v47 dst_sel:WORD_0 dst_unused:UNUSED_PAD src0_sel:WORD_0
	v_exp_f16_sdwa v52, v48 dst_sel:WORD_0 dst_unused:UNUSED_PAD src0_sel:WORD_0
	v_exp_f16_sdwa v53, v49 dst_sel:WORD_0 dst_unused:UNUSED_PAD src0_sel:WORD_0
	v_exp_f16_sdwa v50, v46 dst_sel:WORD_1 dst_unused:UNUSED_PRESERVE src0_sel:WORD_1
	v_exp_f16_sdwa v51, v47 dst_sel:WORD_1 dst_unused:UNUSED_PRESERVE src0_sel:WORD_1
	v_exp_f16_sdwa v52, v48 dst_sel:WORD_1 dst_unused:UNUSED_PRESERVE src0_sel:WORD_1
	v_exp_f16_sdwa v53, v49 dst_sel:WORD_1 dst_unused:UNUSED_PRESERVE src0_sel:WORD_1
	v_pk_add_f16 v46, v97, v114 neg_lo:[0,1] neg_hi:[0,1]
	v_pk_add_f16 v37, v37, v50
	v_pk_add_f16 v36, v36, v51
	v_pk_add_f16 v35, v35, v52
	v_pk_add_f16 v34, v34, v53
	v_pk_fma_f16 v22, v10, v50, v22
	v_pk_fma_f16 v23, v11, v51, v23
	v_pk_fma_f16 v24, v12, v52, v24
	v_pk_fma_f16 v25, v13, v53, v25
	v_pk_add_f16 v47, v96, v115 neg_lo:[0,1] neg_hi:[0,1]
	v_pk_add_f16 v48, v95, v116 neg_lo:[0,1] neg_hi:[0,1]
	v_pk_add_f16 v49, v94, v117 neg_lo:[0,1] neg_hi:[0,1]
	v_exp_f16_sdwa v50, v46 dst_sel:WORD_0 dst_unused:UNUSED_PAD src0_sel:WORD_0
	v_exp_f16_sdwa v51, v47 dst_sel:WORD_0 dst_unused:UNUSED_PAD src0_sel:WORD_0
	v_exp_f16_sdwa v52, v48 dst_sel:WORD_0 dst_unused:UNUSED_PAD src0_sel:WORD_0
	v_exp_f16_sdwa v53, v49 dst_sel:WORD_0 dst_unused:UNUSED_PAD src0_sel:WORD_0
	v_exp_f16_sdwa v50, v46 dst_sel:WORD_1 dst_unused:UNUSED_PRESERVE src0_sel:WORD_1
	v_exp_f16_sdwa v51, v47 dst_sel:WORD_1 dst_unused:UNUSED_PRESERVE src0_sel:WORD_1
	v_exp_f16_sdwa v52, v48 dst_sel:WORD_1 dst_unused:UNUSED_PRESERVE src0_sel:WORD_1
	v_exp_f16_sdwa v53, v49 dst_sel:WORD_1 dst_unused:UNUSED_PRESERVE src0_sel:WORD_1
	v_pk_add_f16 v46, v66, v114 neg_lo:[0,1] neg_hi:[0,1]
	v_pk_add_f16 v37, v37, v50
	v_pk_add_f16 v34, v34, v53
	v_pk_add_f16 v35, v35, v52
	v_pk_add_f16 v36, v36, v51
	v_pk_fma_f16 v25, v17, v53, v25
	v_pk_fma_f16 v24, v16, v52, v24
	v_pk_fma_f16 v23, v15, v51, v23
	v_pk_fma_f16 v22, v14, v50, v22
	v_pk_add_f16 v47, v67, v115 neg_lo:[0,1] neg_hi:[0,1]
	v_pk_add_f16 v48, v68, v116 neg_lo:[0,1] neg_hi:[0,1]
	v_pk_add_f16 v49, v69, v117 neg_lo:[0,1] neg_hi:[0,1]
	v_exp_f16_sdwa v50, v46 dst_sel:WORD_0 dst_unused:UNUSED_PAD src0_sel:WORD_0
	v_exp_f16_sdwa v51, v47 dst_sel:WORD_0 dst_unused:UNUSED_PAD src0_sel:WORD_0
	v_exp_f16_sdwa v52, v48 dst_sel:WORD_0 dst_unused:UNUSED_PAD src0_sel:WORD_0
	v_exp_f16_sdwa v53, v49 dst_sel:WORD_0 dst_unused:UNUSED_PAD src0_sel:WORD_0
	v_exp_f16_sdwa v50, v46 dst_sel:WORD_1 dst_unused:UNUSED_PRESERVE src0_sel:WORD_1
	v_exp_f16_sdwa v51, v47 dst_sel:WORD_1 dst_unused:UNUSED_PRESERVE src0_sel:WORD_1
	v_exp_f16_sdwa v52, v48 dst_sel:WORD_1 dst_unused:UNUSED_PRESERVE src0_sel:WORD_1
	v_exp_f16_sdwa v53, v49 dst_sel:WORD_1 dst_unused:UNUSED_PRESERVE src0_sel:WORD_1
	v_pk_add_f16 v46, v101, v114 neg_lo:[0,1] neg_hi:[0,1]
	v_pk_add_f16 v37, v37, v50
	v_pk_add_f16 v36, v36, v51
	v_pk_add_f16 v35, v35, v52
	v_pk_add_f16 v34, v34, v53
	v_pk_fma_f16 v22, v18, v50, v22
	v_pk_fma_f16 v23, v19, v51, v23
	v_pk_fma_f16 v24, v20, v52, v24
	v_pk_fma_f16 v25, v21, v53, v25
	v_pk_add_f16 v47, v100, v115 neg_lo:[0,1] neg_hi:[0,1]
	v_pk_add_f16 v48, v99, v116 neg_lo:[0,1] neg_hi:[0,1]
	v_pk_add_f16 v49, v98, v117 neg_lo:[0,1] neg_hi:[0,1]
	v_exp_f16_sdwa v50, v46 dst_sel:WORD_0 dst_unused:UNUSED_PAD src0_sel:WORD_0
	v_exp_f16_sdwa v51, v47 dst_sel:WORD_0 dst_unused:UNUSED_PAD src0_sel:WORD_0
	v_exp_f16_sdwa v52, v48 dst_sel:WORD_0 dst_unused:UNUSED_PAD src0_sel:WORD_0
	v_exp_f16_sdwa v53, v49 dst_sel:WORD_0 dst_unused:UNUSED_PAD src0_sel:WORD_0
	v_exp_f16_sdwa v50, v46 dst_sel:WORD_1 dst_unused:UNUSED_PRESERVE src0_sel:WORD_1
	v_exp_f16_sdwa v51, v47 dst_sel:WORD_1 dst_unused:UNUSED_PRESERVE src0_sel:WORD_1
	v_exp_f16_sdwa v52, v48 dst_sel:WORD_1 dst_unused:UNUSED_PRESERVE src0_sel:WORD_1
	v_exp_f16_sdwa v53, v49 dst_sel:WORD_1 dst_unused:UNUSED_PRESERVE src0_sel:WORD_1
	v_pk_add_f16 v46, v113, v114 neg_lo:[0,1] neg_hi:[0,1]
	v_pk_add_f16 v37, v37, v50
	v_pk_add_f16 v34, v34, v53
	v_pk_add_f16 v35, v35, v52
	v_pk_add_f16 v36, v36, v51
	v_pk_fma_f16 v25, v33, v53, v25
	v_pk_fma_f16 v24, v32, v52, v24
	v_pk_fma_f16 v23, v31, v51, v23
	v_pk_fma_f16 v22, v30, v50, v22
	v_pk_add_f16 v47, v112, v115 neg_lo:[0,1] neg_hi:[0,1]
	v_pk_add_f16 v48, v111, v116 neg_lo:[0,1] neg_hi:[0,1]
	v_pk_add_f16 v49, v110, v117 neg_lo:[0,1] neg_hi:[0,1]
	v_exp_f16_sdwa v50, v46 dst_sel:WORD_0 dst_unused:UNUSED_PAD src0_sel:WORD_0
	v_exp_f16_sdwa v51, v47 dst_sel:WORD_0 dst_unused:UNUSED_PAD src0_sel:WORD_0
	v_exp_f16_sdwa v52, v48 dst_sel:WORD_0 dst_unused:UNUSED_PAD src0_sel:WORD_0
	v_exp_f16_sdwa v53, v49 dst_sel:WORD_0 dst_unused:UNUSED_PAD src0_sel:WORD_0
	v_exp_f16_sdwa v50, v46 dst_sel:WORD_1 dst_unused:UNUSED_PRESERVE src0_sel:WORD_1
	v_exp_f16_sdwa v51, v47 dst_sel:WORD_1 dst_unused:UNUSED_PRESERVE src0_sel:WORD_1
	v_exp_f16_sdwa v52, v48 dst_sel:WORD_1 dst_unused:UNUSED_PRESERVE src0_sel:WORD_1
	v_exp_f16_sdwa v53, v49 dst_sel:WORD_1 dst_unused:UNUSED_PRESERVE src0_sel:WORD_1
	v_pk_add_f16 v46, v86, v114 neg_lo:[0,1] neg_hi:[0,1]
	v_pk_add_f16 v37, v37, v50
	v_pk_add_f16 v36, v36, v51
	v_pk_add_f16 v35, v35, v52
	v_pk_add_f16 v34, v34, v53
	v_pk_fma_f16 v22, v42, v50, v22
	v_pk_fma_f16 v23, v43, v51, v23
	v_pk_fma_f16 v24, v44, v52, v24
	v_pk_fma_f16 v25, v45, v53, v25
	v_pk_add_f16 v47, v87, v115 neg_lo:[0,1] neg_hi:[0,1]
	v_pk_add_f16 v48, v88, v116 neg_lo:[0,1] neg_hi:[0,1]
	v_pk_add_f16 v49, v89, v117 neg_lo:[0,1] neg_hi:[0,1]
	v_exp_f16_sdwa v50, v46 dst_sel:WORD_0 dst_unused:UNUSED_PAD src0_sel:WORD_0
	v_exp_f16_sdwa v51, v47 dst_sel:WORD_0 dst_unused:UNUSED_PAD src0_sel:WORD_0
	v_exp_f16_sdwa v52, v48 dst_sel:WORD_0 dst_unused:UNUSED_PAD src0_sel:WORD_0
	v_exp_f16_sdwa v53, v49 dst_sel:WORD_0 dst_unused:UNUSED_PAD src0_sel:WORD_0
	v_exp_f16_sdwa v50, v46 dst_sel:WORD_1 dst_unused:UNUSED_PRESERVE src0_sel:WORD_1
	v_exp_f16_sdwa v51, v47 dst_sel:WORD_1 dst_unused:UNUSED_PRESERVE src0_sel:WORD_1
	v_exp_f16_sdwa v52, v48 dst_sel:WORD_1 dst_unused:UNUSED_PRESERVE src0_sel:WORD_1
	v_exp_f16_sdwa v53, v49 dst_sel:WORD_1 dst_unused:UNUSED_PRESERVE src0_sel:WORD_1
	v_pk_add_f16 v37, v37, v50
	v_pk_add_f16 v36, v36, v51
	v_rcp_f16_e32 v46, v37
	v_rcp_f16_sdwa v37, v37 dst_sel:DWORD dst_unused:UNUSED_PAD src0_sel:WORD_1
	v_pk_add_f16 v35, v35, v52
	v_rcp_f16_e32 v47, v36
	v_rcp_f16_sdwa v36, v36 dst_sel:DWORD dst_unused:UNUSED_PAD src0_sel:WORD_1
	v_pk_add_f16 v34, v34, v53
	v_rcp_f16_e32 v48, v35
	v_rcp_f16_sdwa v35, v35 dst_sel:DWORD dst_unused:UNUSED_PAD src0_sel:WORD_1
	v_rcp_f16_e32 v49, v34
	v_rcp_f16_sdwa v34, v34 dst_sel:DWORD dst_unused:UNUSED_PAD src0_sel:WORD_1
	v_pk_fma_f16 v22, v62, v50, v22
	v_pack_b32_f16 v37, v46, v37
	v_pk_fma_f16 v23, v63, v51, v23
	v_pk_mul_f16 v57, v22, v37
	v_pack_b32_f16 v22, v47, v36
	v_pk_fma_f16 v24, v64, v52, v24
	v_pk_mul_f16 v56, v23, v22
	v_pack_b32_f16 v22, v48, v35
	v_pk_fma_f16 v25, v65, v53, v25
	v_pk_mul_f16 v55, v24, v22
	v_pack_b32_f16 v22, v49, v34
	v_pk_mul_f16 v54, v25, v22
	s_waitcnt vmcnt(0)
	v_pk_mul_f16 v22, v160, v146 op_sel_hi:[0,1]
	v_pk_mul_f16 v23, v160, v147 op_sel_hi:[0,1]
	v_pk_mul_f16 v24, v160, v148 op_sel_hi:[0,1]
	v_pk_mul_f16 v25, v160, v149 op_sel_hi:[0,1]
	v_pk_mul_f16 v46, v159, v146 op_sel_hi:[0,1]
	v_pk_mul_f16 v47, v159, v147 op_sel_hi:[0,1]
	v_pk_mul_f16 v48, v159, v148 op_sel_hi:[0,1]
	v_pk_mul_f16 v49, v159, v149 op_sel_hi:[0,1]
	v_pk_mul_f16 v34, v158, v146 op_sel_hi:[0,1]
	v_pk_mul_f16 v35, v158, v147 op_sel_hi:[0,1]
	v_pk_mul_f16 v36, v158, v148 op_sel_hi:[0,1]
	v_pk_mul_f16 v37, v158, v149 op_sel_hi:[0,1]
	v_pk_fma_f16 v29, v29, v149, v25
	v_pk_fma_f16 v28, v28, v148, v24
	v_pk_fma_f16 v27, v27, v147, v23
	v_pk_fma_f16 v26, v26, v146, v22
	v_pk_fma_f16 v41, v41, v149, v25
	v_pk_fma_f16 v40, v40, v148, v24
	v_pk_fma_f16 v39, v39, v147, v23
	v_pk_fma_f16 v38, v38, v146, v22
	v_pk_fma_f16 v25, v61, v149, v25
	v_pk_fma_f16 v24, v60, v148, v24
	v_pk_fma_f16 v23, v59, v147, v23
	v_pk_fma_f16 v22, v58, v146, v22
	v_pk_fma_f16 v66, v137, v149, v49
	v_pk_fma_f16 v67, v136, v148, v48
	v_pk_fma_f16 v68, v135, v147, v47
	v_pk_fma_f16 v69, v134, v146, v46
	v_pk_fma_f16 v70, v145, v149, v49
	v_pk_fma_f16 v71, v144, v148, v48
	v_pk_fma_f16 v72, v143, v147, v47
	v_pk_fma_f16 v73, v142, v146, v46
	v_pk_fma_f16 v9, v9, v149, v49
	v_pk_fma_f16 v8, v8, v148, v48
	v_pk_fma_f16 v7, v7, v147, v47
	v_pk_fma_f16 v6, v6, v146, v46
	v_pk_maximum3_f16 v46, v26, v38, v22
	v_pk_maximum3_f16 v47, v27, v39, v23
	v_pk_maximum3_f16 v48, v28, v40, v24
	v_pk_maximum3_f16 v49, v29, v41, v25
	v_pk_fma_f16 v50, v81, v149, v37
	v_pk_fma_f16 v51, v80, v148, v36
	v_pk_fma_f16 v52, v79, v147, v35
	v_pk_fma_f16 v53, v78, v146, v34
	v_pk_fma_f16 v58, v109, v149, v37
	v_pk_fma_f16 v59, v108, v148, v36
	v_pk_fma_f16 v60, v107, v147, v35
	v_pk_fma_f16 v61, v106, v146, v34
	v_pk_fma_f16 v37, v125, v149, v37
	v_pk_fma_f16 v36, v124, v148, v36
	v_pk_fma_f16 v35, v123, v147, v35
	v_pk_fma_f16 v34, v122, v146, v34
	v_pk_maximum3_f16 v79, v52, v60, v35
	v_pk_maximum3_f16 v80, v51, v59, v36
	v_pk_maximum3_f16 v81, v50, v58, v37
	v_pk_maximum3_f16 v86, v69, v73, v6
	v_pk_maximum3_f16 v87, v68, v72, v7
	v_pk_maximum3_f16 v78, v53, v61, v34
	v_pk_maximum3_f16 v88, v67, v71, v8
	v_pk_maximum3_f16 v89, v66, v70, v9
	v_pk_maximum3_f16 v46, v46, v78, v86
	v_pk_maximum3_f16 v47, v47, v79, v87
	v_pk_maximum3_f16 v48, v48, v80, v88
	v_pk_maximum3_f16 v49, v49, v81, v89
	s_nop 0
	v_pk_add_f16 v26, v26, v46 neg_lo:[0,1] neg_hi:[0,1]
	v_pk_add_f16 v27, v27, v47 neg_lo:[0,1] neg_hi:[0,1]
	v_pk_add_f16 v28, v28, v48 neg_lo:[0,1] neg_hi:[0,1]
	v_pk_add_f16 v29, v29, v49 neg_lo:[0,1] neg_hi:[0,1]
	v_pk_add_f16 v38, v38, v46 neg_lo:[0,1] neg_hi:[0,1]
	v_exp_f16_sdwa v78, v26 dst_sel:WORD_0 dst_unused:UNUSED_PAD src0_sel:WORD_0
	v_exp_f16_sdwa v79, v27 dst_sel:WORD_0 dst_unused:UNUSED_PAD src0_sel:WORD_0
	v_exp_f16_sdwa v80, v28 dst_sel:WORD_0 dst_unused:UNUSED_PAD src0_sel:WORD_0
	v_exp_f16_sdwa v81, v29 dst_sel:WORD_0 dst_unused:UNUSED_PAD src0_sel:WORD_0
	v_exp_f16_sdwa v78, v26 dst_sel:WORD_1 dst_unused:UNUSED_PRESERVE src0_sel:WORD_1
	v_exp_f16_sdwa v79, v27 dst_sel:WORD_1 dst_unused:UNUSED_PRESERVE src0_sel:WORD_1
	v_exp_f16_sdwa v80, v28 dst_sel:WORD_1 dst_unused:UNUSED_PRESERVE src0_sel:WORD_1
	v_exp_f16_sdwa v81, v29 dst_sel:WORD_1 dst_unused:UNUSED_PRESERVE src0_sel:WORD_1
	v_pk_add_f16 v39, v39, v47 neg_lo:[0,1] neg_hi:[0,1]
	v_pk_add_f16 v26, v78, 0
	v_pk_add_f16 v27, v79, 0
	v_pk_add_f16 v28, v80, 0
	v_pk_add_f16 v29, v81, 0
	v_pk_fma_f16 v10, v10, v78, 0
	v_pk_fma_f16 v11, v11, v79, 0
	v_pk_fma_f16 v12, v12, v80, 0
	v_pk_fma_f16 v13, v13, v81, 0
	v_pk_add_f16 v40, v40, v48 neg_lo:[0,1] neg_hi:[0,1]
	v_pk_add_f16 v41, v41, v49 neg_lo:[0,1] neg_hi:[0,1]
	v_pk_add_f16 v6, v6, v46 neg_lo:[0,1] neg_hi:[0,1]
	v_exp_f16_sdwa v78, v38 dst_sel:WORD_0 dst_unused:UNUSED_PAD src0_sel:WORD_0
	v_exp_f16_sdwa v79, v39 dst_sel:WORD_0 dst_unused:UNUSED_PAD src0_sel:WORD_0
	v_exp_f16_sdwa v80, v40 dst_sel:WORD_0 dst_unused:UNUSED_PAD src0_sel:WORD_0
	v_exp_f16_sdwa v81, v41 dst_sel:WORD_0 dst_unused:UNUSED_PAD src0_sel:WORD_0
	v_exp_f16_sdwa v78, v38 dst_sel:WORD_1 dst_unused:UNUSED_PRESERVE src0_sel:WORD_1
	v_exp_f16_sdwa v79, v39 dst_sel:WORD_1 dst_unused:UNUSED_PRESERVE src0_sel:WORD_1
	v_exp_f16_sdwa v80, v40 dst_sel:WORD_1 dst_unused:UNUSED_PRESERVE src0_sel:WORD_1
	v_exp_f16_sdwa v81, v41 dst_sel:WORD_1 dst_unused:UNUSED_PRESERVE src0_sel:WORD_1
	v_pk_add_f16 v7, v7, v47 neg_lo:[0,1] neg_hi:[0,1]
	v_pk_add_f16 v29, v29, v81
	v_pk_add_f16 v28, v28, v80
	v_pk_add_f16 v27, v27, v79
	v_pk_add_f16 v26, v26, v78
	v_pk_fma_f16 v13, v17, v81, v13
	v_pk_fma_f16 v12, v16, v80, v12
	v_pk_fma_f16 v11, v15, v79, v11
	v_pk_fma_f16 v10, v14, v78, v10
	v_pk_add_f16 v14, v22, v46 neg_lo:[0,1] neg_hi:[0,1]
	v_pk_add_f16 v15, v23, v47 neg_lo:[0,1] neg_hi:[0,1]
	v_pk_add_f16 v16, v24, v48 neg_lo:[0,1] neg_hi:[0,1]
	v_pk_add_f16 v17, v25, v49 neg_lo:[0,1] neg_hi:[0,1]
	v_pk_add_f16 v8, v8, v48 neg_lo:[0,1] neg_hi:[0,1]
	v_exp_f16_sdwa v22, v14 dst_sel:WORD_0 dst_unused:UNUSED_PAD src0_sel:WORD_0
	v_exp_f16_sdwa v23, v15 dst_sel:WORD_0 dst_unused:UNUSED_PAD src0_sel:WORD_0
	v_exp_f16_sdwa v24, v16 dst_sel:WORD_0 dst_unused:UNUSED_PAD src0_sel:WORD_0
	v_exp_f16_sdwa v25, v17 dst_sel:WORD_0 dst_unused:UNUSED_PAD src0_sel:WORD_0
	v_exp_f16_sdwa v22, v14 dst_sel:WORD_1 dst_unused:UNUSED_PRESERVE src0_sel:WORD_1
	v_exp_f16_sdwa v23, v15 dst_sel:WORD_1 dst_unused:UNUSED_PRESERVE src0_sel:WORD_1
	v_exp_f16_sdwa v24, v16 dst_sel:WORD_1 dst_unused:UNUSED_PRESERVE src0_sel:WORD_1
	v_exp_f16_sdwa v25, v17 dst_sel:WORD_1 dst_unused:UNUSED_PRESERVE src0_sel:WORD_1
	v_pk_add_f16 v9, v9, v49 neg_lo:[0,1] neg_hi:[0,1]
	v_pk_add_f16 v14, v26, v22
	v_pk_add_f16 v15, v27, v23
	v_pk_add_f16 v16, v28, v24
	v_pk_add_f16 v17, v29, v25
	v_pk_fma_f16 v10, v18, v22, v10
	v_pk_fma_f16 v11, v19, v23, v11
	v_pk_fma_f16 v12, v20, v24, v12
	v_pk_fma_f16 v13, v21, v25, v13
	v_pk_add_f16 v18, v53, v46 neg_lo:[0,1] neg_hi:[0,1]
	v_pk_add_f16 v19, v52, v47 neg_lo:[0,1] neg_hi:[0,1]
	v_pk_add_f16 v20, v51, v48 neg_lo:[0,1] neg_hi:[0,1]
	v_pk_add_f16 v21, v50, v49 neg_lo:[0,1] neg_hi:[0,1]
	v_exp_f16_sdwa v22, v18 dst_sel:WORD_0 dst_unused:UNUSED_PAD src0_sel:WORD_0
	v_exp_f16_sdwa v23, v19 dst_sel:WORD_0 dst_unused:UNUSED_PAD src0_sel:WORD_0
	v_exp_f16_sdwa v24, v20 dst_sel:WORD_0 dst_unused:UNUSED_PAD src0_sel:WORD_0
	v_exp_f16_sdwa v25, v21 dst_sel:WORD_0 dst_unused:UNUSED_PAD src0_sel:WORD_0
	v_exp_f16_sdwa v22, v18 dst_sel:WORD_1 dst_unused:UNUSED_PRESERVE src0_sel:WORD_1
	v_exp_f16_sdwa v23, v19 dst_sel:WORD_1 dst_unused:UNUSED_PRESERVE src0_sel:WORD_1
	v_exp_f16_sdwa v24, v20 dst_sel:WORD_1 dst_unused:UNUSED_PRESERVE src0_sel:WORD_1
	v_exp_f16_sdwa v25, v21 dst_sel:WORD_1 dst_unused:UNUSED_PRESERVE src0_sel:WORD_1
	v_pk_add_f16 v18, v61, v46 neg_lo:[0,1] neg_hi:[0,1]
	v_pk_add_f16 v17, v17, v25
	v_pk_add_f16 v16, v16, v24
	v_pk_add_f16 v15, v15, v23
	v_pk_add_f16 v14, v14, v22
	v_pk_fma_f16 v13, v33, v25, v13
	v_pk_fma_f16 v12, v32, v24, v12
	v_pk_fma_f16 v11, v31, v23, v11
	v_pk_fma_f16 v10, v30, v22, v10
	v_pk_add_f16 v19, v60, v47 neg_lo:[0,1] neg_hi:[0,1]
	v_pk_add_f16 v20, v59, v48 neg_lo:[0,1] neg_hi:[0,1]
	v_pk_add_f16 v21, v58, v49 neg_lo:[0,1] neg_hi:[0,1]
	v_exp_f16_sdwa v30, v6 dst_sel:WORD_0 dst_unused:UNUSED_PAD src0_sel:WORD_0
	v_exp_f16_sdwa v31, v7 dst_sel:WORD_0 dst_unused:UNUSED_PAD src0_sel:WORD_0
	v_exp_f16_sdwa v32, v8 dst_sel:WORD_0 dst_unused:UNUSED_PAD src0_sel:WORD_0
	v_exp_f16_sdwa v33, v9 dst_sel:WORD_0 dst_unused:UNUSED_PAD src0_sel:WORD_0
	v_exp_f16_sdwa v30, v6 dst_sel:WORD_1 dst_unused:UNUSED_PRESERVE src0_sel:WORD_1
	v_exp_f16_sdwa v31, v7 dst_sel:WORD_1 dst_unused:UNUSED_PRESERVE src0_sel:WORD_1
	v_exp_f16_sdwa v32, v8 dst_sel:WORD_1 dst_unused:UNUSED_PRESERVE src0_sel:WORD_1
	v_exp_f16_sdwa v33, v9 dst_sel:WORD_1 dst_unused:UNUSED_PRESERVE src0_sel:WORD_1
	v_exp_f16_sdwa v22, v18 dst_sel:WORD_0 dst_unused:UNUSED_PAD src0_sel:WORD_0
	v_exp_f16_sdwa v23, v19 dst_sel:WORD_0 dst_unused:UNUSED_PAD src0_sel:WORD_0
	v_exp_f16_sdwa v24, v20 dst_sel:WORD_0 dst_unused:UNUSED_PAD src0_sel:WORD_0
	v_exp_f16_sdwa v25, v21 dst_sel:WORD_0 dst_unused:UNUSED_PAD src0_sel:WORD_0
	v_exp_f16_sdwa v22, v18 dst_sel:WORD_1 dst_unused:UNUSED_PRESERVE src0_sel:WORD_1
	v_exp_f16_sdwa v23, v19 dst_sel:WORD_1 dst_unused:UNUSED_PRESERVE src0_sel:WORD_1
	v_exp_f16_sdwa v24, v20 dst_sel:WORD_1 dst_unused:UNUSED_PRESERVE src0_sel:WORD_1
	v_exp_f16_sdwa v25, v21 dst_sel:WORD_1 dst_unused:UNUSED_PRESERVE src0_sel:WORD_1
	v_pk_add_f16 v18, v34, v46 neg_lo:[0,1] neg_hi:[0,1]
	v_pk_add_f16 v14, v14, v22
	v_pk_add_f16 v15, v15, v23
	v_pk_add_f16 v16, v16, v24
	v_pk_add_f16 v17, v17, v25
	v_pk_fma_f16 v10, v42, v22, v10
	v_pk_fma_f16 v11, v43, v23, v11
	v_pk_fma_f16 v12, v44, v24, v12
	v_pk_fma_f16 v13, v45, v25, v13
	v_pk_add_f16 v19, v35, v47 neg_lo:[0,1] neg_hi:[0,1]
	v_pk_add_f16 v20, v36, v48 neg_lo:[0,1] neg_hi:[0,1]
	v_pk_add_f16 v21, v37, v49 neg_lo:[0,1] neg_hi:[0,1]
	v_exp_f16_sdwa v22, v18 dst_sel:WORD_0 dst_unused:UNUSED_PAD src0_sel:WORD_0
	v_exp_f16_sdwa v23, v19 dst_sel:WORD_0 dst_unused:UNUSED_PAD src0_sel:WORD_0
	v_exp_f16_sdwa v24, v20 dst_sel:WORD_0 dst_unused:UNUSED_PAD src0_sel:WORD_0
	v_exp_f16_sdwa v25, v21 dst_sel:WORD_0 dst_unused:UNUSED_PAD src0_sel:WORD_0
	v_exp_f16_sdwa v22, v18 dst_sel:WORD_1 dst_unused:UNUSED_PRESERVE src0_sel:WORD_1
	v_exp_f16_sdwa v23, v19 dst_sel:WORD_1 dst_unused:UNUSED_PRESERVE src0_sel:WORD_1
	v_exp_f16_sdwa v24, v20 dst_sel:WORD_1 dst_unused:UNUSED_PRESERVE src0_sel:WORD_1
	v_exp_f16_sdwa v25, v21 dst_sel:WORD_1 dst_unused:UNUSED_PRESERVE src0_sel:WORD_1
	v_pk_add_f16 v18, v69, v46 neg_lo:[0,1] neg_hi:[0,1]
	v_pk_add_f16 v17, v17, v25
	v_pk_add_f16 v16, v16, v24
	v_pk_add_f16 v15, v15, v23
	v_pk_add_f16 v14, v14, v22
	v_pk_fma_f16 v13, v65, v25, v13
	v_pk_fma_f16 v12, v64, v24, v12
	v_pk_fma_f16 v11, v63, v23, v11
	v_pk_fma_f16 v10, v62, v22, v10
	v_pk_add_f16 v19, v68, v47 neg_lo:[0,1] neg_hi:[0,1]
	v_pk_add_f16 v20, v67, v48 neg_lo:[0,1] neg_hi:[0,1]
	v_pk_add_f16 v21, v66, v49 neg_lo:[0,1] neg_hi:[0,1]
	v_exp_f16_sdwa v22, v18 dst_sel:WORD_0 dst_unused:UNUSED_PAD src0_sel:WORD_0
	v_exp_f16_sdwa v23, v19 dst_sel:WORD_0 dst_unused:UNUSED_PAD src0_sel:WORD_0
	v_exp_f16_sdwa v24, v20 dst_sel:WORD_0 dst_unused:UNUSED_PAD src0_sel:WORD_0
	v_exp_f16_sdwa v25, v21 dst_sel:WORD_0 dst_unused:UNUSED_PAD src0_sel:WORD_0
	v_exp_f16_sdwa v22, v18 dst_sel:WORD_1 dst_unused:UNUSED_PRESERVE src0_sel:WORD_1
	v_exp_f16_sdwa v23, v19 dst_sel:WORD_1 dst_unused:UNUSED_PRESERVE src0_sel:WORD_1
	v_exp_f16_sdwa v24, v20 dst_sel:WORD_1 dst_unused:UNUSED_PRESERVE src0_sel:WORD_1
	v_exp_f16_sdwa v25, v21 dst_sel:WORD_1 dst_unused:UNUSED_PRESERVE src0_sel:WORD_1
	v_pk_add_f16 v18, v73, v46 neg_lo:[0,1] neg_hi:[0,1]
	v_pk_add_f16 v14, v14, v22
	v_pk_add_f16 v15, v15, v23
	v_pk_add_f16 v16, v16, v24
	v_pk_add_f16 v17, v17, v25
	v_pk_fma_f16 v10, v82, v22, v10
	v_pk_fma_f16 v11, v83, v23, v11
	v_pk_fma_f16 v12, v84, v24, v12
	v_pk_fma_f16 v13, v85, v25, v13
	v_pk_add_f16 v19, v72, v47 neg_lo:[0,1] neg_hi:[0,1]
	v_pk_add_f16 v20, v71, v48 neg_lo:[0,1] neg_hi:[0,1]
	v_pk_add_f16 v21, v70, v49 neg_lo:[0,1] neg_hi:[0,1]
	v_exp_f16_sdwa v22, v18 dst_sel:WORD_0 dst_unused:UNUSED_PAD src0_sel:WORD_0
	v_exp_f16_sdwa v23, v19 dst_sel:WORD_0 dst_unused:UNUSED_PAD src0_sel:WORD_0
	v_exp_f16_sdwa v24, v20 dst_sel:WORD_0 dst_unused:UNUSED_PAD src0_sel:WORD_0
	v_exp_f16_sdwa v25, v21 dst_sel:WORD_0 dst_unused:UNUSED_PAD src0_sel:WORD_0
	v_exp_f16_sdwa v22, v18 dst_sel:WORD_1 dst_unused:UNUSED_PRESERVE src0_sel:WORD_1
	v_exp_f16_sdwa v23, v19 dst_sel:WORD_1 dst_unused:UNUSED_PRESERVE src0_sel:WORD_1
	v_exp_f16_sdwa v24, v20 dst_sel:WORD_1 dst_unused:UNUSED_PRESERVE src0_sel:WORD_1
	v_exp_f16_sdwa v25, v21 dst_sel:WORD_1 dst_unused:UNUSED_PRESERVE src0_sel:WORD_1
	s_nop 0
	v_pk_add_f16 v17, v17, v25
	v_pk_add_f16 v16, v16, v24
	v_pk_add_f16 v15, v15, v23
	v_pk_add_f16 v14, v14, v22
	v_pk_fma_f16 v21, v105, v25, v13
	v_pk_fma_f16 v20, v104, v24, v12
	v_pk_fma_f16 v19, v103, v23, v11
	v_pk_fma_f16 v18, v102, v22, v10
	v_mov_b32_e32 v13, v5
	v_mov_b32_e32 v12, v4
	v_mov_b32_e32 v11, v3
	v_mov_b32_e32 v10, v2
.LBB4_80:
	v_lshlrev_b64 v[6:7], 9, v[168:169]
	v_or_b32_e32 v6, v6, v198
	v_lshl_add_u64 v[2:3], s[20:21], 0, v[6:7]
	global_load_dwordx4 v[2:5], v[2:3], off nt
	v_lshl_add_u64 v[6:7], s[22:23], 0, v[6:7]
	global_load_dwordx4 v[6:9], v[6:7], off nt
	v_add_u32_e32 v168, v185, v199
	v_lshlrev_b64 v[26:27], 9, v[168:169]
	v_or_b32_e32 v26, v26, v198
	v_lshl_add_u64 v[22:23], s[20:21], 0, v[26:27]
	global_load_dwordx4 v[22:25], v[22:23], off nt
	v_lshl_add_u64 v[26:27], s[22:23], 0, v[26:27]
	global_load_dwordx4 v[26:29], v[26:27], off nt
	v_pk_add_f16 v17, v17, v33
	v_pk_add_f16 v16, v16, v32
	v_pk_add_f16 v15, v15, v31
	v_pk_add_f16 v14, v14, v30
	v_pk_fma_f16 v42, v13, v33, v21
	v_pk_fma_f16 v43, v12, v32, v20
	v_rcp_f16_e32 v12, v14
	v_rcp_f16_sdwa v13, v14 dst_sel:DWORD dst_unused:UNUSED_PAD src0_sel:WORD_1
	v_rcp_f16_e32 v14, v15
	v_rcp_f16_sdwa v15, v15 dst_sel:DWORD dst_unused:UNUSED_PAD src0_sel:WORD_1
	v_rcp_f16_e32 v46, v16
	v_rcp_f16_sdwa v16, v16 dst_sel:DWORD dst_unused:UNUSED_PAD src0_sel:WORD_1
	v_rcp_f16_e32 v47, v17
	v_rcp_f16_sdwa v17, v17 dst_sel:DWORD dst_unused:UNUSED_PAD src0_sel:WORD_1
	v_add_u32_e32 v168, v187, v199
	v_pk_fma_f16 v44, v10, v30, v18
	v_pk_fma_f16 v45, v11, v31, v19
	v_lshlrev_b64 v[10:11], 9, v[168:169]
	v_or_b32_e32 v10, v10, v198
	v_lshl_add_u64 v[38:39], s[20:21], 0, v[10:11]
	v_lshl_add_u64 v[40:41], s[22:23], 0, v[10:11]
	v_pack_b32_f16 v48, v14, v15
	v_pack_b32_f16 v49, v12, v13
	v_pack_b32_f16 v46, v46, v16
	v_pack_b32_f16 v47, v47, v17
	global_load_dwordx4 v[10:13], v[38:39], off nt
	global_load_dwordx4 v[14:17], v[40:41], off nt
	v_cvt_f32_f16_sdwa v21, v139 dst_sel:DWORD dst_unused:UNUSED_PAD src0_sel:WORD_1
	v_cvt_f32_f16_e32 v20, v139
	v_cvt_f32_f16_sdwa v19, v138 dst_sel:DWORD dst_unused:UNUSED_PAD src0_sel:WORD_1
	v_cvt_f32_f16_e32 v18, v138
	v_cvt_f32_f16_sdwa v33, v141 dst_sel:DWORD dst_unused:UNUSED_PAD src0_sel:WORD_1
	v_cvt_f32_f16_e32 v32, v141
	v_pk_mul_f16 v58, v43, v46
	v_pk_mul_f16 v59, v42, v47
	v_cvt_f32_f16_sdwa v31, v140 dst_sel:DWORD dst_unused:UNUSED_PAD src0_sel:WORD_1
	v_cvt_f32_f16_e32 v30, v140
	v_pk_mul_f16 v52, v45, v48
	v_pk_mul_f16 v53, v44, v49
	v_add_u32_e32 v168, v190, v199
	v_lshlrev_b64 v[36:37], 9, v[168:169]
	v_or_b32_e32 v36, v36, v198
	v_lshl_or_b32 v50, s46, 6, v178
	v_lshlrev_b32_e32 v51, 9, v50
	v_add_u32_e32 v203, v184, v51
	v_cvt_f32_f16_sdwa v35, v77 dst_sel:DWORD dst_unused:UNUSED_PAD src0_sel:WORD_1
	v_cvt_f32_f16_e32 v34, v77
	v_add_lshl_u32 v202, v188, v50, 9
	s_mov_b64 s[4:5], -1
	s_and_b64 vcc, exec, s[26:27]
	s_waitcnt vmcnt(5)
	v_cvt_f32_f16_e32 v38, v2
	v_cvt_f32_f16_sdwa v39, v2 dst_sel:DWORD dst_unused:UNUSED_PAD src0_sel:WORD_1
	v_cvt_f32_f16_e32 v2, v3
	v_cvt_f32_f16_sdwa v3, v3 dst_sel:DWORD dst_unused:UNUSED_PAD src0_sel:WORD_1
	s_waitcnt vmcnt(4)
	v_cvt_f32_f16_e32 v40, v6
	v_cvt_f32_f16_sdwa v41, v6 dst_sel:DWORD dst_unused:UNUSED_PAD src0_sel:WORD_1
	v_cvt_f32_f16_e32 v6, v7
	v_cvt_f32_f16_sdwa v7, v7 dst_sel:DWORD dst_unused:UNUSED_PAD src0_sel:WORD_1
	v_cvt_f32_f16_e32 v42, v4
	v_cvt_f32_f16_sdwa v43, v4 dst_sel:DWORD dst_unused:UNUSED_PAD src0_sel:WORD_1
	v_cvt_f32_f16_e32 v4, v5
	v_cvt_f32_f16_sdwa v5, v5 dst_sel:DWORD dst_unused:UNUSED_PAD src0_sel:WORD_1
	v_cvt_f32_f16_e32 v44, v8
	v_cvt_f32_f16_sdwa v45, v8 dst_sel:DWORD dst_unused:UNUSED_PAD src0_sel:WORD_1
	v_cvt_f32_f16_e32 v8, v9
	v_cvt_f32_f16_sdwa v9, v9 dst_sel:DWORD dst_unused:UNUSED_PAD src0_sel:WORD_1
	v_pk_add_f32 v[2:3], v[20:21], v[2:3]
	v_pk_add_f32 v[18:19], v[18:19], v[38:39]
	v_pk_add_f32 v[4:5], v[32:33], v[4:5]
	v_pk_add_f32 v[6:7], v[2:3], v[6:7]
	v_pk_add_f32 v[20:21], v[30:31], v[42:43]
	v_pk_add_f32 v[18:19], v[18:19], v[40:41]
	v_pk_add_f32 v[8:9], v[4:5], v[8:9]
	v_cvt_pk_f16_f32 v3, v6, v7
	v_lshl_add_u64 v[6:7], s[20:21], 0, v[36:37]
	v_pk_add_f32 v[20:21], v[20:21], v[44:45]
	v_cvt_pk_f16_f32 v2, v18, v19
	v_cvt_pk_f16_f32 v5, v8, v9
	global_load_dwordx4 v[6:9], v[6:7], off nt
	v_lshl_add_u64 v[18:19], s[22:23], 0, v[36:37]
	v_cvt_pk_f16_f32 v4, v20, v21
	global_load_dwordx4 v[18:21], v[18:19], off nt
	s_waitcnt vmcnt(5)
	v_cvt_f32_f16_e32 v46, v22
	v_cvt_f32_f16_sdwa v47, v22 dst_sel:DWORD dst_unused:UNUSED_PAD src0_sel:WORD_1
	ds_write_b128 v203, v[2:5]
	v_cvt_f32_f16_sdwa v5, v76 dst_sel:DWORD dst_unused:UNUSED_PAD src0_sel:WORD_1
	v_cvt_f32_f16_e32 v4, v76
	v_cvt_f32_f16_e32 v22, v23
	v_cvt_f32_f16_sdwa v23, v23 dst_sel:DWORD dst_unused:UNUSED_PAD src0_sel:WORD_1
	s_waitcnt vmcnt(4)
	v_cvt_f32_f16_e32 v48, v26
	v_cvt_f32_f16_sdwa v49, v26 dst_sel:DWORD dst_unused:UNUSED_PAD src0_sel:WORD_1
	v_cvt_f32_f16_e32 v26, v27
	v_cvt_f32_f16_sdwa v27, v27 dst_sel:DWORD dst_unused:UNUSED_PAD src0_sel:WORD_1
	v_cvt_f32_f16_sdwa v31, v75 dst_sel:DWORD dst_unused:UNUSED_PAD src0_sel:WORD_1
	v_cvt_f32_f16_e32 v30, v75
	v_cvt_f32_f16_e32 v32, v24
	v_cvt_f32_f16_sdwa v33, v24 dst_sel:DWORD dst_unused:UNUSED_PAD src0_sel:WORD_1
	v_pk_add_f32 v[4:5], v[4:5], v[22:23]
	v_cvt_f32_f16_e32 v22, v28
	v_pk_add_f32 v[4:5], v[4:5], v[26:27]
	v_cvt_f32_f16_sdwa v23, v28 dst_sel:DWORD dst_unused:UNUSED_PAD src0_sel:WORD_1
	v_cvt_f32_f16_sdwa v27, v74 dst_sel:DWORD dst_unused:UNUSED_PAD src0_sel:WORD_1
	v_cvt_f32_f16_e32 v26, v74
	v_cvt_f32_f16_e32 v24, v25
	v_cvt_f32_f16_sdwa v25, v25 dst_sel:DWORD dst_unused:UNUSED_PAD src0_sel:WORD_1
	v_pk_add_f32 v[2:3], v[34:35], v[46:47]
	v_cvt_f32_f16_e32 v28, v29
	v_cvt_f32_f16_sdwa v29, v29 dst_sel:DWORD dst_unused:UNUSED_PAD src0_sel:WORD_1
	v_pk_add_f32 v[2:3], v[2:3], v[48:49]
	s_nop 0
	v_cvt_pk_f16_f32 v2, v2, v3
	v_cvt_pk_f16_f32 v3, v4, v5
	v_pk_add_f32 v[4:5], v[30:31], v[32:33]
	s_nop 0
	v_pk_add_f32 v[4:5], v[4:5], v[22:23]
	v_pk_add_f32 v[22:23], v[26:27], v[24:25]
	v_cvt_pk_f16_f32 v4, v4, v5
	v_pk_add_f32 v[22:23], v[22:23], v[28:29]
	s_waitcnt vmcnt(3)
	v_cvt_f32_f16_e32 v24, v10
	v_cvt_pk_f16_f32 v5, v22, v23
	v_add_u32_e32 v22, v186, v50
	v_lshlrev_b32_e32 v204, 9, v22
	v_bitop3_b32 v22, v22, v179, 15 bitop3:0x6c
	v_lshlrev_b32_e32 v205, 4, v22
	v_cvt_f32_f16_sdwa v25, v10 dst_sel:DWORD dst_unused:UNUSED_PAD src0_sel:WORD_1
	v_or_b32_e32 v10, v205, v204
	v_cvt_f32_f16_sdwa v23, v57 dst_sel:DWORD dst_unused:UNUSED_PAD src0_sel:WORD_1
	v_cvt_f32_f16_e32 v22, v57
	ds_write_b128 v10, v[2:5]
	v_cvt_f32_f16_sdwa v5, v56 dst_sel:DWORD dst_unused:UNUSED_PAD src0_sel:WORD_1
	v_cvt_f32_f16_e32 v4, v56
	v_cvt_f32_f16_e32 v10, v11
	v_cvt_f32_f16_sdwa v11, v11 dst_sel:DWORD dst_unused:UNUSED_PAD src0_sel:WORD_1
	s_waitcnt vmcnt(2)
	v_cvt_f32_f16_e32 v26, v14
	v_cvt_f32_f16_sdwa v27, v14 dst_sel:DWORD dst_unused:UNUSED_PAD src0_sel:WORD_1
	v_cvt_f32_f16_e32 v14, v15
	v_cvt_f32_f16_sdwa v15, v15 dst_sel:DWORD dst_unused:UNUSED_PAD src0_sel:WORD_1
	v_pk_add_f32 v[2:3], v[22:23], v[24:25]
	v_cvt_f32_f16_sdwa v23, v55 dst_sel:DWORD dst_unused:UNUSED_PAD src0_sel:WORD_1
	v_cvt_f32_f16_e32 v22, v55
	v_cvt_f32_f16_e32 v24, v12
	v_cvt_f32_f16_sdwa v25, v12 dst_sel:DWORD dst_unused:UNUSED_PAD src0_sel:WORD_1
	v_pk_add_f32 v[4:5], v[4:5], v[10:11]
	v_cvt_f32_f16_e32 v10, v16
	v_pk_add_f32 v[4:5], v[4:5], v[14:15]
	v_cvt_f32_f16_sdwa v11, v16 dst_sel:DWORD dst_unused:UNUSED_PAD src0_sel:WORD_1
	v_cvt_f32_f16_sdwa v15, v54 dst_sel:DWORD dst_unused:UNUSED_PAD src0_sel:WORD_1
	v_cvt_f32_f16_e32 v14, v54
	v_cvt_f32_f16_e32 v12, v13
	v_cvt_f32_f16_sdwa v13, v13 dst_sel:DWORD dst_unused:UNUSED_PAD src0_sel:WORD_1
	v_cvt_f32_f16_e32 v16, v17
	v_cvt_f32_f16_sdwa v17, v17 dst_sel:DWORD dst_unused:UNUSED_PAD src0_sel:WORD_1
	v_pk_add_f32 v[2:3], v[2:3], v[26:27]
	s_nop 0
	v_cvt_pk_f16_f32 v2, v2, v3
	v_cvt_pk_f16_f32 v3, v4, v5
	v_pk_add_f32 v[4:5], v[22:23], v[24:25]
	s_nop 0
	v_pk_add_f32 v[4:5], v[4:5], v[10:11]
	v_pk_add_f32 v[10:11], v[14:15], v[12:13]
	v_cvt_pk_f16_f32 v4, v4, v5
	v_pk_add_f32 v[10:11], v[10:11], v[16:17]
	s_waitcnt vmcnt(1)
	v_cvt_f32_f16_e32 v12, v6
	v_cvt_pk_f16_f32 v5, v10, v11
	v_cvt_f32_f16_e32 v10, v53
	v_cvt_f32_f16_sdwa v11, v53 dst_sel:DWORD dst_unused:UNUSED_PAD src0_sel:WORD_1
	v_cvt_f32_f16_sdwa v13, v6 dst_sel:DWORD dst_unused:UNUSED_PAD src0_sel:WORD_1
	s_waitcnt vmcnt(0)
	v_cvt_f32_f16_e32 v14, v18
	v_cvt_f32_f16_sdwa v15, v18 dst_sel:DWORD dst_unused:UNUSED_PAD src0_sel:WORD_1
	v_or_b32_e32 v6, v189, v202
	ds_write_b128 v6, v[2:5]
	v_cvt_f32_f16_e32 v4, v52
	v_cvt_f32_f16_sdwa v5, v52 dst_sel:DWORD dst_unused:UNUSED_PAD src0_sel:WORD_1
	v_cvt_f32_f16_e32 v6, v7
	v_cvt_f32_f16_sdwa v7, v7 dst_sel:DWORD dst_unused:UNUSED_PAD src0_sel:WORD_1
	v_pk_add_f32 v[2:3], v[10:11], v[12:13]
	v_cvt_f32_f16_e32 v10, v19
	v_cvt_f32_f16_sdwa v11, v19 dst_sel:DWORD dst_unused:UNUSED_PAD src0_sel:WORD_1
	v_pk_add_f32 v[2:3], v[2:3], v[14:15]
	v_cvt_f32_f16_e32 v12, v58
	v_cvt_f32_f16_sdwa v13, v58 dst_sel:DWORD dst_unused:UNUSED_PAD src0_sel:WORD_1
	v_cvt_f32_f16_e32 v14, v8
	v_cvt_f32_f16_sdwa v15, v8 dst_sel:DWORD dst_unused:UNUSED_PAD src0_sel:WORD_1
	v_pk_add_f32 v[4:5], v[4:5], v[6:7]
	v_cvt_f32_f16_e32 v6, v20
	v_pk_add_f32 v[4:5], v[4:5], v[10:11]
	v_cvt_f32_f16_sdwa v7, v20 dst_sel:DWORD dst_unused:UNUSED_PAD src0_sel:WORD_1
	v_cvt_f32_f16_e32 v10, v59
	v_cvt_f32_f16_sdwa v11, v59 dst_sel:DWORD dst_unused:UNUSED_PAD src0_sel:WORD_1
	v_cvt_f32_f16_e32 v8, v9
	v_cvt_f32_f16_sdwa v9, v9 dst_sel:DWORD dst_unused:UNUSED_PAD src0_sel:WORD_1
	v_cvt_pk_f16_f32 v2, v2, v3
	v_cvt_pk_f16_f32 v3, v4, v5
	v_pk_add_f32 v[4:5], v[12:13], v[14:15]
	v_cvt_f32_f16_e32 v12, v21
	v_cvt_f32_f16_sdwa v13, v21 dst_sel:DWORD dst_unused:UNUSED_PAD src0_sel:WORD_1
	v_pk_add_f32 v[4:5], v[4:5], v[6:7]
	v_pk_add_f32 v[6:7], v[10:11], v[8:9]
	v_cvt_pk_f16_f32 v4, v4, v5
	v_pk_add_f32 v[6:7], v[6:7], v[12:13]
	s_nop 0
	v_cvt_pk_f16_f32 v5, v6, v7
	v_add_lshl_u32 v6, v191, v50, 9
	v_add_u32_e32 v168, v192, v6
	ds_write_b128 v168, v[2:5]
	global_load_dwordx4 v[2:5], v[174:175], off
	global_load_dwordx4 v[8:11], v[176:177], off
	global_load_dwordx4 v[12:15], v[174:175], off offset:16
	global_load_dwordx4 v[16:19], v[176:177], off offset:16
	s_cbranch_vccz .LBB4_118
	global_load_dwordx3 v[154:156], v169, s[18:19]
	s_mov_b32 s14, s38
	s_mov_b32 s15, s39
	v_cmp_lt_u32_e64 s[64:65], 0, v199
	v_cmp_gt_u32_e64 s[66:67], 63, v199
	v_cmp_lt_u32_e64 s[68:69], 0, v180
	v_cmp_gt_u32_e64 s[70:71], 60, v180
	buffer_load_dwordx4 v[210:213], v200, s[12:15], 0 offen nt
	s_and_b64 s[72:73], s[68:69], s[64:65]
	s_and_b64 s[74:75], s[68:69], s[66:67]
	s_and_b64 s[76:77], s[70:71], s[64:65]
	s_and_b64 s[78:79], s[70:71], s[66:67]
	v_add_u32_e32 v245, 0xfffe7c00, v200
	v_add_u32_e32 v246, 0xfffe8000, v200
	s_mov_b64 exec, s[72:73]
	buffer_load_dwordx4 v[122:125], v245, s[12:15], 0 offen
	buffer_load_dwordx4 v[82:85], v245, s[12:15], 0 offen offset:512
	s_mov_b64 exec, -1
	s_mov_b64 exec, s[68:69]
	buffer_load_dwordx4 v[138:141], v246, s[12:15], 0 offen offset:512
	buffer_load_dwordx4 v[106:109], v246, s[12:15], 0 offen offset:1024
	s_mov_b64 exec, -1
	s_mov_b64 exec, s[74:75]
	buffer_load_dwordx4 v[146:149], v246, s[12:15], 0 offen offset:2048
	buffer_load_dwordx4 v[126:129], v246, s[12:15], 0 offen offset:2560
	s_mov_b64 exec, -1
	v_add_u32_e32 v245, 0xfffffc00, v200
	s_mov_b64 exec, s[64:65]
	buffer_load_dwordx4 v[94:97], v245, s[12:15], 0 offen
	buffer_load_dwordx4 v[54:57], v245, s[12:15], 0 offen offset:512
	s_mov_b64 exec, -1
	buffer_load_dwordx4 v[118:121], v200, s[12:15], 0 offen offset:512
	buffer_load_dwordx4 v[74:77], v200, s[12:15], 0 offen offset:1024
	s_mov_b64 exec, s[66:67]
	buffer_load_dwordx4 v[134:137], v200, s[12:15], 0 offen offset:2048
	buffer_load_dwordx4 v[98:101], v200, s[12:15], 0 offen offset:2560
	s_mov_b64 exec, -1
	v_add_u32_e32 v245, 0x17c00, v200
	v_add_u32_e32 v246, 0x18000, v200
	s_mov_b64 exec, s[64:65]
	buffer_load_dwordx4 v[62:65], v245, s[12:15], 0 offen
	buffer_load_dwordx4 v[30:33], v245, s[12:15], 0 offen offset:512
	s_mov_b64 exec, -1
	buffer_load_dwordx4 v[78:81], v246, s[12:15], 0 offen offset:512
	buffer_load_dwordx4 v[42:45], v246, s[12:15], 0 offen offset:1024
	s_mov_b64 exec, s[66:67]
	buffer_load_dwordx4 v[102:105], v246, s[12:15], 0 offen offset:2048
	buffer_load_dwordx4 v[58:61], v246, s[12:15], 0 offen offset:2560
	s_mov_b64 exec, -1
	v_add_u32_e32 v245, 0x18000, v200
	buffer_load_dwordx4 v[162:165], v245, s[12:15], 0 offen nt
	v_add_u32_e32 v246, 0x30000, v200
	buffer_load_dwordx4 v[158:161], v246, s[12:15], 0 offen nt
	v_add_u32_e32 v245, 0x2fc00, v200
	v_add_u32_e32 v246, 0x30000, v200
	v_add_u32_e32 v247, 0x47c00, v200
	v_add_u32_e32 v248, 0x48000, v200
	v_add_u32_e32 v249, 0x5fc00, v200
	v_add_u32_e32 v250, 0x60000, v200
	s_waitcnt vmcnt(22)
	v_cvt_pk_f16_f32 v6, v2, v3
	v_cvt_pk_f16_f32 v2, v8, v9
	v_cvt_pk_f16_f32 v7, v4, v5
	v_cvt_pk_f16_f32 v3, v10, v11
	v_cvt_pk_f16_f32 v8, v12, v13
	v_cvt_pk_f16_f32 v4, v16, v17
	v_cvt_pk_f16_f32 v9, v14, v15
	v_cvt_pk_f16_f32 v5, v18, v19
	s_not_b64 exec, s[72:73]
	s_cbranch_execz .Lmyf_C3_0
	v_mov_b32_e32 v122, v6
	v_mov_b32_e32 v123, v7
	v_mov_b32_e32 v124, v8
	v_mov_b32_e32 v125, v9
	v_mov_b32_e32 v82, v2
	v_mov_b32_e32 v83, v3
	v_mov_b32_e32 v84, v4
	v_mov_b32_e32 v85, v5

.Lmyf_C3_7:
	s_mov_b64 exec, -1
	s_waitcnt vmcnt(21)
	v_cvt_f16_f32_e32 v206, v155
	v_cvt_f16_f32_e32 v208, v154
	v_cvt_f16_f32_e32 v207, v156
	v_add_u32_e32 v251, 0x48000, v200
	buffer_load_dwordx4 v[154:157], v251, s[12:15], 0 offen nt
	s_mov_b64 s[4:5], 0
	s_waitcnt vmcnt(3)
	v_pk_mul_f16 v216, v208, v213 op_sel_hi:[0,1]
	v_pk_mul_f16 v220, v206, v213 op_sel_hi:[0,1]
	v_pk_mul_f16 v224, v207, v213 op_sel_hi:[0,1]
	v_pk_mul_f16 v209, v208, v210 op_sel_hi:[0,1]
	v_pk_mul_f16 v214, v208, v211 op_sel_hi:[0,1]
	v_pk_mul_f16 v215, v208, v212 op_sel_hi:[0,1]
	v_pk_mul_f16 v217, v206, v210 op_sel_hi:[0,1]
	s_mov_b64 exec, s[64:65]
	buffer_load_dwordx4 v[34:37], v245, s[12:15], 0 offen
	buffer_load_dwordx4 v[18:21], v245, s[12:15], 0 offen offset:512
	s_mov_b64 exec, -1
	v_pk_mul_f16 v218, v206, v211 op_sel_hi:[0,1]
	v_pk_mul_f16 v219, v206, v212 op_sel_hi:[0,1]
	v_pk_mul_f16 v221, v207, v210 op_sel_hi:[0,1]
	v_pk_mul_f16 v222, v207, v211 op_sel_hi:[0,1]
	v_pk_mul_f16 v223, v207, v212 op_sel_hi:[0,1]
	v_pk_fma_f16 v125, v125, v213, v216
	v_pk_fma_f16 v141, v141, v213, v220
	v_pk_fma_f16 v149, v149, v213, v224
	v_pk_fma_f16 v225, v97, v213, v216
	v_pk_fma_f16 v229, v121, v213, v220
	v_pk_fma_f16 v233, v137, v213, v224
	v_pk_fma_f16 v216, v65, v213, v216
	v_pk_fma_f16 v220, v81, v213, v220
	buffer_load_dwordx4 v[46:49], v246, s[12:15], 0 offen offset:512
	buffer_load_dwordx4 v[22:25], v246, s[12:15], 0 offen offset:1024
	v_pk_fma_f16 v213, v105, v213, v224
	v_pk_maximum3_f16 v224, v125, v141, v149
	v_pk_fma_f16 v124, v124, v212, v215
	v_pk_fma_f16 v123, v123, v211, v214
	v_pk_fma_f16 v122, v122, v210, v209
	v_pk_fma_f16 v140, v140, v212, v219
	v_pk_fma_f16 v139, v139, v211, v218
	v_pk_fma_f16 v138, v138, v210, v217
	v_pk_fma_f16 v148, v148, v212, v223
	v_pk_fma_f16 v147, v147, v211, v222
	v_pk_fma_f16 v146, v146, v210, v221
	v_pk_fma_f16 v226, v96, v212, v215
	v_pk_fma_f16 v227, v95, v211, v214
	v_pk_fma_f16 v228, v94, v210, v209
	v_pk_fma_f16 v230, v120, v212, v219
	v_pk_fma_f16 v231, v119, v211, v218
	s_mov_b64 exec, s[66:67]
	buffer_load_dwordx4 v[66:69], v246, s[12:15], 0 offen offset:2048
	buffer_load_dwordx4 v[26:29], v246, s[12:15], 0 offen offset:2560
	s_mov_b64 exec, -1
	v_pk_fma_f16 v232, v118, v210, v217
	v_pk_fma_f16 v234, v136, v212, v223
	v_pk_fma_f16 v235, v135, v211, v222
	v_pk_fma_f16 v236, v134, v210, v221
	v_pk_fma_f16 v215, v64, v212, v215
	v_pk_fma_f16 v214, v63, v211, v214
	v_pk_fma_f16 v209, v62, v210, v209
	v_pk_fma_f16 v219, v80, v212, v219
	v_pk_fma_f16 v218, v79, v211, v218
	v_pk_fma_f16 v217, v78, v210, v217
	v_pk_fma_f16 v212, v104, v212, v223
	v_pk_fma_f16 v211, v103, v211, v222
	v_pk_fma_f16 v210, v102, v210, v221
	v_pk_maximum3_f16 v221, v122, v138, v146
	v_pk_maximum3_f16 v222, v123, v139, v147
	v_pk_maximum3_f16 v223, v124, v140, v148
	v_pk_maximum3_f16 v240, v225, v229, v233
	v_pk_maximum3_f16 v244, v216, v220, v213
	v_pk_maximum3_f16 v237, v228, v232, v236
	v_pk_maximum3_f16 v238, v227, v231, v235
	v_pk_maximum3_f16 v239, v226, v230, v234
	v_pk_maximum3_f16 v241, v209, v217, v210
	v_pk_maximum3_f16 v242, v214, v218, v211
	v_pk_maximum3_f16 v224, v224, v240, v244
	v_pk_maximum3_f16 v243, v215, v219, v212
	v_pk_maximum3_f16 v221, v221, v237, v241
	v_pk_maximum3_f16 v222, v222, v238, v242
	v_pk_maximum3_f16 v223, v223, v239, v243
	v_pk_add_f16 v125, v125, v224 neg_lo:[0,1] neg_hi:[0,1]
	s_mov_b64 exec, s[64:65]
	buffer_load_dwordx4 v[86:89], v247, s[12:15], 0 offen
	buffer_load_dwordx4 v[38:41], v247, s[12:15], 0 offen offset:512
	s_mov_b64 exec, -1
	v_pk_add_f16 v122, v122, v221 neg_lo:[0,1] neg_hi:[0,1]
	v_pk_add_f16 v123, v123, v222 neg_lo:[0,1] neg_hi:[0,1]
	v_pk_add_f16 v124, v124, v223 neg_lo:[0,1] neg_hi:[0,1]
	v_pk_add_f16 v138, v138, v221 neg_lo:[0,1] neg_hi:[0,1]
	v_exp_f16_sdwa v237, v122 dst_sel:WORD_0 dst_unused:UNUSED_PAD src0_sel:WORD_0
	v_exp_f16_sdwa v238, v123 dst_sel:WORD_0 dst_unused:UNUSED_PAD src0_sel:WORD_0
	v_exp_f16_sdwa v239, v124 dst_sel:WORD_0 dst_unused:UNUSED_PAD src0_sel:WORD_0
	v_exp_f16_sdwa v240, v125 dst_sel:WORD_0 dst_unused:UNUSED_PAD src0_sel:WORD_0
	v_exp_f16_sdwa v237, v122 dst_sel:WORD_1 dst_unused:UNUSED_PRESERVE src0_sel:WORD_1
	v_exp_f16_sdwa v238, v123 dst_sel:WORD_1 dst_unused:UNUSED_PRESERVE src0_sel:WORD_1
	v_exp_f16_sdwa v239, v124 dst_sel:WORD_1 dst_unused:UNUSED_PRESERVE src0_sel:WORD_1
	v_exp_f16_sdwa v240, v125 dst_sel:WORD_1 dst_unused:UNUSED_PRESERVE src0_sel:WORD_1
	v_pk_add_f16 v139, v139, v222 neg_lo:[0,1] neg_hi:[0,1]
	v_pk_add_f16 v125, v237, 0
	v_pk_fma_f16 v85, v85, v240, 0
	v_pk_add_f16 v122, v240, 0
	v_pk_add_f16 v123, v239, 0
	v_pk_add_f16 v124, v238, 0
	v_pk_fma_f16 v84, v84, v239, 0
	v_pk_fma_f16 v83, v83, v238, 0
	v_pk_fma_f16 v82, v82, v237, 0
	v_pk_add_f16 v140, v140, v223 neg_lo:[0,1] neg_hi:[0,1]
	buffer_load_dwordx4 v[114:117], v248, s[12:15], 0 offen offset:512
	buffer_load_dwordx4 v[50:53], v248, s[12:15], 0 offen offset:1024
	v_pk_add_f16 v141, v141, v224 neg_lo:[0,1] neg_hi:[0,1]
	v_exp_f16_sdwa v237, v138 dst_sel:WORD_0 dst_unused:UNUSED_PAD src0_sel:WORD_0
	v_exp_f16_sdwa v238, v139 dst_sel:WORD_0 dst_unused:UNUSED_PAD src0_sel:WORD_0
	v_exp_f16_sdwa v239, v140 dst_sel:WORD_0 dst_unused:UNUSED_PAD src0_sel:WORD_0
	v_exp_f16_sdwa v240, v141 dst_sel:WORD_0 dst_unused:UNUSED_PAD src0_sel:WORD_0
	v_exp_f16_sdwa v237, v138 dst_sel:WORD_1 dst_unused:UNUSED_PRESERVE src0_sel:WORD_1
	v_exp_f16_sdwa v238, v139 dst_sel:WORD_1 dst_unused:UNUSED_PRESERVE src0_sel:WORD_1
	v_exp_f16_sdwa v239, v140 dst_sel:WORD_1 dst_unused:UNUSED_PRESERVE src0_sel:WORD_1
	v_exp_f16_sdwa v240, v141 dst_sel:WORD_1 dst_unused:UNUSED_PRESERVE src0_sel:WORD_1
	v_pk_add_f16 v125, v125, v237
	v_pk_fma_f16 v85, v109, v240, v85
	v_pk_add_f16 v109, v149, v224 neg_lo:[0,1] neg_hi:[0,1]
	v_pk_add_f16 v124, v124, v238
	v_pk_add_f16 v123, v123, v239
	v_pk_add_f16 v122, v122, v240
	v_pk_fma_f16 v82, v106, v237, v82
	v_pk_fma_f16 v83, v107, v238, v83
	v_pk_fma_f16 v84, v108, v239, v84
	v_pk_add_f16 v106, v146, v221 neg_lo:[0,1] neg_hi:[0,1]
	v_pk_add_f16 v107, v147, v222 neg_lo:[0,1] neg_hi:[0,1]
	v_pk_add_f16 v108, v148, v223 neg_lo:[0,1] neg_hi:[0,1]
	v_exp_f16_sdwa v138, v106 dst_sel:WORD_0 dst_unused:UNUSED_PAD src0_sel:WORD_0
	v_exp_f16_sdwa v139, v107 dst_sel:WORD_0 dst_unused:UNUSED_PAD src0_sel:WORD_0
	v_exp_f16_sdwa v140, v108 dst_sel:WORD_0 dst_unused:UNUSED_PAD src0_sel:WORD_0
	v_exp_f16_sdwa v141, v109 dst_sel:WORD_0 dst_unused:UNUSED_PAD src0_sel:WORD_0
	v_exp_f16_sdwa v138, v106 dst_sel:WORD_1 dst_unused:UNUSED_PRESERVE src0_sel:WORD_1
	v_exp_f16_sdwa v139, v107 dst_sel:WORD_1 dst_unused:UNUSED_PRESERVE src0_sel:WORD_1
	v_exp_f16_sdwa v140, v108 dst_sel:WORD_1 dst_unused:UNUSED_PRESERVE src0_sel:WORD_1
	v_exp_f16_sdwa v141, v109 dst_sel:WORD_1 dst_unused:UNUSED_PRESERVE src0_sel:WORD_1
	v_pk_add_f16 v109, v125, v138
	v_pk_add_f16 v106, v122, v141
	s_mov_b64 exec, s[66:67]
	buffer_load_dwordx4 v[130:133], v248, s[12:15], 0 offen offset:2048
	buffer_load_dwordx4 v[70:73], v248, s[12:15], 0 offen offset:2560
	s_mov_b64 exec, -1
	v_pk_add_f16 v107, v123, v140
	v_pk_add_f16 v108, v124, v139
	v_pk_fma_f16 v85, v129, v141, v85
	v_pk_fma_f16 v84, v128, v140, v84
	v_pk_fma_f16 v83, v127, v139, v83
	v_pk_fma_f16 v82, v126, v138, v82
	v_pk_add_f16 v122, v228, v221 neg_lo:[0,1] neg_hi:[0,1]
	v_pk_add_f16 v123, v227, v222 neg_lo:[0,1] neg_hi:[0,1]
	v_pk_add_f16 v124, v226, v223 neg_lo:[0,1] neg_hi:[0,1]
	v_pk_add_f16 v125, v225, v224 neg_lo:[0,1] neg_hi:[0,1]
	v_exp_f16_sdwa v126, v122 dst_sel:WORD_0 dst_unused:UNUSED_PAD src0_sel:WORD_0
	v_exp_f16_sdwa v127, v123 dst_sel:WORD_0 dst_unused:UNUSED_PAD src0_sel:WORD_0
	v_exp_f16_sdwa v128, v124 dst_sel:WORD_0 dst_unused:UNUSED_PAD src0_sel:WORD_0
	v_exp_f16_sdwa v129, v125 dst_sel:WORD_0 dst_unused:UNUSED_PAD src0_sel:WORD_0
	v_exp_f16_sdwa v126, v122 dst_sel:WORD_1 dst_unused:UNUSED_PRESERVE src0_sel:WORD_1
	v_exp_f16_sdwa v127, v123 dst_sel:WORD_1 dst_unused:UNUSED_PRESERVE src0_sel:WORD_1
	v_exp_f16_sdwa v128, v124 dst_sel:WORD_1 dst_unused:UNUSED_PRESERVE src0_sel:WORD_1
	v_exp_f16_sdwa v129, v125 dst_sel:WORD_1 dst_unused:UNUSED_PRESERVE src0_sel:WORD_1
	v_pk_add_f16 v122, v232, v221 neg_lo:[0,1] neg_hi:[0,1]
	v_pk_add_f16 v109, v109, v126
	v_pk_add_f16 v108, v108, v127
	v_pk_add_f16 v107, v107, v128
	s_mov_b64 exec, s[76:77]
	buffer_load_dwordx4 v[142:145], v249, s[12:15], 0 offen
	buffer_load_dwordx4 v[90:93], v249, s[12:15], 0 offen offset:512
	s_mov_b64 exec, -1
	v_pk_add_f16 v106, v106, v129
	v_pk_fma_f16 v82, v54, v126, v82
	v_pk_fma_f16 v83, v55, v127, v83
	v_pk_fma_f16 v84, v56, v128, v84
	v_pk_fma_f16 v85, v57, v129, v85
	v_pk_add_f16 v123, v231, v222 neg_lo:[0,1] neg_hi:[0,1]
	v_pk_add_f16 v124, v230, v223 neg_lo:[0,1] neg_hi:[0,1]
	v_pk_add_f16 v125, v229, v224 neg_lo:[0,1] neg_hi:[0,1]
	v_exp_f16_sdwa v126, v122 dst_sel:WORD_0 dst_unused:UNUSED_PAD src0_sel:WORD_0
	v_exp_f16_sdwa v127, v123 dst_sel:WORD_0 dst_unused:UNUSED_PAD src0_sel:WORD_0
	v_exp_f16_sdwa v128, v124 dst_sel:WORD_0 dst_unused:UNUSED_PAD src0_sel:WORD_0
	v_exp_f16_sdwa v129, v125 dst_sel:WORD_0 dst_unused:UNUSED_PAD src0_sel:WORD_0
	v_exp_f16_sdwa v126, v122 dst_sel:WORD_1 dst_unused:UNUSED_PRESERVE src0_sel:WORD_1
	v_exp_f16_sdwa v127, v123 dst_sel:WORD_1 dst_unused:UNUSED_PRESERVE src0_sel:WORD_1
	v_exp_f16_sdwa v128, v124 dst_sel:WORD_1 dst_unused:UNUSED_PRESERVE src0_sel:WORD_1
	v_exp_f16_sdwa v129, v125 dst_sel:WORD_1 dst_unused:UNUSED_PRESERVE src0_sel:WORD_1
	v_pk_add_f16 v122, v236, v221 neg_lo:[0,1] neg_hi:[0,1]
	v_pk_add_f16 v109, v109, v126
	v_pk_add_f16 v106, v106, v129
	v_pk_add_f16 v107, v107, v128
	v_pk_add_f16 v108, v108, v127
	v_pk_fma_f16 v85, v77, v129, v85
	v_pk_fma_f16 v84, v76, v128, v84
	s_mov_b64 exec, s[70:71]
	buffer_load_dwordx4 v[150:153], v250, s[12:15], 0 offen offset:512
	buffer_load_dwordx4 v[110:113], v250, s[12:15], 0 offen offset:1024
	s_mov_b64 exec, -1
	v_pk_fma_f16 v83, v75, v127, v83
	v_pk_fma_f16 v82, v74, v126, v82
	v_pk_add_f16 v123, v235, v222 neg_lo:[0,1] neg_hi:[0,1]
	v_pk_add_f16 v124, v234, v223 neg_lo:[0,1] neg_hi:[0,1]
	v_pk_add_f16 v125, v233, v224 neg_lo:[0,1] neg_hi:[0,1]
	v_exp_f16_sdwa v126, v122 dst_sel:WORD_0 dst_unused:UNUSED_PAD src0_sel:WORD_0
	v_exp_f16_sdwa v127, v123 dst_sel:WORD_0 dst_unused:UNUSED_PAD src0_sel:WORD_0
	v_exp_f16_sdwa v128, v124 dst_sel:WORD_0 dst_unused:UNUSED_PAD src0_sel:WORD_0
	v_exp_f16_sdwa v129, v125 dst_sel:WORD_0 dst_unused:UNUSED_PAD src0_sel:WORD_0
	v_exp_f16_sdwa v126, v122 dst_sel:WORD_1 dst_unused:UNUSED_PRESERVE src0_sel:WORD_1
	v_exp_f16_sdwa v127, v123 dst_sel:WORD_1 dst_unused:UNUSED_PRESERVE src0_sel:WORD_1
	v_exp_f16_sdwa v128, v124 dst_sel:WORD_1 dst_unused:UNUSED_PRESERVE src0_sel:WORD_1
	v_exp_f16_sdwa v129, v125 dst_sel:WORD_1 dst_unused:UNUSED_PRESERVE src0_sel:WORD_1
	v_pk_add_f16 v122, v209, v221 neg_lo:[0,1] neg_hi:[0,1]
	v_pk_add_f16 v109, v109, v126
	v_pk_add_f16 v108, v108, v127
	v_pk_add_f16 v107, v107, v128
	v_pk_add_f16 v106, v106, v129
	v_pk_fma_f16 v82, v98, v126, v82
	v_pk_fma_f16 v83, v99, v127, v83
	v_pk_fma_f16 v84, v100, v128, v84
	v_pk_fma_f16 v85, v101, v129, v85
	s_mov_b64 exec, s[78:79]
	buffer_load_dwordx4 v[14:17], v250, s[12:15], 0 offen offset:2048
	buffer_load_dwordx4 v[10:13], v250, s[12:15], 0 offen offset:2560
	s_mov_b64 exec, -1
	v_pk_add_f16 v123, v214, v222 neg_lo:[0,1] neg_hi:[0,1]
	v_pk_add_f16 v124, v215, v223 neg_lo:[0,1] neg_hi:[0,1]
	v_pk_add_f16 v125, v216, v224 neg_lo:[0,1] neg_hi:[0,1]
	v_exp_f16_sdwa v126, v122 dst_sel:WORD_0 dst_unused:UNUSED_PAD src0_sel:WORD_0
	v_exp_f16_sdwa v127, v123 dst_sel:WORD_0 dst_unused:UNUSED_PAD src0_sel:WORD_0
	v_exp_f16_sdwa v128, v124 dst_sel:WORD_0 dst_unused:UNUSED_PAD src0_sel:WORD_0
	v_exp_f16_sdwa v129, v125 dst_sel:WORD_0 dst_unused:UNUSED_PAD src0_sel:WORD_0
	v_exp_f16_sdwa v126, v122 dst_sel:WORD_1 dst_unused:UNUSED_PRESERVE src0_sel:WORD_1
	v_exp_f16_sdwa v127, v123 dst_sel:WORD_1 dst_unused:UNUSED_PRESERVE src0_sel:WORD_1
	v_exp_f16_sdwa v128, v124 dst_sel:WORD_1 dst_unused:UNUSED_PRESERVE src0_sel:WORD_1
	v_exp_f16_sdwa v129, v125 dst_sel:WORD_1 dst_unused:UNUSED_PRESERVE src0_sel:WORD_1
	v_pk_add_f16 v122, v217, v221 neg_lo:[0,1] neg_hi:[0,1]
	v_pk_add_f16 v109, v109, v126
	v_pk_add_f16 v106, v106, v129
	v_pk_add_f16 v107, v107, v128
	v_pk_add_f16 v108, v108, v127
	v_pk_fma_f16 v85, v33, v129, v85
	v_pk_fma_f16 v84, v32, v128, v84
	v_pk_fma_f16 v83, v31, v127, v83
	v_pk_fma_f16 v82, v30, v126, v82
	v_pk_add_f16 v123, v218, v222 neg_lo:[0,1] neg_hi:[0,1]
	v_pk_add_f16 v124, v219, v223 neg_lo:[0,1] neg_hi:[0,1]
	v_pk_add_f16 v125, v220, v224 neg_lo:[0,1] neg_hi:[0,1]
	v_exp_f16_sdwa v126, v122 dst_sel:WORD_0 dst_unused:UNUSED_PAD src0_sel:WORD_0
	v_exp_f16_sdwa v127, v123 dst_sel:WORD_0 dst_unused:UNUSED_PAD src0_sel:WORD_0
	v_exp_f16_sdwa v128, v124 dst_sel:WORD_0 dst_unused:UNUSED_PAD src0_sel:WORD_0
	v_exp_f16_sdwa v129, v125 dst_sel:WORD_0 dst_unused:UNUSED_PAD src0_sel:WORD_0
	v_exp_f16_sdwa v126, v122 dst_sel:WORD_1 dst_unused:UNUSED_PRESERVE src0_sel:WORD_1
	v_exp_f16_sdwa v127, v123 dst_sel:WORD_1 dst_unused:UNUSED_PRESERVE src0_sel:WORD_1
	v_exp_f16_sdwa v128, v124 dst_sel:WORD_1 dst_unused:UNUSED_PRESERVE src0_sel:WORD_1
	v_exp_f16_sdwa v129, v125 dst_sel:WORD_1 dst_unused:UNUSED_PRESERVE src0_sel:WORD_1
	v_pk_add_f16 v122, v210, v221 neg_lo:[0,1] neg_hi:[0,1]
	v_pk_add_f16 v109, v109, v126
	v_pk_add_f16 v108, v108, v127
	v_pk_add_f16 v107, v107, v128
	v_pk_add_f16 v106, v106, v129
	v_pk_fma_f16 v82, v42, v126, v82
	v_pk_fma_f16 v83, v43, v127, v83
	v_pk_fma_f16 v84, v44, v128, v84
	v_pk_fma_f16 v85, v45, v129, v85
	v_pk_add_f16 v123, v211, v222 neg_lo:[0,1] neg_hi:[0,1]
	v_pk_add_f16 v124, v212, v223 neg_lo:[0,1] neg_hi:[0,1]
	v_pk_add_f16 v125, v213, v224 neg_lo:[0,1] neg_hi:[0,1]
	v_exp_f16_sdwa v126, v122 dst_sel:WORD_0 dst_unused:UNUSED_PAD src0_sel:WORD_0
	v_exp_f16_sdwa v127, v123 dst_sel:WORD_0 dst_unused:UNUSED_PAD src0_sel:WORD_0
	v_exp_f16_sdwa v128, v124 dst_sel:WORD_0 dst_unused:UNUSED_PAD src0_sel:WORD_0
	v_exp_f16_sdwa v129, v125 dst_sel:WORD_0 dst_unused:UNUSED_PAD src0_sel:WORD_0
	v_exp_f16_sdwa v126, v122 dst_sel:WORD_1 dst_unused:UNUSED_PRESERVE src0_sel:WORD_1
	v_exp_f16_sdwa v127, v123 dst_sel:WORD_1 dst_unused:UNUSED_PRESERVE src0_sel:WORD_1
	v_exp_f16_sdwa v128, v124 dst_sel:WORD_1 dst_unused:UNUSED_PRESERVE src0_sel:WORD_1
	v_exp_f16_sdwa v129, v125 dst_sel:WORD_1 dst_unused:UNUSED_PRESERVE src0_sel:WORD_1
	v_pk_add_f16 v109, v109, v126
	v_pk_add_f16 v108, v108, v127
	v_rcp_f16_e32 v122, v109
	v_rcp_f16_sdwa v109, v109 dst_sel:DWORD dst_unused:UNUSED_PAD src0_sel:WORD_1
	v_pk_add_f16 v107, v107, v128
	v_rcp_f16_e32 v123, v108
	v_rcp_f16_sdwa v108, v108 dst_sel:DWORD dst_unused:UNUSED_PAD src0_sel:WORD_1
	v_pk_add_f16 v106, v106, v129
	v_rcp_f16_e32 v124, v107
	v_rcp_f16_sdwa v107, v107 dst_sel:DWORD dst_unused:UNUSED_PAD src0_sel:WORD_1
	v_rcp_f16_e32 v125, v106
	v_rcp_f16_sdwa v106, v106 dst_sel:DWORD dst_unused:UNUSED_PAD src0_sel:WORD_1
	v_pk_fma_f16 v82, v58, v126, v82
	v_pack_b32_f16 v109, v122, v109
	v_pk_fma_f16 v83, v59, v127, v83
	v_pk_mul_f16 v141, v82, v109
	v_pack_b32_f16 v82, v123, v108
	v_pk_fma_f16 v84, v60, v128, v84
	v_pk_mul_f16 v140, v83, v82
	v_pack_b32_f16 v82, v124, v107
	v_pk_fma_f16 v85, v61, v129, v85
	v_pk_mul_f16 v139, v84, v82
	v_pack_b32_f16 v82, v125, v106
	v_pk_mul_f16 v138, v85, v82
	s_waitcnt vmcnt(12)
	v_pk_mul_f16 v85, v208, v165 op_sel_hi:[0,1]
	v_pk_mul_f16 v109, v206, v165 op_sel_hi:[0,1]
	v_pk_mul_f16 v122, v207, v162 op_sel_hi:[0,1]
	v_pk_mul_f16 v125, v207, v165 op_sel_hi:[0,1]
	v_pk_mul_f16 v82, v208, v162 op_sel_hi:[0,1]
	v_pk_mul_f16 v83, v208, v163 op_sel_hi:[0,1]
	v_pk_mul_f16 v84, v208, v164 op_sel_hi:[0,1]
	v_pk_mul_f16 v106, v206, v162 op_sel_hi:[0,1]
	v_pk_mul_f16 v107, v206, v163 op_sel_hi:[0,1]
	v_pk_mul_f16 v108, v206, v164 op_sel_hi:[0,1]
	v_pk_mul_f16 v123, v207, v163 op_sel_hi:[0,1]
	v_pk_mul_f16 v124, v207, v164 op_sel_hi:[0,1]
	v_pk_fma_f16 v97, v97, v165, v85
	v_pk_fma_f16 v121, v121, v165, v109
	v_pk_fma_f16 v126, v137, v165, v125
	v_pk_fma_f16 v129, v134, v162, v122
	v_pk_fma_f16 v134, v65, v165, v85
	v_pk_fma_f16 v146, v81, v165, v109
	v_pk_fma_f16 v209, v105, v165, v125
	v_pk_fma_f16 v85, v37, v165, v85
	v_pk_fma_f16 v109, v49, v165, v109
	v_pk_fma_f16 v125, v69, v165, v125
	v_pk_maximum3_f16 v165, v97, v121, v126
	v_pk_fma_f16 v96, v96, v164, v84
	v_pk_fma_f16 v95, v95, v163, v83
	v_pk_fma_f16 v94, v94, v162, v82
	v_pk_fma_f16 v120, v120, v164, v108
	v_pk_fma_f16 v119, v119, v163, v107
	v_pk_fma_f16 v118, v118, v162, v106
	v_pk_fma_f16 v127, v136, v164, v124
	v_pk_fma_f16 v128, v135, v163, v123
	v_pk_fma_f16 v135, v64, v164, v84
	v_pk_fma_f16 v136, v63, v163, v83
	v_pk_fma_f16 v137, v62, v162, v82
	v_pk_fma_f16 v147, v80, v164, v108
	v_pk_fma_f16 v148, v79, v163, v107
	v_pk_fma_f16 v149, v78, v162, v106
	v_pk_fma_f16 v210, v104, v164, v124
	v_pk_fma_f16 v211, v103, v163, v123
	v_pk_fma_f16 v212, v102, v162, v122
	v_pk_fma_f16 v84, v36, v164, v84
	v_pk_fma_f16 v83, v35, v163, v83
	v_pk_fma_f16 v82, v34, v162, v82
	v_pk_fma_f16 v108, v48, v164, v108
	v_pk_fma_f16 v107, v47, v163, v107
	v_pk_fma_f16 v106, v46, v162, v106
	v_pk_fma_f16 v124, v68, v164, v124
	v_pk_fma_f16 v123, v67, v163, v123
	v_pk_fma_f16 v122, v66, v162, v122
	v_pk_maximum3_f16 v162, v94, v118, v129
	v_pk_maximum3_f16 v163, v95, v119, v128
	v_pk_maximum3_f16 v164, v96, v120, v127
	v_pk_maximum3_f16 v216, v134, v146, v209
	v_pk_maximum3_f16 v220, v85, v109, v125
	v_pk_maximum3_f16 v213, v137, v149, v212
	v_pk_maximum3_f16 v214, v136, v148, v211
	v_pk_maximum3_f16 v215, v135, v147, v210
	v_pk_maximum3_f16 v217, v82, v106, v122
	v_pk_maximum3_f16 v218, v83, v107, v123
	v_pk_maximum3_f16 v165, v165, v216, v220
	v_pk_maximum3_f16 v219, v84, v108, v124
	v_pk_maximum3_f16 v162, v162, v213, v217
	v_pk_maximum3_f16 v163, v163, v214, v218
	v_pk_maximum3_f16 v164, v164, v215, v219
	v_pk_add_f16 v97, v97, v165 neg_lo:[0,1] neg_hi:[0,1]
	v_pk_add_f16 v94, v94, v162 neg_lo:[0,1] neg_hi:[0,1]
	v_pk_add_f16 v95, v95, v163 neg_lo:[0,1] neg_hi:[0,1]
	v_pk_add_f16 v96, v96, v164 neg_lo:[0,1] neg_hi:[0,1]
	v_pk_add_f16 v118, v118, v162 neg_lo:[0,1] neg_hi:[0,1]
	v_exp_f16_sdwa v213, v94 dst_sel:WORD_0 dst_unused:UNUSED_PAD src0_sel:WORD_0
	v_exp_f16_sdwa v214, v95 dst_sel:WORD_0 dst_unused:UNUSED_PAD src0_sel:WORD_0
	v_exp_f16_sdwa v215, v96 dst_sel:WORD_0 dst_unused:UNUSED_PAD src0_sel:WORD_0
	v_exp_f16_sdwa v216, v97 dst_sel:WORD_0 dst_unused:UNUSED_PAD src0_sel:WORD_0
	v_exp_f16_sdwa v213, v94 dst_sel:WORD_1 dst_unused:UNUSED_PRESERVE src0_sel:WORD_1
	v_exp_f16_sdwa v214, v95 dst_sel:WORD_1 dst_unused:UNUSED_PRESERVE src0_sel:WORD_1
	v_exp_f16_sdwa v215, v96 dst_sel:WORD_1 dst_unused:UNUSED_PRESERVE src0_sel:WORD_1
	v_exp_f16_sdwa v216, v97 dst_sel:WORD_1 dst_unused:UNUSED_PRESERVE src0_sel:WORD_1
	v_pk_add_f16 v119, v119, v163 neg_lo:[0,1] neg_hi:[0,1]
	v_pk_add_f16 v97, v213, 0
	v_pk_fma_f16 v57, v57, v216, 0
	v_pk_add_f16 v94, v216, 0
	v_pk_add_f16 v95, v215, 0
	v_pk_add_f16 v96, v214, 0
	v_pk_fma_f16 v56, v56, v215, 0
	v_pk_fma_f16 v55, v55, v214, 0
	v_pk_fma_f16 v54, v54, v213, 0
	v_pk_add_f16 v120, v120, v164 neg_lo:[0,1] neg_hi:[0,1]
	v_pk_add_f16 v121, v121, v165 neg_lo:[0,1] neg_hi:[0,1]
	v_pk_add_f16 v82, v82, v162 neg_lo:[0,1] neg_hi:[0,1]
	v_exp_f16_sdwa v213, v118 dst_sel:WORD_0 dst_unused:UNUSED_PAD src0_sel:WORD_0
	v_exp_f16_sdwa v214, v119 dst_sel:WORD_0 dst_unused:UNUSED_PAD src0_sel:WORD_0
	v_exp_f16_sdwa v215, v120 dst_sel:WORD_0 dst_unused:UNUSED_PAD src0_sel:WORD_0
	v_exp_f16_sdwa v216, v121 dst_sel:WORD_0 dst_unused:UNUSED_PAD src0_sel:WORD_0
	v_exp_f16_sdwa v213, v118 dst_sel:WORD_1 dst_unused:UNUSED_PRESERVE src0_sel:WORD_1
	v_exp_f16_sdwa v214, v119 dst_sel:WORD_1 dst_unused:UNUSED_PRESERVE src0_sel:WORD_1
	v_exp_f16_sdwa v215, v120 dst_sel:WORD_1 dst_unused:UNUSED_PRESERVE src0_sel:WORD_1
	v_exp_f16_sdwa v216, v121 dst_sel:WORD_1 dst_unused:UNUSED_PRESERVE src0_sel:WORD_1
	v_pk_add_f16 v83, v83, v163 neg_lo:[0,1] neg_hi:[0,1]
	v_pk_add_f16 v97, v97, v213
	v_pk_fma_f16 v57, v77, v216, v57
	v_pk_add_f16 v77, v126, v165 neg_lo:[0,1] neg_hi:[0,1]
	v_pk_add_f16 v96, v96, v214
	v_pk_add_f16 v95, v95, v215
	v_pk_add_f16 v94, v94, v216
	v_pk_fma_f16 v54, v74, v213, v54
	v_pk_fma_f16 v55, v75, v214, v55
	v_pk_fma_f16 v56, v76, v215, v56
	v_pk_add_f16 v74, v129, v162 neg_lo:[0,1] neg_hi:[0,1]
	v_pk_add_f16 v75, v128, v163 neg_lo:[0,1] neg_hi:[0,1]
	v_pk_add_f16 v76, v127, v164 neg_lo:[0,1] neg_hi:[0,1]
	v_pk_add_f16 v84, v84, v164 neg_lo:[0,1] neg_hi:[0,1]
	v_exp_f16_sdwa v118, v74 dst_sel:WORD_0 dst_unused:UNUSED_PAD src0_sel:WORD_0
	v_exp_f16_sdwa v119, v75 dst_sel:WORD_0 dst_unused:UNUSED_PAD src0_sel:WORD_0
	v_exp_f16_sdwa v120, v76 dst_sel:WORD_0 dst_unused:UNUSED_PAD src0_sel:WORD_0
	v_exp_f16_sdwa v121, v77 dst_sel:WORD_0 dst_unused:UNUSED_PAD src0_sel:WORD_0
	v_exp_f16_sdwa v118, v74 dst_sel:WORD_1 dst_unused:UNUSED_PRESERVE src0_sel:WORD_1
	v_exp_f16_sdwa v119, v75 dst_sel:WORD_1 dst_unused:UNUSED_PRESERVE src0_sel:WORD_1
	v_exp_f16_sdwa v120, v76 dst_sel:WORD_1 dst_unused:UNUSED_PRESERVE src0_sel:WORD_1
	v_exp_f16_sdwa v121, v77 dst_sel:WORD_1 dst_unused:UNUSED_PRESERVE src0_sel:WORD_1
	v_pk_add_f16 v85, v85, v165 neg_lo:[0,1] neg_hi:[0,1]
	v_pk_add_f16 v77, v97, v118
	v_pk_add_f16 v74, v94, v121
	v_pk_add_f16 v75, v95, v120
	v_pk_add_f16 v76, v96, v119
	v_pk_fma_f16 v57, v101, v121, v57
	v_pk_fma_f16 v56, v100, v120, v56
	v_pk_fma_f16 v55, v99, v119, v55
	v_pk_fma_f16 v54, v98, v118, v54
	v_pk_add_f16 v94, v137, v162 neg_lo:[0,1] neg_hi:[0,1]
	v_pk_add_f16 v95, v136, v163 neg_lo:[0,1] neg_hi:[0,1]
	v_pk_add_f16 v96, v135, v164 neg_lo:[0,1] neg_hi:[0,1]
	v_pk_add_f16 v97, v134, v165 neg_lo:[0,1] neg_hi:[0,1]
	v_exp_f16_sdwa v98, v94 dst_sel:WORD_0 dst_unused:UNUSED_PAD src0_sel:WORD_0
	v_exp_f16_sdwa v99, v95 dst_sel:WORD_0 dst_unused:UNUSED_PAD src0_sel:WORD_0
	v_exp_f16_sdwa v100, v96 dst_sel:WORD_0 dst_unused:UNUSED_PAD src0_sel:WORD_0
	v_exp_f16_sdwa v101, v97 dst_sel:WORD_0 dst_unused:UNUSED_PAD src0_sel:WORD_0
	v_exp_f16_sdwa v98, v94 dst_sel:WORD_1 dst_unused:UNUSED_PRESERVE src0_sel:WORD_1
	v_exp_f16_sdwa v99, v95 dst_sel:WORD_1 dst_unused:UNUSED_PRESERVE src0_sel:WORD_1
	v_exp_f16_sdwa v100, v96 dst_sel:WORD_1 dst_unused:UNUSED_PRESERVE src0_sel:WORD_1
	v_exp_f16_sdwa v101, v97 dst_sel:WORD_1 dst_unused:UNUSED_PRESERVE src0_sel:WORD_1
	v_pk_add_f16 v94, v149, v162 neg_lo:[0,1] neg_hi:[0,1]
	v_pk_add_f16 v77, v77, v98
	v_pk_add_f16 v76, v76, v99
	v_pk_add_f16 v75, v75, v100
	v_pk_add_f16 v74, v74, v101
	v_pk_fma_f16 v54, v30, v98, v54
	v_pk_fma_f16 v55, v31, v99, v55
	v_pk_fma_f16 v56, v32, v100, v56
	v_pk_fma_f16 v57, v33, v101, v57
	v_pk_add_f16 v95, v148, v163 neg_lo:[0,1] neg_hi:[0,1]
	v_pk_add_f16 v96, v147, v164 neg_lo:[0,1] neg_hi:[0,1]
	v_pk_add_f16 v97, v146, v165 neg_lo:[0,1] neg_hi:[0,1]
	v_exp_f16_sdwa v98, v94 dst_sel:WORD_0 dst_unused:UNUSED_PAD src0_sel:WORD_0
	v_exp_f16_sdwa v99, v95 dst_sel:WORD_0 dst_unused:UNUSED_PAD src0_sel:WORD_0
	v_exp_f16_sdwa v100, v96 dst_sel:WORD_0 dst_unused:UNUSED_PAD src0_sel:WORD_0
	v_exp_f16_sdwa v101, v97 dst_sel:WORD_0 dst_unused:UNUSED_PAD src0_sel:WORD_0
	v_exp_f16_sdwa v98, v94 dst_sel:WORD_1 dst_unused:UNUSED_PRESERVE src0_sel:WORD_1
	v_exp_f16_sdwa v99, v95 dst_sel:WORD_1 dst_unused:UNUSED_PRESERVE src0_sel:WORD_1
	v_exp_f16_sdwa v100, v96 dst_sel:WORD_1 dst_unused:UNUSED_PRESERVE src0_sel:WORD_1
	v_exp_f16_sdwa v101, v97 dst_sel:WORD_1 dst_unused:UNUSED_PRESERVE src0_sel:WORD_1
	v_pk_add_f16 v94, v212, v162 neg_lo:[0,1] neg_hi:[0,1]
	v_pk_add_f16 v77, v77, v98
	v_pk_add_f16 v74, v74, v101
	v_pk_add_f16 v75, v75, v100
	v_pk_add_f16 v76, v76, v99
	v_pk_fma_f16 v57, v45, v101, v57
	v_pk_fma_f16 v56, v44, v100, v56
	v_pk_fma_f16 v55, v43, v99, v55
	v_pk_fma_f16 v54, v42, v98, v54
	v_pk_add_f16 v95, v211, v163 neg_lo:[0,1] neg_hi:[0,1]
	v_pk_add_f16 v96, v210, v164 neg_lo:[0,1] neg_hi:[0,1]
	v_pk_add_f16 v97, v209, v165 neg_lo:[0,1] neg_hi:[0,1]
	v_exp_f16_sdwa v98, v94 dst_sel:WORD_0 dst_unused:UNUSED_PAD src0_sel:WORD_0
	v_exp_f16_sdwa v99, v95 dst_sel:WORD_0 dst_unused:UNUSED_PAD src0_sel:WORD_0
	v_exp_f16_sdwa v100, v96 dst_sel:WORD_0 dst_unused:UNUSED_PAD src0_sel:WORD_0
	v_exp_f16_sdwa v101, v97 dst_sel:WORD_0 dst_unused:UNUSED_PAD src0_sel:WORD_0
	v_exp_f16_sdwa v98, v94 dst_sel:WORD_1 dst_unused:UNUSED_PRESERVE src0_sel:WORD_1
	v_exp_f16_sdwa v99, v95 dst_sel:WORD_1 dst_unused:UNUSED_PRESERVE src0_sel:WORD_1
	v_exp_f16_sdwa v100, v96 dst_sel:WORD_1 dst_unused:UNUSED_PRESERVE src0_sel:WORD_1
	v_exp_f16_sdwa v101, v97 dst_sel:WORD_1 dst_unused:UNUSED_PRESERVE src0_sel:WORD_1
	v_exp_f16_sdwa v94, v82 dst_sel:WORD_0 dst_unused:UNUSED_PAD src0_sel:WORD_0
	v_exp_f16_sdwa v95, v83 dst_sel:WORD_0 dst_unused:UNUSED_PAD src0_sel:WORD_0
	v_exp_f16_sdwa v96, v84 dst_sel:WORD_0 dst_unused:UNUSED_PAD src0_sel:WORD_0
	v_exp_f16_sdwa v97, v85 dst_sel:WORD_0 dst_unused:UNUSED_PAD src0_sel:WORD_0
	v_exp_f16_sdwa v94, v82 dst_sel:WORD_1 dst_unused:UNUSED_PRESERVE src0_sel:WORD_1
	v_exp_f16_sdwa v95, v83 dst_sel:WORD_1 dst_unused:UNUSED_PRESERVE src0_sel:WORD_1
	v_exp_f16_sdwa v96, v84 dst_sel:WORD_1 dst_unused:UNUSED_PRESERVE src0_sel:WORD_1
	v_exp_f16_sdwa v97, v85 dst_sel:WORD_1 dst_unused:UNUSED_PRESERVE src0_sel:WORD_1
	v_pk_add_f16 v82, v106, v162 neg_lo:[0,1] neg_hi:[0,1]
	v_pk_add_f16 v77, v77, v98
	v_pk_add_f16 v76, v76, v99
	v_pk_add_f16 v75, v75, v100
	v_pk_add_f16 v74, v74, v101
	v_pk_fma_f16 v54, v58, v98, v54
	v_pk_fma_f16 v55, v59, v99, v55
	v_pk_fma_f16 v56, v60, v100, v56
	v_pk_fma_f16 v57, v61, v101, v57
	v_pk_add_f16 v77, v77, v94
	v_pk_add_f16 v74, v74, v97
	v_pk_add_f16 v75, v75, v96
	v_pk_add_f16 v76, v76, v95
	v_pk_fma_f16 v57, v21, v97, v57
	v_pk_fma_f16 v56, v20, v96, v56
	v_pk_fma_f16 v55, v19, v95, v55
	v_pk_fma_f16 v54, v18, v94, v54
	v_pk_add_f16 v83, v107, v163 neg_lo:[0,1] neg_hi:[0,1]
	v_pk_add_f16 v84, v108, v164 neg_lo:[0,1] neg_hi:[0,1]
	v_pk_add_f16 v85, v109, v165 neg_lo:[0,1] neg_hi:[0,1]
	v_exp_f16_sdwa v94, v82 dst_sel:WORD_0 dst_unused:UNUSED_PAD src0_sel:WORD_0
	v_exp_f16_sdwa v95, v83 dst_sel:WORD_0 dst_unused:UNUSED_PAD src0_sel:WORD_0
	v_exp_f16_sdwa v96, v84 dst_sel:WORD_0 dst_unused:UNUSED_PAD src0_sel:WORD_0
	v_exp_f16_sdwa v97, v85 dst_sel:WORD_0 dst_unused:UNUSED_PAD src0_sel:WORD_0
	v_exp_f16_sdwa v94, v82 dst_sel:WORD_1 dst_unused:UNUSED_PRESERVE src0_sel:WORD_1
	v_exp_f16_sdwa v95, v83 dst_sel:WORD_1 dst_unused:UNUSED_PRESERVE src0_sel:WORD_1
	v_exp_f16_sdwa v96, v84 dst_sel:WORD_1 dst_unused:UNUSED_PRESERVE src0_sel:WORD_1
	v_exp_f16_sdwa v97, v85 dst_sel:WORD_1 dst_unused:UNUSED_PRESERVE src0_sel:WORD_1
	v_pk_add_f16 v82, v122, v162 neg_lo:[0,1] neg_hi:[0,1]
	v_pk_add_f16 v77, v77, v94
	v_pk_add_f16 v76, v76, v95
	v_pk_add_f16 v75, v75, v96
	v_pk_add_f16 v74, v74, v97
	v_pk_fma_f16 v54, v22, v94, v54
	v_pk_fma_f16 v55, v23, v95, v55
	v_pk_fma_f16 v56, v24, v96, v56
	v_pk_fma_f16 v57, v25, v97, v57
	v_pk_add_f16 v83, v123, v163 neg_lo:[0,1] neg_hi:[0,1]
	v_pk_add_f16 v84, v124, v164 neg_lo:[0,1] neg_hi:[0,1]
	v_pk_add_f16 v85, v125, v165 neg_lo:[0,1] neg_hi:[0,1]
	v_exp_f16_sdwa v94, v82 dst_sel:WORD_0 dst_unused:UNUSED_PAD src0_sel:WORD_0
	v_exp_f16_sdwa v95, v83 dst_sel:WORD_0 dst_unused:UNUSED_PAD src0_sel:WORD_0
	v_exp_f16_sdwa v96, v84 dst_sel:WORD_0 dst_unused:UNUSED_PAD src0_sel:WORD_0
	v_exp_f16_sdwa v97, v85 dst_sel:WORD_0 dst_unused:UNUSED_PAD src0_sel:WORD_0
	v_exp_f16_sdwa v94, v82 dst_sel:WORD_1 dst_unused:UNUSED_PRESERVE src0_sel:WORD_1
	v_exp_f16_sdwa v95, v83 dst_sel:WORD_1 dst_unused:UNUSED_PRESERVE src0_sel:WORD_1
	v_exp_f16_sdwa v96, v84 dst_sel:WORD_1 dst_unused:UNUSED_PRESERVE src0_sel:WORD_1
	v_exp_f16_sdwa v97, v85 dst_sel:WORD_1 dst_unused:UNUSED_PRESERVE src0_sel:WORD_1
	v_pk_add_f16 v77, v77, v94
	v_pk_add_f16 v76, v76, v95
	v_rcp_f16_e32 v82, v77
	v_rcp_f16_sdwa v77, v77 dst_sel:DWORD dst_unused:UNUSED_PAD src0_sel:WORD_1
	v_pk_add_f16 v75, v75, v96
	v_rcp_f16_e32 v83, v76
	v_rcp_f16_sdwa v76, v76 dst_sel:DWORD dst_unused:UNUSED_PAD src0_sel:WORD_1
	v_pk_add_f16 v74, v74, v97
	v_rcp_f16_e32 v84, v75
	v_rcp_f16_sdwa v75, v75 dst_sel:DWORD dst_unused:UNUSED_PAD src0_sel:WORD_1
	v_rcp_f16_e32 v85, v74
	v_rcp_f16_sdwa v74, v74 dst_sel:DWORD dst_unused:UNUSED_PAD src0_sel:WORD_1
	v_pk_fma_f16 v54, v26, v94, v54
	v_pack_b32_f16 v77, v82, v77
	v_pk_fma_f16 v57, v29, v97, v57
	v_pk_fma_f16 v55, v27, v95, v55
	v_pk_mul_f16 v97, v54, v77
	v_pack_b32_f16 v54, v83, v76
	v_pk_fma_f16 v56, v28, v96, v56
	v_pk_mul_f16 v96, v55, v54
	v_pack_b32_f16 v54, v84, v75
	v_pk_mul_f16 v95, v56, v54
	v_pack_b32_f16 v54, v85, v74
	v_pk_mul_f16 v94, v57, v54
	s_waitcnt vmcnt(6)
	v_pk_mul_f16 v57, v208, v161 op_sel_hi:[0,1]
	v_pk_mul_f16 v77, v206, v161 op_sel_hi:[0,1]
	v_pk_mul_f16 v85, v207, v161 op_sel_hi:[0,1]
	v_pk_mul_f16 v54, v208, v158 op_sel_hi:[0,1]
	v_pk_mul_f16 v55, v208, v159 op_sel_hi:[0,1]
	v_pk_mul_f16 v56, v208, v160 op_sel_hi:[0,1]
	v_pk_mul_f16 v74, v206, v158 op_sel_hi:[0,1]
	v_pk_mul_f16 v75, v206, v159 op_sel_hi:[0,1]
	v_pk_mul_f16 v76, v206, v160 op_sel_hi:[0,1]
	v_pk_mul_f16 v82, v207, v158 op_sel_hi:[0,1]
	v_pk_mul_f16 v83, v207, v159 op_sel_hi:[0,1]
	v_pk_mul_f16 v84, v207, v160 op_sel_hi:[0,1]
	v_pk_fma_f16 v65, v65, v161, v57
	v_pk_fma_f16 v81, v81, v161, v77
	v_pk_fma_f16 v98, v105, v161, v85
	v_pk_fma_f16 v64, v64, v160, v56
	v_pk_maximum3_f16 v125, v65, v81, v98
	v_pk_fma_f16 v63, v63, v159, v55
	v_pk_fma_f16 v62, v62, v158, v54
	v_pk_fma_f16 v80, v80, v160, v76
	v_pk_fma_f16 v79, v79, v159, v75
	v_pk_fma_f16 v78, v78, v158, v74
	v_pk_fma_f16 v99, v104, v160, v84
	v_pk_fma_f16 v100, v103, v159, v83
	v_pk_fma_f16 v101, v102, v158, v82
	v_pk_fma_f16 v102, v37, v161, v57
	v_pk_fma_f16 v106, v49, v161, v77
	v_pk_fma_f16 v118, v69, v161, v85
	v_pk_fma_f16 v57, v89, v161, v57
	v_pk_fma_f16 v77, v117, v161, v77
	v_pk_fma_f16 v85, v133, v161, v85
	v_pk_maximum3_f16 v122, v62, v78, v101
	v_pk_maximum3_f16 v123, v63, v79, v100
	v_pk_maximum3_f16 v124, v64, v80, v99
	v_pk_maximum3_f16 v129, v102, v106, v118
	v_pk_fma_f16 v103, v36, v160, v56
	v_pk_maximum3_f16 v137, v57, v77, v85
	v_pk_fma_f16 v104, v35, v159, v55
	v_pk_maximum3_f16 v125, v125, v129, v137
	v_pk_fma_f16 v105, v34, v158, v54
	v_pk_fma_f16 v107, v48, v160, v76
	v_pk_fma_f16 v108, v47, v159, v75
	v_pk_fma_f16 v109, v46, v158, v74
	v_pk_fma_f16 v119, v68, v160, v84
	v_pk_fma_f16 v120, v67, v159, v83
	v_pk_fma_f16 v121, v66, v158, v82
	v_pk_fma_f16 v56, v88, v160, v56
	v_pk_fma_f16 v55, v87, v159, v55
	v_pk_fma_f16 v54, v86, v158, v54
	v_pk_fma_f16 v76, v116, v160, v76
	v_pk_fma_f16 v75, v115, v159, v75
	v_pk_fma_f16 v74, v114, v158, v74
	v_pk_fma_f16 v84, v132, v160, v84
	v_pk_fma_f16 v83, v131, v159, v83
	v_pk_fma_f16 v82, v130, v158, v82
	v_pk_maximum3_f16 v126, v105, v109, v121
	v_pk_maximum3_f16 v127, v104, v108, v120
	v_pk_maximum3_f16 v128, v103, v107, v119
	v_pk_maximum3_f16 v135, v55, v75, v83
	v_pk_maximum3_f16 v136, v56, v76, v84
	v_pk_maximum3_f16 v134, v54, v74, v82
	v_pk_maximum3_f16 v122, v122, v126, v134
	v_pk_maximum3_f16 v123, v123, v127, v135
	v_pk_maximum3_f16 v124, v124, v128, v136
	v_pk_add_f16 v65, v65, v125 neg_lo:[0,1] neg_hi:[0,1]
	v_pk_add_f16 v62, v62, v122 neg_lo:[0,1] neg_hi:[0,1]
	v_pk_add_f16 v63, v63, v123 neg_lo:[0,1] neg_hi:[0,1]
	v_pk_add_f16 v64, v64, v124 neg_lo:[0,1] neg_hi:[0,1]
	v_pk_add_f16 v78, v78, v122 neg_lo:[0,1] neg_hi:[0,1]
	v_exp_f16_sdwa v126, v62 dst_sel:WORD_0 dst_unused:UNUSED_PAD src0_sel:WORD_0
	v_exp_f16_sdwa v127, v63 dst_sel:WORD_0 dst_unused:UNUSED_PAD src0_sel:WORD_0
	v_exp_f16_sdwa v128, v64 dst_sel:WORD_0 dst_unused:UNUSED_PAD src0_sel:WORD_0
	v_exp_f16_sdwa v129, v65 dst_sel:WORD_0 dst_unused:UNUSED_PAD src0_sel:WORD_0
	v_exp_f16_sdwa v126, v62 dst_sel:WORD_1 dst_unused:UNUSED_PRESERVE src0_sel:WORD_1
	v_exp_f16_sdwa v127, v63 dst_sel:WORD_1 dst_unused:UNUSED_PRESERVE src0_sel:WORD_1
	v_exp_f16_sdwa v128, v64 dst_sel:WORD_1 dst_unused:UNUSED_PRESERVE src0_sel:WORD_1
	v_exp_f16_sdwa v129, v65 dst_sel:WORD_1 dst_unused:UNUSED_PRESERVE src0_sel:WORD_1
	v_pk_add_f16 v79, v79, v123 neg_lo:[0,1] neg_hi:[0,1]
	v_pk_add_f16 v65, v126, 0
	v_pk_fma_f16 v33, v33, v129, 0
	v_pk_add_f16 v62, v129, 0
	v_pk_add_f16 v63, v128, 0
	v_pk_add_f16 v64, v127, 0
	v_pk_fma_f16 v32, v32, v128, 0
	v_pk_fma_f16 v31, v31, v127, 0
	v_pk_fma_f16 v30, v30, v126, 0
	v_pk_add_f16 v80, v80, v124 neg_lo:[0,1] neg_hi:[0,1]
	v_pk_add_f16 v81, v81, v125 neg_lo:[0,1] neg_hi:[0,1]
	v_pk_add_f16 v54, v54, v122 neg_lo:[0,1] neg_hi:[0,1]
	v_exp_f16_sdwa v126, v78 dst_sel:WORD_0 dst_unused:UNUSED_PAD src0_sel:WORD_0
	v_exp_f16_sdwa v127, v79 dst_sel:WORD_0 dst_unused:UNUSED_PAD src0_sel:WORD_0
	v_exp_f16_sdwa v128, v80 dst_sel:WORD_0 dst_unused:UNUSED_PAD src0_sel:WORD_0
	v_exp_f16_sdwa v129, v81 dst_sel:WORD_0 dst_unused:UNUSED_PAD src0_sel:WORD_0
	v_exp_f16_sdwa v126, v78 dst_sel:WORD_1 dst_unused:UNUSED_PRESERVE src0_sel:WORD_1
	v_exp_f16_sdwa v127, v79 dst_sel:WORD_1 dst_unused:UNUSED_PRESERVE src0_sel:WORD_1
	v_exp_f16_sdwa v128, v80 dst_sel:WORD_1 dst_unused:UNUSED_PRESERVE src0_sel:WORD_1
	v_exp_f16_sdwa v129, v81 dst_sel:WORD_1 dst_unused:UNUSED_PRESERVE src0_sel:WORD_1
	v_pk_add_f16 v55, v55, v123 neg_lo:[0,1] neg_hi:[0,1]
	v_pk_add_f16 v65, v65, v126
	v_pk_fma_f16 v33, v45, v129, v33
	v_pk_add_f16 v45, v98, v125 neg_lo:[0,1] neg_hi:[0,1]
	v_pk_add_f16 v64, v64, v127
	v_pk_add_f16 v63, v63, v128
	v_pk_add_f16 v62, v62, v129
	v_pk_fma_f16 v30, v42, v126, v30
	v_pk_fma_f16 v31, v43, v127, v31
	v_pk_fma_f16 v32, v44, v128, v32
	v_pk_add_f16 v42, v101, v122 neg_lo:[0,1] neg_hi:[0,1]
	v_pk_add_f16 v43, v100, v123 neg_lo:[0,1] neg_hi:[0,1]
	v_pk_add_f16 v44, v99, v124 neg_lo:[0,1] neg_hi:[0,1]
	v_pk_add_f16 v56, v56, v124 neg_lo:[0,1] neg_hi:[0,1]
	v_exp_f16_sdwa v78, v42 dst_sel:WORD_0 dst_unused:UNUSED_PAD src0_sel:WORD_0
	v_exp_f16_sdwa v79, v43 dst_sel:WORD_0 dst_unused:UNUSED_PAD src0_sel:WORD_0
	v_exp_f16_sdwa v80, v44 dst_sel:WORD_0 dst_unused:UNUSED_PAD src0_sel:WORD_0
	v_exp_f16_sdwa v81, v45 dst_sel:WORD_0 dst_unused:UNUSED_PAD src0_sel:WORD_0
	v_exp_f16_sdwa v78, v42 dst_sel:WORD_1 dst_unused:UNUSED_PRESERVE src0_sel:WORD_1
	v_exp_f16_sdwa v79, v43 dst_sel:WORD_1 dst_unused:UNUSED_PRESERVE src0_sel:WORD_1
	v_exp_f16_sdwa v80, v44 dst_sel:WORD_1 dst_unused:UNUSED_PRESERVE src0_sel:WORD_1
	v_exp_f16_sdwa v81, v45 dst_sel:WORD_1 dst_unused:UNUSED_PRESERVE src0_sel:WORD_1
	v_pk_add_f16 v57, v57, v125 neg_lo:[0,1] neg_hi:[0,1]
	v_pk_add_f16 v45, v65, v78
	v_pk_add_f16 v42, v62, v81
	v_pk_add_f16 v43, v63, v80
	v_pk_add_f16 v44, v64, v79
	v_pk_fma_f16 v33, v61, v81, v33
	v_pk_fma_f16 v32, v60, v80, v32
	v_pk_fma_f16 v31, v59, v79, v31
	v_pk_fma_f16 v30, v58, v78, v30
	v_pk_add_f16 v58, v105, v122 neg_lo:[0,1] neg_hi:[0,1]
	v_pk_add_f16 v59, v104, v123 neg_lo:[0,1] neg_hi:[0,1]
	v_pk_add_f16 v60, v103, v124 neg_lo:[0,1] neg_hi:[0,1]
	v_pk_add_f16 v61, v102, v125 neg_lo:[0,1] neg_hi:[0,1]
	v_exp_f16_sdwa v62, v58 dst_sel:WORD_0 dst_unused:UNUSED_PAD src0_sel:WORD_0
	v_exp_f16_sdwa v63, v59 dst_sel:WORD_0 dst_unused:UNUSED_PAD src0_sel:WORD_0
	v_exp_f16_sdwa v64, v60 dst_sel:WORD_0 dst_unused:UNUSED_PAD src0_sel:WORD_0
	v_exp_f16_sdwa v65, v61 dst_sel:WORD_0 dst_unused:UNUSED_PAD src0_sel:WORD_0
	v_exp_f16_sdwa v62, v58 dst_sel:WORD_1 dst_unused:UNUSED_PRESERVE src0_sel:WORD_1
	v_exp_f16_sdwa v63, v59 dst_sel:WORD_1 dst_unused:UNUSED_PRESERVE src0_sel:WORD_1
	v_exp_f16_sdwa v64, v60 dst_sel:WORD_1 dst_unused:UNUSED_PRESERVE src0_sel:WORD_1
	v_exp_f16_sdwa v65, v61 dst_sel:WORD_1 dst_unused:UNUSED_PRESERVE src0_sel:WORD_1
	v_pk_add_f16 v58, v109, v122 neg_lo:[0,1] neg_hi:[0,1]
	v_pk_add_f16 v45, v45, v62
	v_pk_add_f16 v44, v44, v63
	v_pk_add_f16 v43, v43, v64
	v_pk_add_f16 v42, v42, v65
	v_pk_fma_f16 v30, v18, v62, v30
	v_pk_fma_f16 v31, v19, v63, v31
	v_pk_fma_f16 v32, v20, v64, v32
	v_pk_fma_f16 v33, v21, v65, v33
	v_pk_add_f16 v59, v108, v123 neg_lo:[0,1] neg_hi:[0,1]
	v_pk_add_f16 v60, v107, v124 neg_lo:[0,1] neg_hi:[0,1]
	v_pk_add_f16 v61, v106, v125 neg_lo:[0,1] neg_hi:[0,1]
	v_exp_f16_sdwa v62, v58 dst_sel:WORD_0 dst_unused:UNUSED_PAD src0_sel:WORD_0
	v_exp_f16_sdwa v63, v59 dst_sel:WORD_0 dst_unused:UNUSED_PAD src0_sel:WORD_0
	v_exp_f16_sdwa v64, v60 dst_sel:WORD_0 dst_unused:UNUSED_PAD src0_sel:WORD_0
	v_exp_f16_sdwa v65, v61 dst_sel:WORD_0 dst_unused:UNUSED_PAD src0_sel:WORD_0
	v_exp_f16_sdwa v62, v58 dst_sel:WORD_1 dst_unused:UNUSED_PRESERVE src0_sel:WORD_1
	v_exp_f16_sdwa v63, v59 dst_sel:WORD_1 dst_unused:UNUSED_PRESERVE src0_sel:WORD_1
	v_exp_f16_sdwa v64, v60 dst_sel:WORD_1 dst_unused:UNUSED_PRESERVE src0_sel:WORD_1
	v_exp_f16_sdwa v65, v61 dst_sel:WORD_1 dst_unused:UNUSED_PRESERVE src0_sel:WORD_1
	v_pk_add_f16 v58, v121, v122 neg_lo:[0,1] neg_hi:[0,1]
	v_pk_add_f16 v45, v45, v62
	v_pk_add_f16 v42, v42, v65
	v_pk_add_f16 v43, v43, v64
	v_pk_add_f16 v44, v44, v63
	v_pk_fma_f16 v33, v25, v65, v33
	v_pk_fma_f16 v32, v24, v64, v32
	v_pk_fma_f16 v31, v23, v63, v31
	v_pk_fma_f16 v30, v22, v62, v30
	v_pk_add_f16 v59, v120, v123 neg_lo:[0,1] neg_hi:[0,1]
	v_pk_add_f16 v60, v119, v124 neg_lo:[0,1] neg_hi:[0,1]
	v_pk_add_f16 v61, v118, v125 neg_lo:[0,1] neg_hi:[0,1]
	v_exp_f16_sdwa v62, v58 dst_sel:WORD_0 dst_unused:UNUSED_PAD src0_sel:WORD_0
	v_exp_f16_sdwa v63, v59 dst_sel:WORD_0 dst_unused:UNUSED_PAD src0_sel:WORD_0
	v_exp_f16_sdwa v64, v60 dst_sel:WORD_0 dst_unused:UNUSED_PAD src0_sel:WORD_0
	v_exp_f16_sdwa v65, v61 dst_sel:WORD_0 dst_unused:UNUSED_PAD src0_sel:WORD_0
	v_exp_f16_sdwa v62, v58 dst_sel:WORD_1 dst_unused:UNUSED_PRESERVE src0_sel:WORD_1
	v_exp_f16_sdwa v63, v59 dst_sel:WORD_1 dst_unused:UNUSED_PRESERVE src0_sel:WORD_1
	v_exp_f16_sdwa v64, v60 dst_sel:WORD_1 dst_unused:UNUSED_PRESERVE src0_sel:WORD_1
	v_exp_f16_sdwa v65, v61 dst_sel:WORD_1 dst_unused:UNUSED_PRESERVE src0_sel:WORD_1
	v_exp_f16_sdwa v58, v54 dst_sel:WORD_0 dst_unused:UNUSED_PAD src0_sel:WORD_0
	v_exp_f16_sdwa v59, v55 dst_sel:WORD_0 dst_unused:UNUSED_PAD src0_sel:WORD_0
	v_exp_f16_sdwa v60, v56 dst_sel:WORD_0 dst_unused:UNUSED_PAD src0_sel:WORD_0
	v_exp_f16_sdwa v61, v57 dst_sel:WORD_0 dst_unused:UNUSED_PAD src0_sel:WORD_0
	v_exp_f16_sdwa v58, v54 dst_sel:WORD_1 dst_unused:UNUSED_PRESERVE src0_sel:WORD_1
	v_exp_f16_sdwa v59, v55 dst_sel:WORD_1 dst_unused:UNUSED_PRESERVE src0_sel:WORD_1
	v_exp_f16_sdwa v60, v56 dst_sel:WORD_1 dst_unused:UNUSED_PRESERVE src0_sel:WORD_1
	v_exp_f16_sdwa v61, v57 dst_sel:WORD_1 dst_unused:UNUSED_PRESERVE src0_sel:WORD_1
	v_pk_add_f16 v54, v74, v122 neg_lo:[0,1] neg_hi:[0,1]
	v_pk_add_f16 v45, v45, v62
	v_pk_add_f16 v44, v44, v63
	v_pk_add_f16 v43, v43, v64
	v_pk_add_f16 v42, v42, v65
	v_pk_fma_f16 v30, v26, v62, v30
	v_pk_fma_f16 v31, v27, v63, v31
	v_pk_fma_f16 v32, v28, v64, v32
	v_pk_fma_f16 v33, v29, v65, v33
	v_pk_add_f16 v45, v45, v58
	v_pk_add_f16 v42, v42, v61
	v_pk_add_f16 v43, v43, v60
	v_pk_add_f16 v44, v44, v59
	v_pk_fma_f16 v33, v41, v61, v33
	v_pk_fma_f16 v32, v40, v60, v32
	v_pk_fma_f16 v31, v39, v59, v31
	v_pk_fma_f16 v30, v38, v58, v30
	v_pk_add_f16 v55, v75, v123 neg_lo:[0,1] neg_hi:[0,1]
	v_pk_add_f16 v56, v76, v124 neg_lo:[0,1] neg_hi:[0,1]
	v_pk_add_f16 v57, v77, v125 neg_lo:[0,1] neg_hi:[0,1]
	v_exp_f16_sdwa v58, v54 dst_sel:WORD_0 dst_unused:UNUSED_PAD src0_sel:WORD_0
	v_exp_f16_sdwa v59, v55 dst_sel:WORD_0 dst_unused:UNUSED_PAD src0_sel:WORD_0
	v_exp_f16_sdwa v60, v56 dst_sel:WORD_0 dst_unused:UNUSED_PAD src0_sel:WORD_0
	v_exp_f16_sdwa v61, v57 dst_sel:WORD_0 dst_unused:UNUSED_PAD src0_sel:WORD_0
	v_exp_f16_sdwa v58, v54 dst_sel:WORD_1 dst_unused:UNUSED_PRESERVE src0_sel:WORD_1
	v_exp_f16_sdwa v59, v55 dst_sel:WORD_1 dst_unused:UNUSED_PRESERVE src0_sel:WORD_1
	v_exp_f16_sdwa v60, v56 dst_sel:WORD_1 dst_unused:UNUSED_PRESERVE src0_sel:WORD_1
	v_exp_f16_sdwa v61, v57 dst_sel:WORD_1 dst_unused:UNUSED_PRESERVE src0_sel:WORD_1
	v_pk_add_f16 v54, v82, v122 neg_lo:[0,1] neg_hi:[0,1]
	v_pk_add_f16 v45, v45, v58
	v_pk_add_f16 v44, v44, v59
	v_pk_add_f16 v43, v43, v60
	v_pk_add_f16 v42, v42, v61
	v_pk_fma_f16 v30, v50, v58, v30
	v_pk_fma_f16 v31, v51, v59, v31
	v_pk_fma_f16 v32, v52, v60, v32
	v_pk_fma_f16 v33, v53, v61, v33
	v_pk_add_f16 v55, v83, v123 neg_lo:[0,1] neg_hi:[0,1]
	v_pk_add_f16 v56, v84, v124 neg_lo:[0,1] neg_hi:[0,1]
	v_pk_add_f16 v57, v85, v125 neg_lo:[0,1] neg_hi:[0,1]
	v_exp_f16_sdwa v58, v54 dst_sel:WORD_0 dst_unused:UNUSED_PAD src0_sel:WORD_0
	v_exp_f16_sdwa v59, v55 dst_sel:WORD_0 dst_unused:UNUSED_PAD src0_sel:WORD_0
	v_exp_f16_sdwa v60, v56 dst_sel:WORD_0 dst_unused:UNUSED_PAD src0_sel:WORD_0
	v_exp_f16_sdwa v61, v57 dst_sel:WORD_0 dst_unused:UNUSED_PAD src0_sel:WORD_0
	v_exp_f16_sdwa v58, v54 dst_sel:WORD_1 dst_unused:UNUSED_PRESERVE src0_sel:WORD_1
	v_exp_f16_sdwa v59, v55 dst_sel:WORD_1 dst_unused:UNUSED_PRESERVE src0_sel:WORD_1
	v_exp_f16_sdwa v60, v56 dst_sel:WORD_1 dst_unused:UNUSED_PRESERVE src0_sel:WORD_1
	v_exp_f16_sdwa v61, v57 dst_sel:WORD_1 dst_unused:UNUSED_PRESERVE src0_sel:WORD_1
	v_pk_add_f16 v45, v45, v58
	v_pk_add_f16 v44, v44, v59
	v_rcp_f16_e32 v54, v45
	v_rcp_f16_sdwa v45, v45 dst_sel:DWORD dst_unused:UNUSED_PAD src0_sel:WORD_1
	v_pk_add_f16 v43, v43, v60
	v_rcp_f16_e32 v55, v44
	v_rcp_f16_sdwa v44, v44 dst_sel:DWORD dst_unused:UNUSED_PAD src0_sel:WORD_1
	v_pk_add_f16 v42, v42, v61
	v_rcp_f16_e32 v56, v43
	v_rcp_f16_sdwa v43, v43 dst_sel:DWORD dst_unused:UNUSED_PAD src0_sel:WORD_1
	v_rcp_f16_e32 v57, v42
	v_rcp_f16_sdwa v42, v42 dst_sel:DWORD dst_unused:UNUSED_PAD src0_sel:WORD_1
	v_pk_fma_f16 v30, v70, v58, v30
	v_pack_b32_f16 v45, v54, v45
	v_pk_fma_f16 v31, v71, v59, v31
	v_pk_mul_f16 v45, v30, v45
	v_pack_b32_f16 v30, v55, v44
	v_pk_fma_f16 v32, v72, v60, v32
	v_pk_mul_f16 v44, v31, v30
	v_pack_b32_f16 v30, v56, v43
	v_pk_fma_f16 v33, v73, v61, v33
	v_pk_mul_f16 v43, v32, v30
	v_pack_b32_f16 v30, v57, v42
	v_pk_mul_f16 v42, v33, v30
	s_waitcnt vmcnt(0)
	v_pk_mul_f16 v30, v208, v154 op_sel_hi:[0,1]
	v_pk_mul_f16 v31, v208, v155 op_sel_hi:[0,1]
	v_pk_mul_f16 v32, v208, v156 op_sel_hi:[0,1]
	v_pk_mul_f16 v33, v208, v157 op_sel_hi:[0,1]
	v_pk_mul_f16 v54, v206, v154 op_sel_hi:[0,1]
	v_pk_mul_f16 v55, v206, v155 op_sel_hi:[0,1]
	v_pk_mul_f16 v56, v206, v156 op_sel_hi:[0,1]
	v_pk_mul_f16 v57, v206, v157 op_sel_hi:[0,1]
	v_pk_mul_f16 v58, v207, v154 op_sel_hi:[0,1]
	v_pk_mul_f16 v59, v207, v155 op_sel_hi:[0,1]
	v_pk_mul_f16 v60, v207, v156 op_sel_hi:[0,1]
	v_pk_mul_f16 v61, v207, v157 op_sel_hi:[0,1]
	v_pk_fma_f16 v37, v37, v157, v33
	v_pk_fma_f16 v36, v36, v156, v32
	v_pk_fma_f16 v35, v35, v155, v31
	v_pk_fma_f16 v34, v34, v154, v30
	v_pk_fma_f16 v49, v49, v157, v57
	v_pk_fma_f16 v48, v48, v156, v56
	v_pk_fma_f16 v47, v47, v155, v55
	v_pk_fma_f16 v46, v46, v154, v54
	v_pk_fma_f16 v62, v69, v157, v61
	v_pk_fma_f16 v63, v68, v156, v60
	v_pk_fma_f16 v64, v67, v155, v59
	v_pk_fma_f16 v65, v66, v154, v58
	v_pk_fma_f16 v66, v89, v157, v33
	v_pk_fma_f16 v67, v88, v156, v32
	v_pk_fma_f16 v68, v87, v155, v31
	v_pk_fma_f16 v69, v86, v154, v30
	v_pk_fma_f16 v74, v117, v157, v57
	v_pk_fma_f16 v75, v116, v156, v56
	v_pk_fma_f16 v76, v115, v155, v55
	v_pk_fma_f16 v77, v114, v154, v54
	v_pk_fma_f16 v78, v133, v157, v61
	v_pk_fma_f16 v79, v132, v156, v60
	v_pk_fma_f16 v80, v131, v155, v59
	v_pk_fma_f16 v81, v130, v154, v58
	v_pk_fma_f16 v61, v17, v157, v61
	v_pk_fma_f16 v60, v16, v156, v60
	v_pk_fma_f16 v59, v15, v155, v59
	v_pk_fma_f16 v58, v14, v154, v58
	v_pk_maximum3_f16 v14, v34, v46, v65
	v_pk_maximum3_f16 v15, v35, v47, v64
	v_pk_maximum3_f16 v16, v36, v48, v63
	v_pk_maximum3_f16 v17, v37, v49, v62
	v_pk_maximum3_f16 v82, v69, v77, v81
	v_pk_maximum3_f16 v83, v68, v76, v80
	v_pk_maximum3_f16 v84, v67, v75, v79
	v_pk_maximum3_f16 v85, v66, v74, v78
	v_pk_fma_f16 v33, v145, v157, v33
	v_pk_fma_f16 v32, v144, v156, v32
	v_pk_fma_f16 v31, v143, v155, v31
	v_pk_fma_f16 v30, v142, v154, v30
	v_pk_fma_f16 v57, v153, v157, v57
	v_pk_fma_f16 v56, v152, v156, v56
	v_pk_fma_f16 v55, v151, v155, v55
	v_pk_fma_f16 v54, v150, v154, v54
	v_pk_maximum3_f16 v87, v31, v55, v59
	v_pk_maximum3_f16 v88, v32, v56, v60
	v_pk_maximum3_f16 v89, v33, v57, v61
	v_pk_maximum3_f16 v86, v30, v54, v58
	v_pk_maximum3_f16 v15, v15, v83, v87
	v_pk_maximum3_f16 v16, v16, v84, v88
	v_pk_maximum3_f16 v17, v17, v85, v89
	v_pk_maximum3_f16 v14, v14, v82, v86
	v_xor_b32_e32 v82, 0x80008000, v17
	v_xor_b32_e32 v83, 0x80008000, v16
	v_xor_b32_e32 v84, 0x80008000, v15
	v_xor_b32_e32 v85, 0x80008000, v14
	v_pk_add_f16 v14, v34, v85
	v_pk_add_f16 v15, v35, v84
	v_pk_add_f16 v16, v36, v83
	v_pk_add_f16 v17, v37, v82
	v_exp_f16_sdwa v34, v14 dst_sel:WORD_0 dst_unused:UNUSED_PAD src0_sel:WORD_0
	v_exp_f16_sdwa v35, v15 dst_sel:WORD_0 dst_unused:UNUSED_PAD src0_sel:WORD_0
	v_exp_f16_sdwa v36, v16 dst_sel:WORD_0 dst_unused:UNUSED_PAD src0_sel:WORD_0
	v_exp_f16_sdwa v37, v17 dst_sel:WORD_0 dst_unused:UNUSED_PAD src0_sel:WORD_0
	v_exp_f16_sdwa v34, v14 dst_sel:WORD_1 dst_unused:UNUSED_PRESERVE src0_sel:WORD_1
	v_exp_f16_sdwa v35, v15 dst_sel:WORD_1 dst_unused:UNUSED_PRESERVE src0_sel:WORD_1
	v_exp_f16_sdwa v36, v16 dst_sel:WORD_1 dst_unused:UNUSED_PRESERVE src0_sel:WORD_1
	v_exp_f16_sdwa v37, v17 dst_sel:WORD_1 dst_unused:UNUSED_PRESERVE src0_sel:WORD_1
	v_pk_add_f16 v14, v34, 0
	v_pk_add_f16 v15, v35, 0
	v_pk_add_f16 v16, v36, 0
	v_pk_add_f16 v17, v37, 0
	v_pk_fma_f16 v18, v18, v34, 0
	v_pk_fma_f16 v19, v19, v35, 0
	v_pk_fma_f16 v20, v20, v36, 0
	v_pk_fma_f16 v21, v21, v37, 0
	v_pk_add_f16 v34, v46, v85
	v_pk_add_f16 v35, v47, v84
	v_pk_add_f16 v36, v48, v83
	v_pk_add_f16 v37, v49, v82
	v_exp_f16_sdwa v46, v34 dst_sel:WORD_0 dst_unused:UNUSED_PAD src0_sel:WORD_0
	v_exp_f16_sdwa v47, v35 dst_sel:WORD_0 dst_unused:UNUSED_PAD src0_sel:WORD_0
	v_exp_f16_sdwa v48, v36 dst_sel:WORD_0 dst_unused:UNUSED_PAD src0_sel:WORD_0
	v_exp_f16_sdwa v49, v37 dst_sel:WORD_0 dst_unused:UNUSED_PAD src0_sel:WORD_0
	v_exp_f16_sdwa v46, v34 dst_sel:WORD_1 dst_unused:UNUSED_PRESERVE src0_sel:WORD_1
	v_exp_f16_sdwa v47, v35 dst_sel:WORD_1 dst_unused:UNUSED_PRESERVE src0_sel:WORD_1
	v_exp_f16_sdwa v48, v36 dst_sel:WORD_1 dst_unused:UNUSED_PRESERVE src0_sel:WORD_1
	v_exp_f16_sdwa v49, v37 dst_sel:WORD_1 dst_unused:UNUSED_PRESERVE src0_sel:WORD_1
	s_nop 0
	v_pk_add_f16 v17, v17, v49
	v_pk_add_f16 v16, v16, v48
	v_pk_add_f16 v15, v15, v47
	v_pk_add_f16 v14, v14, v46
	v_pk_fma_f16 v21, v25, v49, v21
	v_pk_fma_f16 v20, v24, v48, v20
	v_pk_fma_f16 v19, v23, v47, v19
	v_pk_fma_f16 v18, v22, v46, v18
	v_pk_add_f16 v22, v65, v85
	v_pk_add_f16 v23, v64, v84
	v_pk_add_f16 v24, v63, v83
	v_pk_add_f16 v25, v62, v82
	v_exp_f16_sdwa v34, v22 dst_sel:WORD_0 dst_unused:UNUSED_PAD src0_sel:WORD_0
	v_exp_f16_sdwa v35, v23 dst_sel:WORD_0 dst_unused:UNUSED_PAD src0_sel:WORD_0
	v_exp_f16_sdwa v36, v24 dst_sel:WORD_0 dst_unused:UNUSED_PAD src0_sel:WORD_0
	v_exp_f16_sdwa v37, v25 dst_sel:WORD_0 dst_unused:UNUSED_PAD src0_sel:WORD_0
	v_exp_f16_sdwa v34, v22 dst_sel:WORD_1 dst_unused:UNUSED_PRESERVE src0_sel:WORD_1
	v_exp_f16_sdwa v35, v23 dst_sel:WORD_1 dst_unused:UNUSED_PRESERVE src0_sel:WORD_1
	v_exp_f16_sdwa v36, v24 dst_sel:WORD_1 dst_unused:UNUSED_PRESERVE src0_sel:WORD_1
	v_exp_f16_sdwa v37, v25 dst_sel:WORD_1 dst_unused:UNUSED_PRESERVE src0_sel:WORD_1
	v_pk_add_f16 v22, v69, v85
	v_pk_add_f16 v14, v14, v34
	v_pk_add_f16 v15, v15, v35
	v_pk_add_f16 v16, v16, v36
	v_pk_add_f16 v17, v17, v37
	v_pk_fma_f16 v18, v26, v34, v18
	v_pk_fma_f16 v19, v27, v35, v19
	v_pk_fma_f16 v20, v28, v36, v20
	v_pk_fma_f16 v21, v29, v37, v21
	v_pk_add_f16 v23, v68, v84
	v_pk_add_f16 v24, v67, v83
	v_pk_add_f16 v25, v66, v82
	v_exp_f16_sdwa v26, v22 dst_sel:WORD_0 dst_unused:UNUSED_PAD src0_sel:WORD_0
	v_exp_f16_sdwa v27, v23 dst_sel:WORD_0 dst_unused:UNUSED_PAD src0_sel:WORD_0
	v_exp_f16_sdwa v28, v24 dst_sel:WORD_0 dst_unused:UNUSED_PAD src0_sel:WORD_0
	v_exp_f16_sdwa v29, v25 dst_sel:WORD_0 dst_unused:UNUSED_PAD src0_sel:WORD_0
	v_exp_f16_sdwa v26, v22 dst_sel:WORD_1 dst_unused:UNUSED_PRESERVE src0_sel:WORD_1
	v_exp_f16_sdwa v27, v23 dst_sel:WORD_1 dst_unused:UNUSED_PRESERVE src0_sel:WORD_1
	v_exp_f16_sdwa v28, v24 dst_sel:WORD_1 dst_unused:UNUSED_PRESERVE src0_sel:WORD_1
	v_exp_f16_sdwa v29, v25 dst_sel:WORD_1 dst_unused:UNUSED_PRESERVE src0_sel:WORD_1
	v_pk_add_f16 v22, v77, v85
	v_pk_add_f16 v17, v17, v29
	v_pk_add_f16 v16, v16, v28
	v_pk_add_f16 v15, v15, v27
	v_pk_add_f16 v14, v14, v26
	v_pk_fma_f16 v21, v41, v29, v21
	v_pk_fma_f16 v20, v40, v28, v20
	v_pk_fma_f16 v19, v39, v27, v19
	v_pk_fma_f16 v18, v38, v26, v18
	v_pk_add_f16 v23, v76, v84
	v_pk_add_f16 v24, v75, v83
	v_pk_add_f16 v25, v74, v82
	v_exp_f16_sdwa v26, v22 dst_sel:WORD_0 dst_unused:UNUSED_PAD src0_sel:WORD_0
	v_exp_f16_sdwa v27, v23 dst_sel:WORD_0 dst_unused:UNUSED_PAD src0_sel:WORD_0
	v_exp_f16_sdwa v28, v24 dst_sel:WORD_0 dst_unused:UNUSED_PAD src0_sel:WORD_0
	v_exp_f16_sdwa v29, v25 dst_sel:WORD_0 dst_unused:UNUSED_PAD src0_sel:WORD_0
	v_exp_f16_sdwa v26, v22 dst_sel:WORD_1 dst_unused:UNUSED_PRESERVE src0_sel:WORD_1
	v_exp_f16_sdwa v27, v23 dst_sel:WORD_1 dst_unused:UNUSED_PRESERVE src0_sel:WORD_1
	v_exp_f16_sdwa v28, v24 dst_sel:WORD_1 dst_unused:UNUSED_PRESERVE src0_sel:WORD_1
	v_exp_f16_sdwa v29, v25 dst_sel:WORD_1 dst_unused:UNUSED_PRESERVE src0_sel:WORD_1
	v_pk_add_f16 v22, v81, v85
	v_pk_add_f16 v14, v14, v26
	v_pk_add_f16 v15, v15, v27
	v_pk_add_f16 v16, v16, v28
	v_pk_add_f16 v17, v17, v29
	v_pk_fma_f16 v18, v50, v26, v18
	v_pk_fma_f16 v19, v51, v27, v19
	v_pk_fma_f16 v20, v52, v28, v20
	v_pk_fma_f16 v21, v53, v29, v21
	v_pk_add_f16 v23, v80, v84
	v_pk_add_f16 v24, v79, v83
	v_pk_add_f16 v25, v78, v82
	v_exp_f16_sdwa v26, v22 dst_sel:WORD_0 dst_unused:UNUSED_PAD src0_sel:WORD_0
	v_exp_f16_sdwa v27, v23 dst_sel:WORD_0 dst_unused:UNUSED_PAD src0_sel:WORD_0
	v_exp_f16_sdwa v28, v24 dst_sel:WORD_0 dst_unused:UNUSED_PAD src0_sel:WORD_0
	v_exp_f16_sdwa v29, v25 dst_sel:WORD_0 dst_unused:UNUSED_PAD src0_sel:WORD_0
	v_exp_f16_sdwa v26, v22 dst_sel:WORD_1 dst_unused:UNUSED_PRESERVE src0_sel:WORD_1
	v_exp_f16_sdwa v27, v23 dst_sel:WORD_1 dst_unused:UNUSED_PRESERVE src0_sel:WORD_1
	v_exp_f16_sdwa v28, v24 dst_sel:WORD_1 dst_unused:UNUSED_PRESERVE src0_sel:WORD_1
	v_exp_f16_sdwa v29, v25 dst_sel:WORD_1 dst_unused:UNUSED_PRESERVE src0_sel:WORD_1
	v_pk_add_f16 v22, v30, v85
	v_pk_add_f16 v17, v17, v29
	v_pk_add_f16 v16, v16, v28
	v_pk_add_f16 v15, v15, v27
	v_pk_add_f16 v14, v14, v26
	v_pk_fma_f16 v21, v73, v29, v21
	v_pk_fma_f16 v20, v72, v28, v20
	v_pk_fma_f16 v19, v71, v27, v19
	v_pk_fma_f16 v18, v70, v26, v18
	v_pk_add_f16 v23, v31, v84
	v_pk_add_f16 v24, v32, v83
	v_pk_add_f16 v25, v33, v82
	v_exp_f16_sdwa v26, v22 dst_sel:WORD_0 dst_unused:UNUSED_PAD src0_sel:WORD_0
	v_exp_f16_sdwa v27, v23 dst_sel:WORD_0 dst_unused:UNUSED_PAD src0_sel:WORD_0
	v_exp_f16_sdwa v28, v24 dst_sel:WORD_0 dst_unused:UNUSED_PAD src0_sel:WORD_0
	v_exp_f16_sdwa v29, v25 dst_sel:WORD_0 dst_unused:UNUSED_PAD src0_sel:WORD_0
	v_exp_f16_sdwa v26, v22 dst_sel:WORD_1 dst_unused:UNUSED_PRESERVE src0_sel:WORD_1
	v_exp_f16_sdwa v27, v23 dst_sel:WORD_1 dst_unused:UNUSED_PRESERVE src0_sel:WORD_1
	v_exp_f16_sdwa v28, v24 dst_sel:WORD_1 dst_unused:UNUSED_PRESERVE src0_sel:WORD_1
	v_exp_f16_sdwa v29, v25 dst_sel:WORD_1 dst_unused:UNUSED_PRESERVE src0_sel:WORD_1
	v_pk_add_f16 v22, v54, v85
	v_pk_add_f16 v14, v14, v26
	v_pk_add_f16 v15, v15, v27
	v_pk_add_f16 v16, v16, v28
	v_pk_add_f16 v17, v17, v29
	v_pk_fma_f16 v18, v90, v26, v18
	v_pk_fma_f16 v19, v91, v27, v19
	v_pk_fma_f16 v20, v92, v28, v20
	v_pk_fma_f16 v21, v93, v29, v21
	v_pk_add_f16 v23, v55, v84
	v_pk_add_f16 v24, v56, v83
	v_pk_add_f16 v25, v57, v82
	v_exp_f16_sdwa v26, v22 dst_sel:WORD_0 dst_unused:UNUSED_PAD src0_sel:WORD_0
	v_exp_f16_sdwa v27, v23 dst_sel:WORD_0 dst_unused:UNUSED_PAD src0_sel:WORD_0
	v_exp_f16_sdwa v28, v24 dst_sel:WORD_0 dst_unused:UNUSED_PAD src0_sel:WORD_0
	v_exp_f16_sdwa v29, v25 dst_sel:WORD_0 dst_unused:UNUSED_PAD src0_sel:WORD_0
	v_exp_f16_sdwa v26, v22 dst_sel:WORD_1 dst_unused:UNUSED_PRESERVE src0_sel:WORD_1
	v_exp_f16_sdwa v27, v23 dst_sel:WORD_1 dst_unused:UNUSED_PRESERVE src0_sel:WORD_1
	v_exp_f16_sdwa v28, v24 dst_sel:WORD_1 dst_unused:UNUSED_PRESERVE src0_sel:WORD_1
	v_exp_f16_sdwa v29, v25 dst_sel:WORD_1 dst_unused:UNUSED_PRESERVE src0_sel:WORD_1
	s_nop 0
	v_pk_add_f16 v17, v17, v29
	v_pk_add_f16 v16, v16, v28
	v_pk_add_f16 v15, v15, v27
	v_pk_add_f16 v14, v14, v26
	v_pk_fma_f16 v21, v113, v29, v21
	v_pk_fma_f16 v20, v112, v28, v20
	v_pk_fma_f16 v19, v111, v27, v19
	v_pk_fma_f16 v18, v110, v26, v18
	v_pk_add_f16 v26, v58, v85
	v_pk_add_f16 v27, v59, v84
	v_pk_add_f16 v28, v60, v83
	v_pk_add_f16 v29, v61, v82
	v_exp_f16_sdwa v22, v26 dst_sel:WORD_0 dst_unused:UNUSED_PAD src0_sel:WORD_0
	v_exp_f16_sdwa v23, v27 dst_sel:WORD_0 dst_unused:UNUSED_PAD src0_sel:WORD_0
	v_exp_f16_sdwa v24, v28 dst_sel:WORD_0 dst_unused:UNUSED_PAD src0_sel:WORD_0
	v_exp_f16_sdwa v25, v29 dst_sel:WORD_0 dst_unused:UNUSED_PAD src0_sel:WORD_0
	v_exp_f16_sdwa v22, v26 dst_sel:WORD_1 dst_unused:UNUSED_PRESERVE src0_sel:WORD_1
	v_exp_f16_sdwa v23, v27 dst_sel:WORD_1 dst_unused:UNUSED_PRESERVE src0_sel:WORD_1
	v_exp_f16_sdwa v24, v28 dst_sel:WORD_1 dst_unused:UNUSED_PRESERVE src0_sel:WORD_1
	v_exp_f16_sdwa v25, v29 dst_sel:WORD_1 dst_unused:UNUSED_PRESERVE src0_sel:WORD_1
	s_nop 0
.LBB4_118:
	s_and_b64 vcc, exec, s[4:5]
	s_cbranch_vccz .LBB4_3
	global_load_dwordx3 v[146:148], v169, s[16:17]
	s_mov_b32 s14, s38
	s_mov_b32 s15, s39
	v_cmp_lt_u32_e64 s[64:65], 0, v199
	v_cmp_gt_u32_e64 s[66:67], 63, v199
	v_cmp_lt_u32_e64 s[68:69], 0, v180
	v_cmp_gt_u32_e64 s[70:71], 60, v180
	buffer_load_dwordx4 v[162:165], v200, s[12:15], 0 offen nt
	s_and_b64 s[72:73], s[68:69], s[64:65]
	s_and_b64 s[74:75], s[68:69], s[66:67]
	s_and_b64 s[76:77], s[70:71], s[64:65]
	s_and_b64 s[78:79], s[70:71], s[66:67]
	v_add_u32_e32 v245, 0xfffe7c00, v200
	v_add_u32_e32 v246, 0xfffe8000, v200
	s_mov_b64 exec, s[72:73]
	buffer_load_dwordx4 v[114:117], v245, s[12:15], 0 offen
	buffer_load_dwordx4 v[70:73], v245, s[12:15], 0 offen offset:512
	s_mov_b64 exec, -1
	s_mov_b64 exec, s[68:69]
	buffer_load_dwordx4 v[130:133], v246, s[12:15], 0 offen offset:512
	buffer_load_dwordx4 v[94:97], v246, s[12:15], 0 offen offset:1024
	s_mov_b64 exec, -1
	s_mov_b64 exec, s[74:75]
	buffer_load_dwordx4 v[138:141], v246, s[12:15], 0 offen offset:2048
	buffer_load_dwordx4 v[118:121], v246, s[12:15], 0 offen offset:2560
	s_mov_b64 exec, -1
	v_add_u32_e32 v245, 0xfffffc00, v200
	s_mov_b64 exec, s[64:65]
	buffer_load_dwordx4 v[86:89], v245, s[12:15], 0 offen
	buffer_load_dwordx4 v[42:45], v245, s[12:15], 0 offen offset:512
	s_mov_b64 exec, -1
	buffer_load_dwordx4 v[110:113], v200, s[12:15], 0 offen offset:512
	buffer_load_dwordx4 v[66:69], v200, s[12:15], 0 offen offset:1024
	s_mov_b64 exec, s[66:67]
	buffer_load_dwordx4 v[126:129], v200, s[12:15], 0 offen offset:2048
	buffer_load_dwordx4 v[90:93], v200, s[12:15], 0 offen offset:2560
	s_mov_b64 exec, -1
	v_add_u32_e32 v245, 0x17c00, v200
	v_add_u32_e32 v246, 0x18000, v200
	s_mov_b64 exec, s[64:65]
	buffer_load_dwordx4 v[54:57], v245, s[12:15], 0 offen
	buffer_load_dwordx4 v[22:25], v245, s[12:15], 0 offen offset:512
	s_mov_b64 exec, -1
	buffer_load_dwordx4 v[74:77], v246, s[12:15], 0 offen offset:512
	buffer_load_dwordx4 v[34:37], v246, s[12:15], 0 offen offset:1024
	s_mov_b64 exec, s[66:67]
	buffer_load_dwordx4 v[98:101], v246, s[12:15], 0 offen offset:2048
	buffer_load_dwordx4 v[50:53], v246, s[12:15], 0 offen offset:2560
	s_mov_b64 exec, -1
	v_add_u32_e32 v245, 0x18000, v200
	buffer_load_dwordx4 v[154:157], v245, s[12:15], 0 offen nt
	v_add_u32_e32 v246, 0x30000, v200
	buffer_load_dwordx4 v[150:153], v246, s[12:15], 0 offen nt
	v_add_u32_e32 v245, 0x2fc00, v200
	v_add_u32_e32 v246, 0x30000, v200
	v_add_u32_e32 v247, 0x47c00, v200
	v_add_u32_e32 v248, 0x48000, v200
	v_add_u32_e32 v249, 0x5fc00, v200
	v_add_u32_e32 v250, 0x60000, v200
	s_waitcnt vmcnt(22)
	v_cvt_pk_f16_f32 v6, v2, v3
	v_cvt_pk_f16_f32 v2, v8, v9
	v_cvt_pk_f16_f32 v7, v4, v5
	v_cvt_pk_f16_f32 v3, v10, v11
	v_cvt_pk_f16_f32 v8, v12, v13
	v_cvt_pk_f16_f32 v4, v16, v17
	v_cvt_pk_f16_f32 v9, v14, v15
	v_cvt_pk_f16_f32 v5, v18, v19
	s_not_b64 exec, s[72:73]
	s_cbranch_execz .Lmyf_C4_0
	v_mov_b32_e32 v114, v6
	v_mov_b32_e32 v115, v7
	v_mov_b32_e32 v116, v8
	v_mov_b32_e32 v117, v9
	v_mov_b32_e32 v70, v2
	v_mov_b32_e32 v71, v3
	v_mov_b32_e32 v72, v4
	v_mov_b32_e32 v73, v5

.Lmyf_C4_7:
	s_mov_b64 exec, -1
	s_waitcnt vmcnt(21)
	v_cvt_f16_f32_e32 v158, v147
	v_cvt_f16_f32_e32 v160, v146
	v_cvt_f16_f32_e32 v159, v148
	v_add_u32_e32 v251, 0x48000, v200
	buffer_load_dwordx4 v[146:149], v251, s[12:15], 0 offen nt
	s_branch .LBB4_2

.LBB5_4:
	v_add_u32_e32 v182, s30, v161
	v_add_u32_e32 v181, -1, v182
	v_or_b32_e32 v2, v181, v164
	v_add_u32_e32 v180, 0x18400, v171
	v_cmp_gt_u32_e64 s[0:1], 64, v2
	s_mov_b64 s[4:5], -1
	s_and_b64 vcc, exec, s[24:25]
	s_cbranch_vccz .LBB5_42
	s_load_dwordx2 s[4:5], s[22:23], 0x20
	s_waitcnt lgkmcnt(0)
	s_load_dwordx2 s[26:27], s[4:5], 0x0
	s_load_dword s31, s[4:5], 0x8
	v_cmp_lt_u32_e64 s[64:65], 0, v182
	v_cmp_gt_u32_e64 s[66:67], 63, v182
	v_cmp_lt_u32_e64 s[68:69], 0, v162
	v_cmp_gt_u32_e64 s[70:71], 60, v162
	buffer_load_dwordx4 v[186:189], v180, s[16:19], 0 offen nt
	s_and_b64 s[72:73], s[68:69], s[64:65]
	s_and_b64 s[74:75], s[68:69], s[66:67]
	s_and_b64 s[76:77], s[70:71], s[64:65]
	s_and_b64 s[78:79], s[70:71], s[66:67]
	v_add_u32_e32 v224, 0xfffe7c00, v180
	v_add_u32_e32 v225, 0xfffe8000, v180
	s_mov_b64 exec, s[72:73]
	buffer_load_dwordx4 v[110:113], v224, s[16:19], 0 offen
	buffer_load_dwordx4 v[70:73], v224, s[16:19], 0 offen offset:512
	s_mov_b64 exec, -1
	s_mov_b64 exec, s[68:69]
	buffer_load_dwordx4 v[126:129], v225, s[16:19], 0 offen offset:512
	buffer_load_dwordx4 v[98:101], v225, s[16:19], 0 offen offset:1024
	s_mov_b64 exec, -1
	s_mov_b64 exec, s[74:75]
	buffer_load_dwordx4 v[134:137], v225, s[16:19], 0 offen offset:2048
	buffer_load_dwordx4 v[114:117], v225, s[16:19], 0 offen offset:2560
	s_mov_b64 exec, -1
	v_add_u32_e32 v224, 0xfffffc00, v180
	s_mov_b64 exec, s[64:65]
	buffer_load_dwordx4 v[82:85], v224, s[16:19], 0 offen
	buffer_load_dwordx4 v[42:45], v224, s[16:19], 0 offen offset:512
	s_mov_b64 exec, -1
	buffer_load_dwordx4 v[106:109], v180, s[16:19], 0 offen offset:512
	buffer_load_dwordx4 v[62:65], v180, s[16:19], 0 offen offset:1024
	s_mov_b64 exec, s[66:67]
	buffer_load_dwordx4 v[122:125], v180, s[16:19], 0 offen offset:2048
	buffer_load_dwordx4 v[86:89], v180, s[16:19], 0 offen offset:2560
	s_mov_b64 exec, -1
	v_add_u32_e32 v224, 0x17c00, v180
	v_add_u32_e32 v225, 0x18000, v180
	s_mov_b64 exec, s[64:65]
	buffer_load_dwordx4 v[50:53], v224, s[16:19], 0 offen
	buffer_load_dwordx4 v[22:25], v224, s[16:19], 0 offen offset:512
	s_mov_b64 exec, -1
	buffer_load_dwordx4 v[66:69], v225, s[16:19], 0 offen offset:512
	buffer_load_dwordx4 v[30:33], v225, s[16:19], 0 offen offset:1024
	s_mov_b64 exec, s[66:67]
	buffer_load_dwordx4 v[94:97], v225, s[16:19], 0 offen offset:2048
	buffer_load_dwordx4 v[46:49], v225, s[16:19], 0 offen offset:2560
	s_mov_b64 exec, -1
	v_add_u32_e32 v224, 0x18000, v180
	buffer_load_dwordx4 v[154:157], v224, s[16:19], 0 offen nt
	v_add_u32_e32 v225, 0x30000, v180
	buffer_load_dwordx4 v[150:153], v225, s[16:19], 0 offen nt
	v_add_u32_e32 v224, 0x48000, v180
	buffer_load_dwordx4 v[146:149], v224, s[16:19], 0 offen nt
	v_add_u32_e32 v224, 0x2fc00, v180
	v_add_u32_e32 v225, 0x30000, v180
	v_add_u32_e32 v226, 0x47c00, v180
	v_add_u32_e32 v227, 0x48000, v180
	v_add_u32_e32 v228, 0x5fc00, v180
	v_add_u32_e32 v229, 0x60000, v180
	s_cmp_lg_u32 s93, 0
	s_cbranch_scc1 .Lmybg_D1
	s_waitcnt vmcnt(22)
	v_cvt_pk_f16_f32 v172, v230, v231
	v_cvt_pk_f16_f32 v173, v234, v235
	v_cvt_pk_f16_f32 v174, v232, v233
	v_cvt_pk_f16_f32 v175, v236, v237
	v_cvt_pk_f16_f32 v176, v238, v239
	v_cvt_pk_f16_f32 v177, v242, v243
	v_cvt_pk_f16_f32 v178, v240, v241
	v_cvt_pk_f16_f32 v179, v244, v245
	s_mov_b32 s93, 1

.LBB5_42:
	s_and_b64 vcc, exec, s[4:5]
	s_cbranch_vccz .LBB5_3
	s_load_dwordx2 s[0:1], s[22:23], 0x18
	s_waitcnt lgkmcnt(0)
	s_load_dwordx2 s[6:7], s[0:1], 0x0
	s_load_dword s28, s[0:1], 0x8
	v_cmp_lt_u32_e64 s[64:65], 0, v182
	v_cmp_gt_u32_e64 s[66:67], 63, v182
	v_cmp_lt_u32_e64 s[68:69], 0, v162
	v_cmp_gt_u32_e64 s[70:71], 60, v162
	buffer_load_dwordx4 v[184:187], v180, s[16:19], 0 offen nt
	s_and_b64 s[72:73], s[68:69], s[64:65]
	s_and_b64 s[74:75], s[68:69], s[66:67]
	s_and_b64 s[76:77], s[70:71], s[64:65]
	s_and_b64 s[78:79], s[70:71], s[66:67]
	v_add_u32_e32 v224, 0xfffe7c00, v180
	v_add_u32_e32 v225, 0xfffe8000, v180
	s_mov_b64 exec, s[72:73]
	buffer_load_dwordx4 v[110:113], v224, s[16:19], 0 offen
	buffer_load_dwordx4 v[78:81], v224, s[16:19], 0 offen offset:512
	s_mov_b64 exec, -1
	s_mov_b64 exec, s[68:69]
	buffer_load_dwordx4 v[126:129], v225, s[16:19], 0 offen offset:512
	buffer_load_dwordx4 v[102:105], v225, s[16:19], 0 offen offset:1024
	s_mov_b64 exec, -1
	s_mov_b64 exec, s[74:75]
	buffer_load_dwordx4 v[134:137], v225, s[16:19], 0 offen offset:2048
	buffer_load_dwordx4 v[114:117], v225, s[16:19], 0 offen offset:2560
	s_mov_b64 exec, -1
	v_add_u32_e32 v224, 0xfffffc00, v180
	s_mov_b64 exec, s[64:65]
	buffer_load_dwordx4 v[82:85], v224, s[16:19], 0 offen
	buffer_load_dwordx4 v[42:45], v224, s[16:19], 0 offen offset:512
	s_mov_b64 exec, -1
	buffer_load_dwordx4 v[106:109], v180, s[16:19], 0 offen offset:512
	buffer_load_dwordx4 v[62:65], v180, s[16:19], 0 offen offset:1024
	s_mov_b64 exec, s[66:67]
	buffer_load_dwordx4 v[122:125], v180, s[16:19], 0 offen offset:2048
	buffer_load_dwordx4 v[86:89], v180, s[16:19], 0 offen offset:2560
	s_mov_b64 exec, -1
	v_add_u32_e32 v224, 0x17c00, v180
	v_add_u32_e32 v225, 0x18000, v180
	s_mov_b64 exec, s[64:65]
	buffer_load_dwordx4 v[50:53], v224, s[16:19], 0 offen
	buffer_load_dwordx4 v[22:25], v224, s[16:19], 0 offen offset:512
	s_mov_b64 exec, -1
	buffer_load_dwordx4 v[66:69], v225, s[16:19], 0 offen offset:512
	buffer_load_dwordx4 v[34:37], v225, s[16:19], 0 offen offset:1024
	s_mov_b64 exec, s[66:67]
	buffer_load_dwordx4 v[94:97], v225, s[16:19], 0 offen offset:2048
	buffer_load_dwordx4 v[46:49], v225, s[16:19], 0 offen offset:2560
	s_mov_b64 exec, -1
	v_add_u32_e32 v224, 0x18000, v180
	buffer_load_dwordx4 v[154:157], v224, s[16:19], 0 offen nt
	v_add_u32_e32 v225, 0x30000, v180
	buffer_load_dwordx4 v[150:153], v225, s[16:19], 0 offen nt
	v_add_u32_e32 v224, 0x48000, v180
	buffer_load_dwordx4 v[146:149], v224, s[16:19], 0 offen nt
	v_add_u32_e32 v224, 0x2fc00, v180
	v_add_u32_e32 v225, 0x30000, v180
	v_add_u32_e32 v226, 0x47c00, v180
	v_add_u32_e32 v227, 0x48000, v180
	v_add_u32_e32 v228, 0x5fc00, v180
	v_add_u32_e32 v229, 0x60000, v180
	s_cmp_lg_u32 s93, 0
	s_cbranch_scc1 .Lmybg_D2
	s_waitcnt vmcnt(22)
	v_cvt_pk_f16_f32 v172, v230, v231
	v_cvt_pk_f16_f32 v173, v234, v235
	v_cvt_pk_f16_f32 v174, v232, v233
	v_cvt_pk_f16_f32 v175, v236, v237
	v_cvt_pk_f16_f32 v176, v238, v239
	v_cvt_pk_f16_f32 v177, v242, v243
	v_cvt_pk_f16_f32 v178, v240, v241
	v_cvt_pk_f16_f32 v179, v244, v245
	s_mov_b32 s93, 1

_Z7k_attn2ILi2EEv8AttnArgs:
	v_readfirstlane_b32 s3, v0
	s_lshl_b32 s12, s3, 1
	v_lshlrev_b32_e32 v3, 3, v0
	s_and_b32 s12, s12, 0x80
	v_and_b32_e32 v3, 0x78, v3
	s_load_dwordx4 s[8:11], s[0:1], 0x0
	s_load_dwordx2 s[4:5], s[0:1], 0x10
	s_load_dwordx2 s[6:7], s[0:1], 0x50
	v_or_b32_e32 v180, s12, v3
	s_lshl_b32 s12, s2, 5
	v_lshrrev_b32_e32 v1, 5, v0
	v_bfe_u32 v2, v0, 4, 2
	s_and_b32 s14, s12, 0xe0
	s_lshr_b32 s12, s2, 3
	v_lshrrev_b32_e32 v0, 6, v0
	v_and_b32_e32 v1, 4, v1
	s_add_i32 s14, s14, s12
	s_and_b32 s2, s2, 56
	v_and_b32_e32 v0, 4, v0
	v_and_or_b32 v181, s14, 56, v0
	v_or3_b32 v182, v2, s2, v1
	s_and_b32 s2, s14, 0x3ffffc0
	v_or_b32_e32 v4, s2, v181
	v_lshlrev_b32_e32 v0, 1, v180
	v_mov_b32_e32 v1, 0
	s_waitcnt lgkmcnt(0)
	v_lshl_add_u64 v[2:3], s[6:7], 0, v[0:1]
	v_lshl_or_b32 v0, v4, 6, v182
	v_lshlrev_b64 v[4:5], 9, v[0:1]
	v_lshl_add_u64 v[8:9], v[2:3], 0, v[4:5]
	v_or_b32_e32 v4, 64, v0
	v_mov_b32_e32 v5, v1
	v_lshlrev_b64 v[4:5], 9, v[4:5]
	v_lshlrev_b32_e32 v20, 2, v180
	v_lshl_add_u64 v[10:11], v[2:3], 0, v[4:5]
	global_load_dwordx4 v[240:243], v20, s[10:11] offset:16
	global_load_dwordx4 v[236:239], v20, s[10:11]
	global_load_dwordx4 v[248:251], v20, s[4:5] offset:16
	global_load_dwordx4 v[244:247], v20, s[4:5]
	global_load_dwordx4 v[12:15], v[8:9], off nt
	global_load_dwordx4 v[4:7], v[10:11], off nt
	v_or_b32_e32 v8, 0x80, v0
	v_mov_b32_e32 v9, v1
	v_lshlrev_b64 v[8:9], 9, v[8:9]
	v_or_b32_e32 v0, 0xc0, v0
	v_lshl_add_u64 v[20:21], v[2:3], 0, v[8:9]
	v_lshlrev_b64 v[0:1], 9, v[0:1]
	v_lshl_add_u64 v[34:35], v[2:3], 0, v[0:1]
	global_load_dwordx4 v[8:11], v[20:21], off nt
	global_load_dwordx4 v[0:3], v[34:35], off nt
	s_bitcmp1_b32 s3, 6
	s_cselect_b64 s[4:5], -1, 0
	s_and_b32 s2, s14, 0x3ffc0
	v_or_b32_e32 v20, s2, v181
	v_lshl_or_b32 v20, v20, 6, v182
	v_add_u32_e32 v184, -1, v182
	v_add_u32_e32 v185, -1, v181
	v_mul_u32_u24_e32 v20, 0x300, v20
	v_or_b32_e32 v34, v185, v184
	v_or_b32_e32 v20, v180, v20
	s_mov_b32 s11, 0x20000
	s_mov_b32 s10, 0x1800000
	s_and_b32 s9, s9, 0xffff
	v_lshlrev_b32_e32 v183, 1, v20
	v_cmp_gt_u32_e64 s[2:3], 64, v34
	s_and_b64 vcc, exec, s[4:5]
	s_cbranch_vccz .LBB6_38
	s_load_dwordx2 s[12:13], s[0:1], 0x20
	s_waitcnt lgkmcnt(0)
	s_load_dwordx2 s[4:5], s[12:13], 0x0
	s_load_dword s12, s[12:13], 0x8
	v_cmp_lt_u32_e64 s[64:65], 0, v182
	v_cmp_gt_u32_e64 s[66:67], 63, v182
	v_cmp_lt_u32_e64 s[68:69], 0, v181
	v_cmp_gt_u32_e64 s[70:71], 60, v181
	buffer_load_dwordx4 v[190:193], v183, s[8:11], 0 offen nt
	s_and_b64 s[72:73], s[68:69], s[64:65]
	s_and_b64 s[74:75], s[68:69], s[66:67]
	s_and_b64 s[76:77], s[70:71], s[64:65]
	s_and_b64 s[78:79], s[70:71], s[66:67]
	v_add_u32_e32 v228, 0xfffe7c00, v183
	v_add_u32_e32 v229, 0xfffe8000, v183
	s_mov_b64 exec, s[72:73]
	buffer_load_dwordx4 v[136:139], v228, s[8:11], 0 offen
	buffer_load_dwordx4 v[96:99], v228, s[8:11], 0 offen offset:512
	s_mov_b64 exec, -1
	s_mov_b64 exec, s[68:69]
	buffer_load_dwordx4 v[152:155], v229, s[8:11], 0 offen offset:512
	buffer_load_dwordx4 v[124:127], v229, s[8:11], 0 offen offset:1024
	s_mov_b64 exec, -1
	s_mov_b64 exec, s[74:75]
	buffer_load_dwordx4 v[160:163], v229, s[8:11], 0 offen offset:2048
	buffer_load_dwordx4 v[140:143], v229, s[8:11], 0 offen offset:2560
	s_mov_b64 exec, -1
	v_add_u32_e32 v228, 0xfffffc00, v183
	s_mov_b64 exec, s[64:65]
	buffer_load_dwordx4 v[112:115], v228, s[8:11], 0 offen
	buffer_load_dwordx4 v[68:71], v228, s[8:11], 0 offen offset:512
	s_mov_b64 exec, -1
	buffer_load_dwordx4 v[132:135], v183, s[8:11], 0 offen offset:512
	buffer_load_dwordx4 v[88:91], v183, s[8:11], 0 offen offset:1024
	s_mov_b64 exec, s[66:67]
	buffer_load_dwordx4 v[148:151], v183, s[8:11], 0 offen offset:2048
	buffer_load_dwordx4 v[108:111], v183, s[8:11], 0 offen offset:2560
	s_mov_b64 exec, -1
	v_add_u32_e32 v228, 0x17c00, v183
	v_add_u32_e32 v229, 0x18000, v183
	s_mov_b64 exec, s[64:65]
	buffer_load_dwordx4 v[76:79], v228, s[8:11], 0 offen
	buffer_load_dwordx4 v[48:51], v228, s[8:11], 0 offen offset:512
	s_mov_b64 exec, -1
	buffer_load_dwordx4 v[92:95], v229, s[8:11], 0 offen offset:512
	buffer_load_dwordx4 v[56:59], v229, s[8:11], 0 offen offset:1024
	s_mov_b64 exec, s[66:67]
	buffer_load_dwordx4 v[116:119], v229, s[8:11], 0 offen offset:2048
	buffer_load_dwordx4 v[72:75], v229, s[8:11], 0 offen offset:2560
	s_mov_b64 exec, -1
	v_add_u32_e32 v228, 0x18000, v183
	buffer_load_dwordx4 v[176:179], v228, s[8:11], 0 offen nt
	v_add_u32_e32 v229, 0x30000, v183
	buffer_load_dwordx4 v[172:175], v229, s[8:11], 0 offen nt
	v_add_u32_e32 v228, 0x48000, v183
	buffer_load_dwordx4 v[168:171], v228, s[8:11], 0 offen nt
	v_add_u32_e32 v228, 0x2fc00, v183
	v_add_u32_e32 v229, 0x30000, v183
	v_add_u32_e32 v230, 0x47c00, v183
	v_add_u32_e32 v231, 0x48000, v183
	v_add_u32_e32 v232, 0x5fc00, v183
	v_add_u32_e32 v233, 0x60000, v183
	s_waitcnt vmcnt(26)
	v_cvt_pk_f16_f32 v22, v240, v241
	v_cvt_pk_f16_f32 v20, v236, v237
	v_cvt_pk_f16_f32 v21, v238, v239
	v_cvt_pk_f16_f32 v16, v244, v245
	v_cvt_pk_f16_f32 v17, v246, v247
	v_cvt_pk_f16_f32 v18, v248, v249
	v_cvt_pk_f16_f32 v23, v242, v243
	v_cvt_pk_f16_f32 v19, v250, v251
	s_not_b64 exec, s[72:73]
	s_cbranch_execz .Lmyf_E1_0
	v_mov_b32_e32 v136, v20
	v_mov_b32_e32 v137, v21
	v_mov_b32_e32 v138, v22
	v_mov_b32_e32 v139, v23
	v_mov_b32_e32 v96, v16
	v_mov_b32_e32 v97, v17
	v_mov_b32_e32 v98, v18
	v_mov_b32_e32 v99, v19

.LBB6_38:
	s_load_dwordx2 s[12:13], s[0:1], 0x60
	s_cbranch_execz .LBB6_76
	s_load_dwordx2 s[2:3], s[0:1], 0x18
	s_waitcnt lgkmcnt(0)
	s_load_dwordx2 s[0:1], s[2:3], 0x0
	s_load_dword s4, s[2:3], 0x8
	v_cmp_lt_u32_e64 s[64:65], 0, v182
	v_cmp_gt_u32_e64 s[66:67], 63, v182
	v_cmp_lt_u32_e64 s[68:69], 0, v181
	v_cmp_gt_u32_e64 s[70:71], 60, v181
	buffer_load_dwordx4 v[168:171], v183, s[8:11], 0 offen nt
	s_and_b64 s[72:73], s[68:69], s[64:65]
	s_and_b64 s[74:75], s[68:69], s[66:67]
	s_and_b64 s[76:77], s[70:71], s[64:65]
	s_and_b64 s[78:79], s[70:71], s[66:67]
	v_add_u32_e32 v228, 0xfffe7c00, v183
	v_add_u32_e32 v229, 0xfffe8000, v183
	s_mov_b64 exec, s[72:73]
	buffer_load_dwordx4 v[140:143], v228, s[8:11], 0 offen
	buffer_load_dwordx4 v[120:123], v228, s[8:11], 0 offen offset:512
	s_mov_b64 exec, -1
	s_mov_b64 exec, s[68:69]
	buffer_load_dwordx4 v[152:155], v229, s[8:11], 0 offen offset:512
	buffer_load_dwordx4 v[132:135], v229, s[8:11], 0 offen offset:1024
	s_mov_b64 exec, -1
	s_mov_b64 exec, s[74:75]
	buffer_load_dwordx4 v[156:159], v229, s[8:11], 0 offen offset:2048
	buffer_load_dwordx4 v[144:147], v229, s[8:11], 0 offen offset:2560
	s_mov_b64 exec, -1
	v_add_u32_e32 v228, 0xfffffc00, v183
	s_mov_b64 exec, s[64:65]
	buffer_load_dwordx4 v[124:127], v228, s[8:11], 0 offen
	buffer_load_dwordx4 v[104:107], v228, s[8:11], 0 offen offset:512
	s_mov_b64 exec, -1
	buffer_load_dwordx4 v[136:139], v183, s[8:11], 0 offen offset:512
	buffer_load_dwordx4 v[108:111], v183, s[8:11], 0 offen offset:1024
	s_mov_b64 exec, s[66:67]
	buffer_load_dwordx4 v[148:151], v183, s[8:11], 0 offen offset:2048
	buffer_load_dwordx4 v[88:91], v183, s[8:11], 0 offen offset:2560
	s_mov_b64 exec, -1
	v_add_u32_e32 v228, 0x17c00, v183
	v_add_u32_e32 v229, 0x18000, v183
	s_mov_b64 exec, s[64:65]
	buffer_load_dwordx4 v[64:67], v228, s[8:11], 0 offen
	buffer_load_dwordx4 v[40:43], v228, s[8:11], 0 offen offset:512
	s_mov_b64 exec, -1
	buffer_load_dwordx4 v[76:79], v229, s[8:11], 0 offen offset:512
	buffer_load_dwordx4 v[48:51], v229, s[8:11], 0 offen offset:1024
	s_mov_b64 exec, s[66:67]
	buffer_load_dwordx4 v[92:95], v229, s[8:11], 0 offen offset:2048
	buffer_load_dwordx4 v[60:63], v229, s[8:11], 0 offen offset:2560
	s_mov_b64 exec, -1
	v_add_u32_e32 v228, 0x2fc00, v183
	v_add_u32_e32 v229, 0x30000, v183
	s_mov_b64 exec, s[64:65]
	buffer_load_dwordx4 v[36:39], v228, s[8:11], 0 offen
	buffer_load_dwordx4 v[24:27], v228, s[8:11], 0 offen offset:512
	s_mov_b64 exec, -1
	buffer_load_dwordx4 v[52:55], v229, s[8:11], 0 offen offset:512
	buffer_load_dwordx4 v[28:31], v229, s[8:11], 0 offen offset:1024
	s_mov_b64 exec, s[66:67]
	buffer_load_dwordx4 v[68:71], v229, s[8:11], 0 offen offset:2048
	buffer_load_dwordx4 v[32:35], v229, s[8:11], 0 offen offset:2560
	s_mov_b64 exec, -1
	v_add_u32_e32 v228, 0x18000, v183
	buffer_load_dwordx4 v[160:163], v228, s[8:11], 0 offen nt
	v_add_u32_e32 v228, 0x47c00, v183
	v_add_u32_e32 v229, 0x48000, v183
	v_add_u32_e32 v230, 0x5fc00, v183
	v_add_u32_e32 v231, 0x60000, v183
	s_waitcnt vmcnt(30)
	v_cvt_pk_f16_f32 v22, v240, v241
	v_cvt_pk_f16_f32 v20, v236, v237
	v_cvt_pk_f16_f32 v21, v238, v239
	v_cvt_pk_f16_f32 v16, v244, v245
	v_cvt_pk_f16_f32 v17, v246, v247
	v_cvt_pk_f16_f32 v18, v248, v249
	v_cvt_pk_f16_f32 v23, v242, v243
	v_cvt_pk_f16_f32 v19, v250, v251
	s_not_b64 exec, s[72:73]
	s_cbranch_execz .Lmyf_E2_0
	v_mov_b32_e32 v140, v20
	v_mov_b32_e32 v141, v21
	v_mov_b32_e32 v142, v22
	v_mov_b32_e32 v143, v23
	v_mov_b32_e32 v120, v16
	v_mov_b32_e32 v121, v17
	v_mov_b32_e32 v122, v18
	v_mov_b32_e32 v123, v19
